# c19
# baseline (speedup 1.0000x reference)
.LBB2_3:
	ds_read_b128 v[202:205], v175
	ds_read_b128 v[206:209], v175 offset:256
	ds_read_b128 v[210:213], v175 offset:512
	ds_read_b128 v[214:217], v175 offset:768
	ds_read_b128 v[218:221], v175 offset:1024
	ds_read_b128 v[222:225], v175 offset:1280
	ds_read_b128 v[226:229], v175 offset:1536
	ds_read_b128 v[230:233], v175 offset:1792
	ds_read2_b64 v[178:181], v171 offset1:1
	ds_read2_b64 v[182:185], v171 offset0:2 offset1:48
	ds_read2_b64 v[186:189], v171 offset0:49 offset1:50
	s_mov_b32 m0, s59
	ds_read2_b64 v[190:193], v171 offset0:96 offset1:97
	global_load_lds_dwordx4 v144, s[76:77]
	s_mov_b32 m0, s58
	ds_read2_b64 v[194:197], v171 offset0:98 offset1:144
	global_load_lds_dwordx4 v145, s[76:77]
	s_mov_b32 m0, s57
	ds_read2_b64 v[198:201], v171 offset0:145 offset1:146
	global_load_lds_dwordx4 v146, s[76:77]
	v_add_u32_e32 v152, s44, v176
	ds_read_u16 v240, v152
	ds_read_u16 v241, v152 offset:32
	ds_read_u16 v242, v152 offset:64
	s_add_i32 s44, s62, 0xfffff800
	s_and_b32 s44, s44, 0x1800
	s_add_i32 m0, s50, s44
	ds_read_u16 v243, v152 offset:96
	global_load_lds_dword v150, s[80:81]
	s_waitcnt vmcnt(6)
	s_waitcnt lgkmcnt(0)
	s_barrier
	v_mfma_scale_f32_16x16x128_f8f6f4 v[126:129], v[202:205], v[178:183], v[126:129], v177, v240 op_sel_hi:[0,0,0] cbsz:4 blgp:2
	v_mfma_scale_f32_16x16x128_f8f6f4 v[122:125], v[206:209], v[178:183], v[122:125], v177, v240 op_sel_hi:[0,0,0] cbsz:4 blgp:2
	v_mfma_scale_f32_16x16x128_f8f6f4 v[114:117], v[210:213], v[178:183], v[114:117], v177, v240 op_sel_hi:[0,0,0] cbsz:4 blgp:2
	v_mfma_scale_f32_16x16x128_f8f6f4 v[102:105], v[214:217], v[178:183], v[102:105], v177, v240 op_sel_hi:[0,0,0] cbsz:4 blgp:2
	v_mfma_scale_f32_16x16x128_f8f6f4 v[86:89], v[218:221], v[178:183], v[86:89], v177, v240 op_sel_hi:[0,0,0] cbsz:4 blgp:2
	v_mfma_scale_f32_16x16x128_f8f6f4 v[70:73], v[222:225], v[178:183], v[70:73], v177, v240 op_sel_hi:[0,0,0] cbsz:4 blgp:2
	v_mfma_scale_f32_16x16x128_f8f6f4 v[54:57], v[226:229], v[178:183], v[54:57], v177, v240 op_sel_hi:[0,0,0] cbsz:4 blgp:2
	v_mfma_scale_f32_16x16x128_f8f6f4 v[38:41], v[230:233], v[178:183], v[38:41], v177, v240 op_sel_hi:[0,0,0] cbsz:4 blgp:2
	v_mfma_scale_f32_16x16x128_f8f6f4 v[118:121], v[202:205], v[184:189], v[118:121], v177, v241 op_sel_hi:[0,0,0] cbsz:4 blgp:2
	v_mfma_scale_f32_16x16x128_f8f6f4 v[110:113], v[206:209], v[184:189], v[110:113], v177, v241 op_sel_hi:[0,0,0] cbsz:4 blgp:2
	v_mfma_scale_f32_16x16x128_f8f6f4 v[98:101], v[210:213], v[184:189], v[98:101], v177, v241 op_sel_hi:[0,0,0] cbsz:4 blgp:2
	v_mfma_scale_f32_16x16x128_f8f6f4 v[82:85], v[214:217], v[184:189], v[82:85], v177, v241 op_sel_hi:[0,0,0] cbsz:4 blgp:2
	v_mfma_scale_f32_16x16x128_f8f6f4 v[66:69], v[218:221], v[184:189], v[66:69], v177, v241 op_sel_hi:[0,0,0] cbsz:4 blgp:2
	v_mfma_scale_f32_16x16x128_f8f6f4 v[50:53], v[222:225], v[184:189], v[50:53], v177, v241 op_sel_hi:[0,0,0] cbsz:4 blgp:2
	v_mfma_scale_f32_16x16x128_f8f6f4 v[34:37], v[226:229], v[184:189], v[34:37], v177, v241 op_sel_hi:[0,0,0] cbsz:4 blgp:2
	v_mfma_scale_f32_16x16x128_f8f6f4 v[106:109], v[202:205], v[190:195], v[106:109], v177, v242 op_sel_hi:[0,0,0] cbsz:4 blgp:2
	v_mfma_scale_f32_16x16x128_f8f6f4 v[94:97], v[206:209], v[190:195], v[94:97], v177, v242 op_sel_hi:[0,0,0] cbsz:4 blgp:2
	v_mfma_scale_f32_16x16x128_f8f6f4 v[78:81], v[210:213], v[190:195], v[78:81], v177, v242 op_sel_hi:[0,0,0] cbsz:4 blgp:2
	v_mfma_scale_f32_16x16x128_f8f6f4 v[62:65], v[214:217], v[190:195], v[62:65], v177, v242 op_sel_hi:[0,0,0] cbsz:4 blgp:2
	v_mfma_scale_f32_16x16x128_f8f6f4 v[46:49], v[218:221], v[190:195], v[46:49], v177, v242 op_sel_hi:[0,0,0] cbsz:4 blgp:2
	v_mfma_scale_f32_16x16x128_f8f6f4 v[30:33], v[222:225], v[190:195], v[30:33], v177, v242 op_sel_hi:[0,0,0] cbsz:4 blgp:2
	v_mfma_scale_f32_16x16x128_f8f6f4 v[90:93], v[202:205], v[196:201], v[90:93], v177, v243 op_sel_hi:[0,0,0] cbsz:4 blgp:2
	v_mfma_scale_f32_16x16x128_f8f6f4 v[74:77], v[206:209], v[196:201], v[74:77], v177, v243 op_sel_hi:[0,0,0] cbsz:4 blgp:2
	v_mfma_scale_f32_16x16x128_f8f6f4 v[58:61], v[210:213], v[196:201], v[58:61], v177, v243 op_sel_hi:[0,0,0] cbsz:4 blgp:2
	v_mfma_scale_f32_16x16x128_f8f6f4 v[42:45], v[214:217], v[196:201], v[42:45], v177, v243 op_sel_hi:[0,0,0] cbsz:4 blgp:2
	v_mfma_scale_f32_16x16x128_f8f6f4 v[26:29], v[218:221], v[196:201], v[26:29], v177, v243 op_sel_hi:[0,0,0] cbsz:4 blgp:2
	v_mfma_scale_f32_16x16x128_f8f6f4 v[178:181], v[230:233], v[184:189], v[22:25], v177, v241 op_sel_hi:[0,0,0] cbsz:4 blgp:2
	v_mfma_scale_f32_16x16x128_f8f6f4 v[182:185], v[226:229], v[190:195], v[18:21], v177, v242 op_sel_hi:[0,0,0] cbsz:4 blgp:2
	v_mfma_scale_f32_16x16x128_f8f6f4 v[186:189], v[230:233], v[190:195], v[10:13], v177, v242 op_sel_hi:[0,0,0] cbsz:4 blgp:2
	v_mfma_scale_f32_16x16x128_f8f6f4 v[190:193], v[222:225], v[196:201], v[14:17], v177, v243 op_sel_hi:[0,0,0] cbsz:4 blgp:2
	v_mfma_scale_f32_16x16x128_f8f6f4 v[234:237], v[226:229], v[196:201], v[6:9], v177, v243 op_sel_hi:[0,0,0] cbsz:4 blgp:2
	v_mfma_scale_f32_16x16x128_f8f6f4 v[194:197], v[230:233], v[196:201], v[2:5], v177, v243 op_sel_hi:[0,0,0] cbsz:4 blgp:2
	s_barrier
	ds_read2_b64 v[2:5], v167 offset1:1
	s_mov_b32 m0, s54
	ds_read2_b64 v[6:9], v167 offset0:2 offset1:48
	global_load_lds_dwordx4 v147, s[76:77]
	s_mov_b32 m0, s52
	ds_read2_b64 v[10:13], v167 offset0:49 offset1:50
	global_load_lds_dwordx4 v148, s[76:77]
	s_mov_b32 m0, s51
	ds_read2_b64 v[14:17], v167 offset0:96 offset1:97
	global_load_lds_dwordx4 v149, s[76:77]
	s_mov_b32 m0, s15
	ds_read2_b64 v[18:21], v167 offset0:98 offset1:144
	global_load_lds_dwordx4 v142, s[72:73]
	s_mov_b32 m0, s46
	ds_read2_b64 v[22:25], v167 offset0:145 offset1:146
	global_load_lds_dwordx4 v143, s[72:73]
	s_waitcnt vmcnt(5)
	s_waitcnt lgkmcnt(0)
	s_barrier
	v_mfma_scale_f32_16x16x128_f8f6f4 v[126:129], v[202:205], v[2:7], v[126:129], v177, v240 op_sel:[0,1,0] op_sel_hi:[0,0,0] cbsz:4 blgp:2
	v_mfma_scale_f32_16x16x128_f8f6f4 v[122:125], v[206:209], v[2:7], v[122:125], v177, v240 op_sel:[0,1,0] op_sel_hi:[0,0,0] cbsz:4 blgp:2
	v_mfma_scale_f32_16x16x128_f8f6f4 v[114:117], v[210:213], v[2:7], v[114:117], v177, v240 op_sel:[0,1,0] op_sel_hi:[0,0,0] cbsz:4 blgp:2
	v_mfma_scale_f32_16x16x128_f8f6f4 v[102:105], v[214:217], v[2:7], v[102:105], v177, v240 op_sel:[0,1,0] op_sel_hi:[0,0,0] cbsz:4 blgp:2
	v_mfma_scale_f32_16x16x128_f8f6f4 v[86:89], v[218:221], v[2:7], v[86:89], v177, v240 op_sel:[0,1,0] op_sel_hi:[0,0,0] cbsz:4 blgp:2
	v_mfma_scale_f32_16x16x128_f8f6f4 v[70:73], v[222:225], v[2:7], v[70:73], v177, v240 op_sel:[0,1,0] op_sel_hi:[0,0,0] cbsz:4 blgp:2
	v_mfma_scale_f32_16x16x128_f8f6f4 v[54:57], v[226:229], v[2:7], v[54:57], v177, v240 op_sel:[0,1,0] op_sel_hi:[0,0,0] cbsz:4 blgp:2
	v_mfma_scale_f32_16x16x128_f8f6f4 v[38:41], v[230:233], v[2:7], v[38:41], v177, v240 op_sel:[0,1,0] op_sel_hi:[0,0,0] cbsz:4 blgp:2
	v_mfma_scale_f32_16x16x128_f8f6f4 v[118:121], v[202:205], v[8:13], v[118:121], v177, v241 op_sel:[0,1,0] op_sel_hi:[0,0,0] cbsz:4 blgp:2
	v_mfma_scale_f32_16x16x128_f8f6f4 v[110:113], v[206:209], v[8:13], v[110:113], v177, v241 op_sel:[0,1,0] op_sel_hi:[0,0,0] cbsz:4 blgp:2
	v_mfma_scale_f32_16x16x128_f8f6f4 v[98:101], v[210:213], v[8:13], v[98:101], v177, v241 op_sel:[0,1,0] op_sel_hi:[0,0,0] cbsz:4 blgp:2
	v_mfma_scale_f32_16x16x128_f8f6f4 v[82:85], v[214:217], v[8:13], v[82:85], v177, v241 op_sel:[0,1,0] op_sel_hi:[0,0,0] cbsz:4 blgp:2
	v_mfma_scale_f32_16x16x128_f8f6f4 v[66:69], v[218:221], v[8:13], v[66:69], v177, v241 op_sel:[0,1,0] op_sel_hi:[0,0,0] cbsz:4 blgp:2
	v_mfma_scale_f32_16x16x128_f8f6f4 v[50:53], v[222:225], v[8:13], v[50:53], v177, v241 op_sel:[0,1,0] op_sel_hi:[0,0,0] cbsz:4 blgp:2
	v_mfma_scale_f32_16x16x128_f8f6f4 v[34:37], v[226:229], v[8:13], v[34:37], v177, v241 op_sel:[0,1,0] op_sel_hi:[0,0,0] cbsz:4 blgp:2
	v_mfma_scale_f32_16x16x128_f8f6f4 v[106:109], v[202:205], v[14:19], v[106:109], v177, v242 op_sel:[0,1,0] op_sel_hi:[0,0,0] cbsz:4 blgp:2
	v_mfma_scale_f32_16x16x128_f8f6f4 v[94:97], v[206:209], v[14:19], v[94:97], v177, v242 op_sel:[0,1,0] op_sel_hi:[0,0,0] cbsz:4 blgp:2
	v_mfma_scale_f32_16x16x128_f8f6f4 v[78:81], v[210:213], v[14:19], v[78:81], v177, v242 op_sel:[0,1,0] op_sel_hi:[0,0,0] cbsz:4 blgp:2
	v_mfma_scale_f32_16x16x128_f8f6f4 v[62:65], v[214:217], v[14:19], v[62:65], v177, v242 op_sel:[0,1,0] op_sel_hi:[0,0,0] cbsz:4 blgp:2
	v_mfma_scale_f32_16x16x128_f8f6f4 v[46:49], v[218:221], v[14:19], v[46:49], v177, v242 op_sel:[0,1,0] op_sel_hi:[0,0,0] cbsz:4 blgp:2
	v_mfma_scale_f32_16x16x128_f8f6f4 v[30:33], v[222:225], v[14:19], v[30:33], v177, v242 op_sel:[0,1,0] op_sel_hi:[0,0,0] cbsz:4 blgp:2
	v_mfma_scale_f32_16x16x128_f8f6f4 v[90:93], v[202:205], v[20:25], v[90:93], v177, v243 op_sel:[0,1,0] op_sel_hi:[0,0,0] cbsz:4 blgp:2
	v_mfma_scale_f32_16x16x128_f8f6f4 v[74:77], v[206:209], v[20:25], v[74:77], v177, v243 op_sel:[0,1,0] op_sel_hi:[0,0,0] cbsz:4 blgp:2
	v_mfma_scale_f32_16x16x128_f8f6f4 v[58:61], v[210:213], v[20:25], v[58:61], v177, v243 op_sel:[0,1,0] op_sel_hi:[0,0,0] cbsz:4 blgp:2
	v_mfma_scale_f32_16x16x128_f8f6f4 v[42:45], v[214:217], v[20:25], v[42:45], v177, v243 op_sel:[0,1,0] op_sel_hi:[0,0,0] cbsz:4 blgp:2
	v_mfma_scale_f32_16x16x128_f8f6f4 v[26:29], v[218:221], v[20:25], v[26:29], v177, v243 op_sel:[0,1,0] op_sel_hi:[0,0,0] cbsz:4 blgp:2
	v_mfma_scale_f32_16x16x128_f8f6f4 v[178:181], v[230:233], v[8:13], v[178:181], v177, v241 op_sel:[0,1,0] op_sel_hi:[0,0,0] cbsz:4 blgp:2
	v_mfma_scale_f32_16x16x128_f8f6f4 v[182:185], v[226:229], v[14:19], v[182:185], v177, v242 op_sel:[0,1,0] op_sel_hi:[0,0,0] cbsz:4 blgp:2
	v_mfma_scale_f32_16x16x128_f8f6f4 v[186:189], v[230:233], v[14:19], v[186:189], v177, v242 op_sel:[0,1,0] op_sel_hi:[0,0,0] cbsz:4 blgp:2
	v_mfma_scale_f32_16x16x128_f8f6f4 v[190:193], v[222:225], v[20:25], v[190:193], v177, v243 op_sel:[0,1,0] op_sel_hi:[0,0,0] cbsz:4 blgp:2
	v_mfma_scale_f32_16x16x128_f8f6f4 v[198:201], v[226:229], v[20:25], v[234:237], v177, v243 op_sel:[0,1,0] op_sel_hi:[0,0,0] cbsz:4 blgp:2
	v_mfma_scale_f32_16x16x128_f8f6f4 v[194:197], v[230:233], v[20:25], v[194:197], v177, v243 op_sel:[0,1,0] op_sel_hi:[0,0,0] cbsz:4 blgp:2
	s_barrier
	ds_read_b128 v[202:205], v166
	ds_read_b128 v[206:209], v166 offset:256
	ds_read_b128 v[210:213], v166 offset:512
	ds_read_b128 v[214:217], v166 offset:768
	ds_read_b128 v[218:221], v166 offset:1024
	ds_read_b128 v[222:225], v166 offset:1280
	ds_read_b128 v[226:229], v166 offset:1536
	ds_read_b128 v[230:233], v166 offset:1792
	ds_read2_b64 v[2:5], v162 offset1:1
	ds_read2_b64 v[6:9], v162 offset0:2 offset1:48
	ds_read2_b64 v[10:13], v162 offset0:49 offset1:50
	s_mov_b32 m0, s47
	ds_read2_b64 v[14:17], v162 offset0:96 offset1:97
	global_load_lds_dwordx4 v144, s[78:79]
	s_mov_b32 m0, s48
	ds_read2_b64 v[18:21], v162 offset0:98 offset1:144
	global_load_lds_dwordx4 v145, s[78:79]
	s_mov_b32 m0, s49
	ds_read2_b64 v[22:25], v162 offset0:145 offset1:146
	global_load_lds_dwordx4 v146, s[78:79]
	v_add_u32_e32 v234, s44, v176
	ds_read_u16 v242, v234
	ds_read_u16 v243, v234 offset:32
	ds_read_u16 v244, v234 offset:64
	s_and_b32 s44, s62, 0x1000
	s_add_i32 m0, s50, s44
	ds_read_u16 v245, v234 offset:96
	global_load_lds_dword v151, s[80:81]
	s_waitcnt vmcnt(6)
	s_waitcnt lgkmcnt(0)
	s_barrier
	v_mfma_scale_f32_16x16x128_f8f6f4 v[126:129], v[202:205], v[2:7], v[126:129], v177, v242 op_sel_hi:[0,0,0] cbsz:4 blgp:2
	v_mfma_scale_f32_16x16x128_f8f6f4 v[122:125], v[206:209], v[2:7], v[122:125], v177, v242 op_sel_hi:[0,0,0] cbsz:4 blgp:2
	v_mfma_scale_f32_16x16x128_f8f6f4 v[114:117], v[210:213], v[2:7], v[114:117], v177, v242 op_sel_hi:[0,0,0] cbsz:4 blgp:2
	v_mfma_scale_f32_16x16x128_f8f6f4 v[102:105], v[214:217], v[2:7], v[102:105], v177, v242 op_sel_hi:[0,0,0] cbsz:4 blgp:2
	v_mfma_scale_f32_16x16x128_f8f6f4 v[86:89], v[218:221], v[2:7], v[86:89], v177, v242 op_sel_hi:[0,0,0] cbsz:4 blgp:2
	v_mfma_scale_f32_16x16x128_f8f6f4 v[70:73], v[222:225], v[2:7], v[70:73], v177, v242 op_sel_hi:[0,0,0] cbsz:4 blgp:2
	v_mfma_scale_f32_16x16x128_f8f6f4 v[54:57], v[226:229], v[2:7], v[54:57], v177, v242 op_sel_hi:[0,0,0] cbsz:4 blgp:2
	v_mfma_scale_f32_16x16x128_f8f6f4 v[38:41], v[230:233], v[2:7], v[38:41], v177, v242 op_sel_hi:[0,0,0] cbsz:4 blgp:2
	v_mfma_scale_f32_16x16x128_f8f6f4 v[118:121], v[202:205], v[8:13], v[118:121], v177, v243 op_sel_hi:[0,0,0] cbsz:4 blgp:2
	v_mfma_scale_f32_16x16x128_f8f6f4 v[110:113], v[206:209], v[8:13], v[110:113], v177, v243 op_sel_hi:[0,0,0] cbsz:4 blgp:2
	v_mfma_scale_f32_16x16x128_f8f6f4 v[98:101], v[210:213], v[8:13], v[98:101], v177, v243 op_sel_hi:[0,0,0] cbsz:4 blgp:2
	v_mfma_scale_f32_16x16x128_f8f6f4 v[82:85], v[214:217], v[8:13], v[82:85], v177, v243 op_sel_hi:[0,0,0] cbsz:4 blgp:2
	v_mfma_scale_f32_16x16x128_f8f6f4 v[66:69], v[218:221], v[8:13], v[66:69], v177, v243 op_sel_hi:[0,0,0] cbsz:4 blgp:2
	v_mfma_scale_f32_16x16x128_f8f6f4 v[50:53], v[222:225], v[8:13], v[50:53], v177, v243 op_sel_hi:[0,0,0] cbsz:4 blgp:2
	v_mfma_scale_f32_16x16x128_f8f6f4 v[34:37], v[226:229], v[8:13], v[34:37], v177, v243 op_sel_hi:[0,0,0] cbsz:4 blgp:2
	v_mfma_scale_f32_16x16x128_f8f6f4 v[106:109], v[202:205], v[14:19], v[106:109], v177, v244 op_sel_hi:[0,0,0] cbsz:4 blgp:2
	v_mfma_scale_f32_16x16x128_f8f6f4 v[94:97], v[206:209], v[14:19], v[94:97], v177, v244 op_sel_hi:[0,0,0] cbsz:4 blgp:2
	v_mfma_scale_f32_16x16x128_f8f6f4 v[78:81], v[210:213], v[14:19], v[78:81], v177, v244 op_sel_hi:[0,0,0] cbsz:4 blgp:2
	v_mfma_scale_f32_16x16x128_f8f6f4 v[62:65], v[214:217], v[14:19], v[62:65], v177, v244 op_sel_hi:[0,0,0] cbsz:4 blgp:2
	v_mfma_scale_f32_16x16x128_f8f6f4 v[46:49], v[218:221], v[14:19], v[46:49], v177, v244 op_sel_hi:[0,0,0] cbsz:4 blgp:2
	v_mfma_scale_f32_16x16x128_f8f6f4 v[30:33], v[222:225], v[14:19], v[30:33], v177, v244 op_sel_hi:[0,0,0] cbsz:4 blgp:2
	v_mfma_scale_f32_16x16x128_f8f6f4 v[238:241], v[226:229], v[14:19], v[182:185], v177, v244 op_sel_hi:[0,0,0] cbsz:4 blgp:2
	v_mfma_scale_f32_16x16x128_f8f6f4 v[14:17], v[230:233], v[14:19], v[186:189], v177, v244 op_sel_hi:[0,0,0] cbsz:4 blgp:2
	v_mfma_scale_f32_16x16x128_f8f6f4 v[90:93], v[202:205], v[20:25], v[90:93], v177, v245 op_sel_hi:[0,0,0] cbsz:4 blgp:2
	v_mfma_scale_f32_16x16x128_f8f6f4 v[74:77], v[206:209], v[20:25], v[74:77], v177, v245 op_sel_hi:[0,0,0] cbsz:4 blgp:2
	v_mfma_scale_f32_16x16x128_f8f6f4 v[58:61], v[210:213], v[20:25], v[58:61], v177, v245 op_sel_hi:[0,0,0] cbsz:4 blgp:2
	v_mfma_scale_f32_16x16x128_f8f6f4 v[42:45], v[214:217], v[20:25], v[42:45], v177, v245 op_sel_hi:[0,0,0] cbsz:4 blgp:2
	v_mfma_scale_f32_16x16x128_f8f6f4 v[26:29], v[218:221], v[20:25], v[26:29], v177, v245 op_sel_hi:[0,0,0] cbsz:4 blgp:2
	v_mfma_scale_f32_16x16x128_f8f6f4 v[234:237], v[230:233], v[8:13], v[178:181], v177, v243 op_sel_hi:[0,0,0] cbsz:4 blgp:2
	v_mfma_scale_f32_16x16x128_f8f6f4 v[190:193], v[222:225], v[20:25], v[190:193], v177, v245 op_sel_hi:[0,0,0] cbsz:4 blgp:2
	v_mfma_scale_f32_16x16x128_f8f6f4 v[198:201], v[226:229], v[20:25], v[198:201], v177, v245 op_sel_hi:[0,0,0] cbsz:4 blgp:2
	v_mfma_scale_f32_16x16x128_f8f6f4 v[194:197], v[230:233], v[20:25], v[194:197], v177, v245 op_sel_hi:[0,0,0] cbsz:4 blgp:2
	s_barrier
	ds_read2_b64 v[2:5], v1 offset1:1
	s_mov_b32 m0, s53
	ds_read2_b64 v[6:9], v1 offset0:2 offset1:48
	global_load_lds_dwordx4 v147, s[78:79]
	s_mov_b32 m0, s55
	ds_read2_b64 v[10:13], v1 offset0:49 offset1:50
	global_load_lds_dwordx4 v148, s[78:79]
	s_mov_b32 m0, s56
	ds_read2_b64 v[178:181], v159 offset1:1
	global_load_lds_dwordx4 v149, s[78:79]
	s_mov_b32 m0, s63
	ds_read2_b64 v[182:185], v159 offset0:2 offset1:48
	global_load_lds_dwordx4 v142, s[74:75]
	s_mov_b32 m0, s60
	ds_read2_b64 v[186:189], v159 offset0:49 offset1:50
	global_load_lds_dwordx4 v143, s[74:75]
	s_waitcnt vmcnt(5)
	s_waitcnt lgkmcnt(0)
	s_barrier
	v_mfma_scale_f32_16x16x128_f8f6f4 v[126:129], v[202:205], v[2:7], v[126:129], v177, v242 op_sel:[0,1,0] op_sel_hi:[0,0,0] cbsz:4 blgp:2
	v_mfma_scale_f32_16x16x128_f8f6f4 v[122:125], v[206:209], v[2:7], v[122:125], v177, v242 op_sel:[0,1,0] op_sel_hi:[0,0,0] cbsz:4 blgp:2
	v_mfma_scale_f32_16x16x128_f8f6f4 v[114:117], v[210:213], v[2:7], v[114:117], v177, v242 op_sel:[0,1,0] op_sel_hi:[0,0,0] cbsz:4 blgp:2
	v_mfma_scale_f32_16x16x128_f8f6f4 v[102:105], v[214:217], v[2:7], v[102:105], v177, v242 op_sel:[0,1,0] op_sel_hi:[0,0,0] cbsz:4 blgp:2
	v_mfma_scale_f32_16x16x128_f8f6f4 v[86:89], v[218:221], v[2:7], v[86:89], v177, v242 op_sel:[0,1,0] op_sel_hi:[0,0,0] cbsz:4 blgp:2
	v_mfma_scale_f32_16x16x128_f8f6f4 v[70:73], v[222:225], v[2:7], v[70:73], v177, v242 op_sel:[0,1,0] op_sel_hi:[0,0,0] cbsz:4 blgp:2
	v_mfma_scale_f32_16x16x128_f8f6f4 v[54:57], v[226:229], v[2:7], v[54:57], v177, v242 op_sel:[0,1,0] op_sel_hi:[0,0,0] cbsz:4 blgp:2
	v_mfma_scale_f32_16x16x128_f8f6f4 v[38:41], v[230:233], v[2:7], v[38:41], v177, v242 op_sel:[0,1,0] op_sel_hi:[0,0,0] cbsz:4 blgp:2
	v_mfma_scale_f32_16x16x128_f8f6f4 v[118:121], v[202:205], v[8:13], v[118:121], v177, v243 op_sel:[0,1,0] op_sel_hi:[0,0,0] cbsz:4 blgp:2
	v_mfma_scale_f32_16x16x128_f8f6f4 v[110:113], v[206:209], v[8:13], v[110:113], v177, v243 op_sel:[0,1,0] op_sel_hi:[0,0,0] cbsz:4 blgp:2
	v_mfma_scale_f32_16x16x128_f8f6f4 v[98:101], v[210:213], v[8:13], v[98:101], v177, v243 op_sel:[0,1,0] op_sel_hi:[0,0,0] cbsz:4 blgp:2
	v_mfma_scale_f32_16x16x128_f8f6f4 v[82:85], v[214:217], v[8:13], v[82:85], v177, v243 op_sel:[0,1,0] op_sel_hi:[0,0,0] cbsz:4 blgp:2
	v_mfma_scale_f32_16x16x128_f8f6f4 v[66:69], v[218:221], v[8:13], v[66:69], v177, v243 op_sel:[0,1,0] op_sel_hi:[0,0,0] cbsz:4 blgp:2
	v_mfma_scale_f32_16x16x128_f8f6f4 v[50:53], v[222:225], v[8:13], v[50:53], v177, v243 op_sel:[0,1,0] op_sel_hi:[0,0,0] cbsz:4 blgp:2
	v_mfma_scale_f32_16x16x128_f8f6f4 v[34:37], v[226:229], v[8:13], v[34:37], v177, v243 op_sel:[0,1,0] op_sel_hi:[0,0,0] cbsz:4 blgp:2
	v_mfma_scale_f32_16x16x128_f8f6f4 v[22:25], v[230:233], v[8:13], v[234:237], v177, v243 op_sel:[0,1,0] op_sel_hi:[0,0,0] cbsz:4 blgp:2
	v_mfma_scale_f32_16x16x128_f8f6f4 v[106:109], v[202:205], v[178:183], v[106:109], v177, v244 op_sel:[0,1,0] op_sel_hi:[0,0,0] cbsz:4 blgp:2
	v_mfma_scale_f32_16x16x128_f8f6f4 v[94:97], v[206:209], v[178:183], v[94:97], v177, v244 op_sel:[0,1,0] op_sel_hi:[0,0,0] cbsz:4 blgp:2
	v_mfma_scale_f32_16x16x128_f8f6f4 v[78:81], v[210:213], v[178:183], v[78:81], v177, v244 op_sel:[0,1,0] op_sel_hi:[0,0,0] cbsz:4 blgp:2
	v_mfma_scale_f32_16x16x128_f8f6f4 v[62:65], v[214:217], v[178:183], v[62:65], v177, v244 op_sel:[0,1,0] op_sel_hi:[0,0,0] cbsz:4 blgp:2
	v_mfma_scale_f32_16x16x128_f8f6f4 v[46:49], v[218:221], v[178:183], v[46:49], v177, v244 op_sel:[0,1,0] op_sel_hi:[0,0,0] cbsz:4 blgp:2
	v_mfma_scale_f32_16x16x128_f8f6f4 v[30:33], v[222:225], v[178:183], v[30:33], v177, v244 op_sel:[0,1,0] op_sel_hi:[0,0,0] cbsz:4 blgp:2
	v_mfma_scale_f32_16x16x128_f8f6f4 v[18:21], v[226:229], v[178:183], v[238:241], v177, v244 op_sel:[0,1,0] op_sel_hi:[0,0,0] cbsz:4 blgp:2
	v_mfma_scale_f32_16x16x128_f8f6f4 v[10:13], v[230:233], v[178:183], v[14:17], v177, v244 op_sel:[0,1,0] op_sel_hi:[0,0,0] cbsz:4 blgp:2
	v_mfma_scale_f32_16x16x128_f8f6f4 v[90:93], v[202:205], v[184:189], v[90:93], v177, v245 op_sel:[0,1,0] op_sel_hi:[0,0,0] cbsz:4 blgp:2
	v_mfma_scale_f32_16x16x128_f8f6f4 v[74:77], v[206:209], v[184:189], v[74:77], v177, v245 op_sel:[0,1,0] op_sel_hi:[0,0,0] cbsz:4 blgp:2
	v_mfma_scale_f32_16x16x128_f8f6f4 v[58:61], v[210:213], v[184:189], v[58:61], v177, v245 op_sel:[0,1,0] op_sel_hi:[0,0,0] cbsz:4 blgp:2
	v_mfma_scale_f32_16x16x128_f8f6f4 v[42:45], v[214:217], v[184:189], v[42:45], v177, v245 op_sel:[0,1,0] op_sel_hi:[0,0,0] cbsz:4 blgp:2
	v_mfma_scale_f32_16x16x128_f8f6f4 v[26:29], v[218:221], v[184:189], v[26:29], v177, v245 op_sel:[0,1,0] op_sel_hi:[0,0,0] cbsz:4 blgp:2
	v_mfma_scale_f32_16x16x128_f8f6f4 v[14:17], v[222:225], v[184:189], v[190:193], v177, v245 op_sel:[0,1,0] op_sel_hi:[0,0,0] cbsz:4 blgp:2
	v_mfma_scale_f32_16x16x128_f8f6f4 v[6:9], v[226:229], v[184:189], v[198:201], v177, v245 op_sel:[0,1,0] op_sel_hi:[0,0,0] cbsz:4 blgp:2
	v_mfma_scale_f32_16x16x128_f8f6f4 v[2:5], v[230:233], v[184:189], v[194:197], v177, v245 op_sel:[0,1,0] op_sel_hi:[0,0,0] cbsz:4 blgp:2
	s_add_i32 s61, s61, 2
	s_addk_i32 s62, 0x1000
	s_add_u32 s72, s72, 0x8000
	s_addc_u32 s73, s73, 0
	s_add_u32 s74, s74, 0x8000
	s_addc_u32 s75, s75, 0
	s_add_u32 s76, s76, 0x18000
	s_addc_u32 s77, s77, 0
	s_add_u32 s78, s78, 0x18000
	s_addc_u32 s79, s79, 0
	s_add_u32 s80, s80, 0x1000
	s_addc_u32 s81, s81, 0
	s_add_i32 s44, s62, 0xfffff000
	s_and_b32 s44, s44, 0x1000
	s_cmp_lt_u32 s61, 4
	s_barrier
	s_cbranch_scc1 .LBB2_3
	ds_read_b128 v[154:157], v175
	ds_read_b128 v[186:189], v175 offset:256
	ds_read_b128 v[190:193], v175 offset:512
	ds_read_b128 v[194:197], v175 offset:768
	ds_read_b128 v[198:201], v175 offset:1024
	ds_read_b128 v[202:205], v175 offset:1280
	ds_read_b128 v[206:209], v175 offset:1536
	ds_read_b128 v[210:213], v175 offset:1792
	ds_read_b64 v[142:143], v171
	ds_read_b64 v[144:145], v171 offset:8
	ds_read_b64 v[146:147], v171 offset:16
	ds_read_b64 v[148:149], v174
	ds_read_b64 v[150:151], v174 offset:8
	ds_read_b64 v[152:153], v174 offset:16
	ds_read_b64 v[174:175], v173
	ds_read_b64 v[176:177], v173 offset:8
	ds_read_b64 v[178:179], v173 offset:16
	ds_read_b64 v[180:181], v172
	ds_read_b64 v[182:183], v172 offset:8
	ds_read_b64 v[184:185], v172 offset:16
	v_add_u32_e32 v171, 0x21000, v161
	v_add_u32_e32 v172, 0x21020, v161
	v_add_u32_e32 v173, 0x21040, v161
	v_add_u32_e32 v214, 0x21060, v161
	s_mov_b64 s[0:1], 0x1c000
	s_mov_b32 m0, s63
	ds_read_u16 v171, v171
	ds_read_u16 v215, v172
	ds_read_u16 v216, v173
	ds_read_u16 v214, v214
	v_lshl_add_u64 v[172:173], v[138:139], 0, s[0:1]
	s_mov_b64 s[0:1], 0x1e000
	v_lshl_add_u64 v[138:139], v[138:139], 0, s[0:1]
	s_mov_b32 m0, s60
	s_mov_b64 s[0:1], 0x54000
	v_lshl_add_u64 v[138:139], v[140:141], 0, s[0:1]
	v_lshl_add_u64 v[140:141], v[138:139], 0, s[18:19]
	s_mov_b32 m0, s59
	v_lshl_add_u64 v[130:131], s[16:17], 0, v[130:131]
	global_load_lds_dwordx4 v[140:141], off
	v_lshl_add_u64 v[140:141], v[138:139], 0, s[20:21]
	s_mov_b32 m0, s58
	v_lshl_add_u64 v[138:139], v[138:139], 0, s[22:23]
	global_load_lds_dwordx4 v[140:141], off
	s_mov_b32 m0, s57
	s_mov_b64 s[0:1], 0x3800
	global_load_lds_dwordx4 v[138:139], off
	v_lshl_add_u64 v[130:131], v[130:131], 0, s[0:1]
	s_add_i32 m0, s3, 0x21800
	s_waitcnt lgkmcnt(0)
	v_mov_b32_e32 v172, v216
	global_load_lds_dword v[130:131], off
	s_waitcnt vmcnt(6)
	s_waitcnt lgkmcnt(0)
	v_mov_b32_e32 v130, v171
	v_mov_b32_e32 v131, v215
	v_mov_b32_e32 v217, v214
	s_barrier
	v_mov_b32_e32 v240, 0x7f7f7f7f
	s_nop 1
	v_mfma_scale_f32_16x16x128_f8f6f4 v[126:129], v[154:157], v[142:147], v[126:129], v240, v130 op_sel_hi:[0,0,0] cbsz:4 blgp:2
	v_mfma_scale_f32_16x16x128_f8f6f4 v[122:125], v[186:189], v[142:147], v[122:125], v240, v130 op_sel_hi:[0,0,0] cbsz:4 blgp:2
	v_mfma_scale_f32_16x16x128_f8f6f4 v[114:117], v[190:193], v[142:147], v[114:117], v240, v130 op_sel_hi:[0,0,0] cbsz:4 blgp:2
	v_mfma_scale_f32_16x16x128_f8f6f4 v[102:105], v[194:197], v[142:147], v[102:105], v240, v130 op_sel_hi:[0,0,0] cbsz:4 blgp:2
	v_mfma_scale_f32_16x16x128_f8f6f4 v[86:89], v[198:201], v[142:147], v[86:89], v240, v130 op_sel_hi:[0,0,0] cbsz:4 blgp:2
	v_mfma_scale_f32_16x16x128_f8f6f4 v[70:73], v[202:205], v[142:147], v[70:73], v240, v130 op_sel_hi:[0,0,0] cbsz:4 blgp:2
	v_mfma_scale_f32_16x16x128_f8f6f4 v[54:57], v[206:209], v[142:147], v[54:57], v240, v130 op_sel_hi:[0,0,0] cbsz:4 blgp:2
	v_mfma_scale_f32_16x16x128_f8f6f4 v[38:41], v[210:213], v[142:147], v[38:41], v240, v130 op_sel_hi:[0,0,0] cbsz:4 blgp:2
	v_mfma_scale_f32_16x16x128_f8f6f4 v[118:121], v[154:157], v[148:153], v[118:121], v240, v131 op_sel_hi:[0,0,0] cbsz:4 blgp:2
	v_mfma_scale_f32_16x16x128_f8f6f4 v[110:113], v[186:189], v[148:153], v[110:113], v240, v131 op_sel_hi:[0,0,0] cbsz:4 blgp:2
	v_mfma_scale_f32_16x16x128_f8f6f4 v[98:101], v[190:193], v[148:153], v[98:101], v240, v131 op_sel_hi:[0,0,0] cbsz:4 blgp:2
	v_mfma_scale_f32_16x16x128_f8f6f4 v[82:85], v[194:197], v[148:153], v[82:85], v240, v131 op_sel_hi:[0,0,0] cbsz:4 blgp:2
	v_mfma_scale_f32_16x16x128_f8f6f4 v[66:69], v[198:201], v[148:153], v[66:69], v240, v131 op_sel_hi:[0,0,0] cbsz:4 blgp:2
	v_mfma_scale_f32_16x16x128_f8f6f4 v[50:53], v[202:205], v[148:153], v[50:53], v240, v131 op_sel_hi:[0,0,0] cbsz:4 blgp:2
	v_mfma_scale_f32_16x16x128_f8f6f4 v[138:141], v[210:213], v[148:153], v[22:25], v240, v131 op_sel_hi:[0,0,0] cbsz:4 blgp:2
	v_mfma_scale_f32_16x16x128_f8f6f4 v[106:109], v[154:157], v[174:179], v[106:109], v240, v172 op_sel_hi:[0,0,0] cbsz:4 blgp:2
	v_mfma_scale_f32_16x16x128_f8f6f4 v[94:97], v[186:189], v[174:179], v[94:97], v240, v172 op_sel_hi:[0,0,0] cbsz:4 blgp:2
	v_mfma_scale_f32_16x16x128_f8f6f4 v[78:81], v[190:193], v[174:179], v[78:81], v240, v172 op_sel_hi:[0,0,0] cbsz:4 blgp:2
	v_mfma_scale_f32_16x16x128_f8f6f4 v[62:65], v[194:197], v[174:179], v[62:65], v240, v172 op_sel_hi:[0,0,0] cbsz:4 blgp:2
	v_mfma_scale_f32_16x16x128_f8f6f4 v[46:49], v[198:201], v[174:179], v[46:49], v240, v172 op_sel_hi:[0,0,0] cbsz:4 blgp:2
	v_mfma_scale_f32_16x16x128_f8f6f4 v[30:33], v[202:205], v[174:179], v[30:33], v240, v172 op_sel_hi:[0,0,0] cbsz:4 blgp:2
	v_mfma_scale_f32_16x16x128_f8f6f4 v[142:145], v[206:209], v[174:179], v[18:21], v240, v172 op_sel_hi:[0,0,0] cbsz:4 blgp:2
	v_mfma_scale_f32_16x16x128_f8f6f4 v[90:93], v[154:157], v[180:185], v[90:93], v240, v217 op_sel_hi:[0,0,0] cbsz:4 blgp:2
	v_mfma_scale_f32_16x16x128_f8f6f4 v[74:77], v[186:189], v[180:185], v[74:77], v240, v217 op_sel_hi:[0,0,0] cbsz:4 blgp:2
	v_mfma_scale_f32_16x16x128_f8f6f4 v[58:61], v[190:193], v[180:185], v[58:61], v240, v217 op_sel_hi:[0,0,0] cbsz:4 blgp:2
	v_mfma_scale_f32_16x16x128_f8f6f4 v[26:29], v[198:201], v[180:185], v[26:29], v240, v217 op_sel_hi:[0,0,0] cbsz:4 blgp:2
	v_mfma_scale_f32_16x16x128_f8f6f4 v[34:37], v[206:209], v[148:153], v[34:37], v240, v131 op_sel_hi:[0,0,0] cbsz:4 blgp:2
	v_mfma_scale_f32_16x16x128_f8f6f4 v[146:149], v[210:213], v[174:179], v[10:13], v240, v172 op_sel_hi:[0,0,0] cbsz:4 blgp:2
	v_mfma_scale_f32_16x16x128_f8f6f4 v[42:45], v[194:197], v[180:185], v[42:45], v240, v217 op_sel_hi:[0,0,0] cbsz:4 blgp:2
	v_mfma_scale_f32_16x16x128_f8f6f4 v[150:153], v[202:205], v[180:185], v[14:17], v240, v217 op_sel_hi:[0,0,0] cbsz:4 blgp:2
	v_mfma_scale_f32_16x16x128_f8f6f4 v[172:175], v[206:209], v[180:185], v[6:9], v240, v217 op_sel_hi:[0,0,0] cbsz:4 blgp:2
	v_mfma_scale_f32_16x16x128_f8f6f4 v[176:179], v[210:213], v[180:185], v[2:5], v240, v217 op_sel_hi:[0,0,0] cbsz:4 blgp:2
	s_barrier
	ds_read_b64 v[2:3], v167
	ds_read_b64 v[4:5], v167 offset:8
	ds_read_b64 v[6:7], v167 offset:16
	ds_read_b64 v[8:9], v170
	ds_read_b64 v[10:11], v170 offset:8
	ds_read_b64 v[12:13], v170 offset:16
	ds_read_b64 v[14:15], v169
	ds_read_b64 v[16:17], v169 offset:8
	ds_read_b64 v[18:19], v169 offset:16
	s_mov_b64 s[0:1], 0x55800
	s_mov_b32 m0, s54
	ds_read_b64 v[20:21], v168
	ds_read_b64 v[22:23], v168 offset:8
	ds_read_b64 v[24:25], v168 offset:16
	v_lshl_add_u64 v[130:131], v[132:133], 0, s[0:1]
	global_load_lds_dwordx4 v[130:131], off
	v_lshl_add_u64 v[130:131], v[134:135], 0, s[0:1]
	s_mov_b32 m0, s52
	v_lshrrev_b32_e32 v167, 8, v216
	global_load_lds_dwordx4 v[130:131], off
	v_lshl_add_u64 v[130:131], v[136:137], 0, s[0:1]
	s_mov_b32 m0, s51
	v_lshrrev_b32_e32 v168, 8, v214
	global_load_lds_dwordx4 v[130:131], off
	s_waitcnt vmcnt(3)
	s_waitcnt lgkmcnt(0)
	v_lshrrev_b32_e32 v130, 8, v171
	v_lshrrev_b32_e32 v131, 8, v215
	s_barrier
	v_mfma_scale_f32_16x16x128_f8f6f4 v[126:129], v[154:157], v[2:7], v[126:129], v240, v130 op_sel_hi:[0,0,0] cbsz:4 blgp:2
	v_mfma_scale_f32_16x16x128_f8f6f4 v[122:125], v[186:189], v[2:7], v[122:125], v240, v130 op_sel_hi:[0,0,0] cbsz:4 blgp:2
	v_mfma_scale_f32_16x16x128_f8f6f4 v[114:117], v[190:193], v[2:7], v[114:117], v240, v130 op_sel_hi:[0,0,0] cbsz:4 blgp:2
	v_mfma_scale_f32_16x16x128_f8f6f4 v[102:105], v[194:197], v[2:7], v[102:105], v240, v130 op_sel_hi:[0,0,0] cbsz:4 blgp:2
	v_mfma_scale_f32_16x16x128_f8f6f4 v[86:89], v[198:201], v[2:7], v[86:89], v240, v130 op_sel_hi:[0,0,0] cbsz:4 blgp:2
	v_mfma_scale_f32_16x16x128_f8f6f4 v[70:73], v[202:205], v[2:7], v[70:73], v240, v130 op_sel_hi:[0,0,0] cbsz:4 blgp:2
	v_mfma_scale_f32_16x16x128_f8f6f4 v[54:57], v[206:209], v[2:7], v[54:57], v240, v130 op_sel_hi:[0,0,0] cbsz:4 blgp:2
	v_mfma_scale_f32_16x16x128_f8f6f4 v[38:41], v[210:213], v[2:7], v[38:41], v240, v130 op_sel_hi:[0,0,0] cbsz:4 blgp:2
	v_mfma_scale_f32_16x16x128_f8f6f4 v[118:121], v[154:157], v[8:13], v[118:121], v240, v131 op_sel_hi:[0,0,0] cbsz:4 blgp:2
	v_mfma_scale_f32_16x16x128_f8f6f4 v[110:113], v[186:189], v[8:13], v[110:113], v240, v131 op_sel_hi:[0,0,0] cbsz:4 blgp:2
	v_mfma_scale_f32_16x16x128_f8f6f4 v[98:101], v[190:193], v[8:13], v[98:101], v240, v131 op_sel_hi:[0,0,0] cbsz:4 blgp:2
	v_mfma_scale_f32_16x16x128_f8f6f4 v[82:85], v[194:197], v[8:13], v[82:85], v240, v131 op_sel_hi:[0,0,0] cbsz:4 blgp:2
	v_mfma_scale_f32_16x16x128_f8f6f4 v[66:69], v[198:201], v[8:13], v[66:69], v240, v131 op_sel_hi:[0,0,0] cbsz:4 blgp:2
	v_mfma_scale_f32_16x16x128_f8f6f4 v[50:53], v[202:205], v[8:13], v[50:53], v240, v131 op_sel_hi:[0,0,0] cbsz:4 blgp:2
	v_mfma_scale_f32_16x16x128_f8f6f4 v[34:37], v[206:209], v[8:13], v[34:37], v240, v131 op_sel_hi:[0,0,0] cbsz:4 blgp:2
	v_mfma_scale_f32_16x16x128_f8f6f4 v[130:133], v[210:213], v[8:13], v[138:141], v240, v131 op_sel_hi:[0,0,0] cbsz:4 blgp:2
	v_mfma_scale_f32_16x16x128_f8f6f4 v[106:109], v[154:157], v[14:19], v[106:109], v240, v167 op_sel_hi:[0,0,0] cbsz:4 blgp:2
	v_mfma_scale_f32_16x16x128_f8f6f4 v[94:97], v[186:189], v[14:19], v[94:97], v240, v167 op_sel_hi:[0,0,0] cbsz:4 blgp:2
	v_mfma_scale_f32_16x16x128_f8f6f4 v[78:81], v[190:193], v[14:19], v[78:81], v240, v167 op_sel_hi:[0,0,0] cbsz:4 blgp:2
	v_mfma_scale_f32_16x16x128_f8f6f4 v[62:65], v[194:197], v[14:19], v[62:65], v240, v167 op_sel_hi:[0,0,0] cbsz:4 blgp:2
	v_mfma_scale_f32_16x16x128_f8f6f4 v[46:49], v[198:201], v[14:19], v[46:49], v240, v167 op_sel_hi:[0,0,0] cbsz:4 blgp:2
	v_mfma_scale_f32_16x16x128_f8f6f4 v[30:33], v[202:205], v[14:19], v[30:33], v240, v167 op_sel_hi:[0,0,0] cbsz:4 blgp:2
	v_mfma_scale_f32_16x16x128_f8f6f4 v[134:137], v[206:209], v[14:19], v[142:145], v240, v167 op_sel_hi:[0,0,0] cbsz:4 blgp:2
	v_mfma_scale_f32_16x16x128_f8f6f4 v[138:141], v[210:213], v[14:19], v[146:149], v240, v167 op_sel_hi:[0,0,0] cbsz:4 blgp:2
	v_mfma_scale_f32_16x16x128_f8f6f4 v[90:93], v[154:157], v[20:25], v[90:93], v240, v168 op_sel_hi:[0,0,0] cbsz:4 blgp:2
	v_mfma_scale_f32_16x16x128_f8f6f4 v[74:77], v[186:189], v[20:25], v[74:77], v240, v168 op_sel_hi:[0,0,0] cbsz:4 blgp:2
	v_mfma_scale_f32_16x16x128_f8f6f4 v[58:61], v[190:193], v[20:25], v[58:61], v240, v168 op_sel_hi:[0,0,0] cbsz:4 blgp:2
	v_mfma_scale_f32_16x16x128_f8f6f4 v[26:29], v[198:201], v[20:25], v[26:29], v240, v168 op_sel_hi:[0,0,0] cbsz:4 blgp:2
	v_mfma_scale_f32_16x16x128_f8f6f4 v[142:145], v[202:205], v[20:25], v[150:153], v240, v168 op_sel_hi:[0,0,0] cbsz:4 blgp:2
	v_mfma_scale_f32_16x16x128_f8f6f4 v[42:45], v[194:197], v[20:25], v[42:45], v240, v168 op_sel_hi:[0,0,0] cbsz:4 blgp:2
	v_mfma_scale_f32_16x16x128_f8f6f4 v[146:149], v[206:209], v[20:25], v[172:175], v240, v168 op_sel_hi:[0,0,0] cbsz:4 blgp:2
	v_mfma_scale_f32_16x16x128_f8f6f4 v[150:153], v[210:213], v[20:25], v[176:179], v240, v168 op_sel_hi:[0,0,0] cbsz:4 blgp:2
	s_barrier
	ds_read_b128 v[154:157], v166
	ds_read_b128 v[168:171], v166 offset:256
	ds_read_b128 v[172:175], v166 offset:512
	ds_read_b128 v[176:179], v166 offset:768
	ds_read_b128 v[180:183], v166 offset:1024
	ds_read_b128 v[184:187], v166 offset:1280
	ds_read_b128 v[188:191], v166 offset:1536
	ds_read_b128 v[192:195], v166 offset:1792
	ds_read_b64 v[2:3], v162
	ds_read_b64 v[4:5], v162 offset:8
	ds_read_b64 v[6:7], v162 offset:16
	ds_read_b64 v[8:9], v165
	ds_read_b64 v[10:11], v165 offset:8
	ds_read_b64 v[12:13], v165 offset:16
	ds_read_b64 v[14:15], v164
	ds_read_b64 v[16:17], v164 offset:8
	ds_read_b64 v[18:19], v164 offset:16
	ds_read_b64 v[20:21], v163
	ds_read_b64 v[22:23], v163 offset:8
	ds_read_b64 v[24:25], v163 offset:16
	v_add_u32_e32 v162, 0x21800, v161
	v_add_u32_e32 v163, 0x21820, v161
	v_add_u32_e32 v164, 0x21840, v161
	v_add_u32_e32 v161, 0x21860, v161
	ds_read_u16 v166, v162
	ds_read_u16 v167, v163
	ds_read_u16 v241, v164
	ds_read_u16 v161, v161
	s_waitcnt vmcnt(0)
	s_waitcnt lgkmcnt(0)
	s_waitcnt lgkmcnt(0)
	v_mov_b32_e32 v162, v166
	v_mov_b32_e32 v200, v167
	v_mov_b32_e32 v216, v241
	v_mov_b32_e32 v242, v161
	s_barrier
	v_mfma_scale_f32_16x16x128_f8f6f4 v[126:129], v[154:157], v[2:7], v[126:129], v240, v162 op_sel_hi:[0,0,0] cbsz:4 blgp:2
	v_mfma_scale_f32_16x16x128_f8f6f4 v[122:125], v[168:171], v[2:7], v[122:125], v240, v162 op_sel_hi:[0,0,0] cbsz:4 blgp:2
	v_mfma_scale_f32_16x16x128_f8f6f4 v[114:117], v[172:175], v[2:7], v[114:117], v240, v162 op_sel_hi:[0,0,0] cbsz:4 blgp:2
	v_mfma_scale_f32_16x16x128_f8f6f4 v[102:105], v[176:179], v[2:7], v[102:105], v240, v162 op_sel_hi:[0,0,0] cbsz:4 blgp:2
	v_mfma_scale_f32_16x16x128_f8f6f4 v[86:89], v[180:183], v[2:7], v[86:89], v240, v162 op_sel_hi:[0,0,0] cbsz:4 blgp:2
	v_mfma_scale_f32_16x16x128_f8f6f4 v[70:73], v[184:187], v[2:7], v[70:73], v240, v162 op_sel_hi:[0,0,0] cbsz:4 blgp:2
	v_mfma_scale_f32_16x16x128_f8f6f4 v[54:57], v[188:191], v[2:7], v[54:57], v240, v162 op_sel_hi:[0,0,0] cbsz:4 blgp:2
	v_mfma_scale_f32_16x16x128_f8f6f4 v[2:5], v[192:195], v[2:7], v[38:41], v240, v162 op_sel_hi:[0,0,0] cbsz:4 blgp:2
	v_mfma_scale_f32_16x16x128_f8f6f4 v[118:121], v[154:157], v[8:13], v[118:121], v240, v200 op_sel_hi:[0,0,0] cbsz:4 blgp:2
	v_mfma_scale_f32_16x16x128_f8f6f4 v[110:113], v[168:171], v[8:13], v[110:113], v240, v200 op_sel_hi:[0,0,0] cbsz:4 blgp:2
	v_mfma_scale_f32_16x16x128_f8f6f4 v[98:101], v[172:175], v[8:13], v[98:101], v240, v200 op_sel_hi:[0,0,0] cbsz:4 blgp:2
	v_mfma_scale_f32_16x16x128_f8f6f4 v[82:85], v[176:179], v[8:13], v[82:85], v240, v200 op_sel_hi:[0,0,0] cbsz:4 blgp:2
	v_mfma_scale_f32_16x16x128_f8f6f4 v[66:69], v[180:183], v[8:13], v[66:69], v240, v200 op_sel_hi:[0,0,0] cbsz:4 blgp:2
	v_mfma_scale_f32_16x16x128_f8f6f4 v[106:109], v[154:157], v[14:19], v[106:109], v240, v216 op_sel_hi:[0,0,0] cbsz:4 blgp:2
	v_mfma_scale_f32_16x16x128_f8f6f4 v[94:97], v[168:171], v[14:19], v[94:97], v240, v216 op_sel_hi:[0,0,0] cbsz:4 blgp:2
	v_mfma_scale_f32_16x16x128_f8f6f4 v[78:81], v[172:175], v[14:19], v[78:81], v240, v216 op_sel_hi:[0,0,0] cbsz:4 blgp:2
	v_mfma_scale_f32_16x16x128_f8f6f4 v[62:65], v[176:179], v[14:19], v[62:65], v240, v216 op_sel_hi:[0,0,0] cbsz:4 blgp:2
	v_mfma_scale_f32_16x16x128_f8f6f4 v[74:77], v[168:171], v[20:25], v[74:77], v240, v242 op_sel_hi:[0,0,0] cbsz:4 blgp:2
	v_mfma_scale_f32_16x16x128_f8f6f4 v[58:61], v[172:175], v[20:25], v[58:61], v240, v242 op_sel_hi:[0,0,0] cbsz:4 blgp:2
	v_mfma_scale_f32_16x16x128_f8f6f4 v[162:165], v[184:187], v[8:13], v[50:53], v240, v200 op_sel_hi:[0,0,0] cbsz:4 blgp:2
	v_mfma_scale_f32_16x16x128_f8f6f4 v[196:199], v[188:191], v[8:13], v[34:37], v240, v200 op_sel_hi:[0,0,0] cbsz:4 blgp:2
	v_mfma_scale_f32_16x16x128_f8f6f4 v[200:203], v[192:195], v[8:13], v[130:133], v240, v200 op_sel_hi:[0,0,0] cbsz:4 blgp:2
	v_mfma_scale_f32_16x16x128_f8f6f4 v[204:207], v[180:183], v[14:19], v[46:49], v240, v216 op_sel_hi:[0,0,0] cbsz:4 blgp:2
	v_mfma_scale_f32_16x16x128_f8f6f4 v[208:211], v[184:187], v[14:19], v[30:33], v240, v216 op_sel_hi:[0,0,0] cbsz:4 blgp:2
	v_mfma_scale_f32_16x16x128_f8f6f4 v[212:215], v[188:191], v[14:19], v[134:137], v240, v216 op_sel_hi:[0,0,0] cbsz:4 blgp:2
	v_mfma_scale_f32_16x16x128_f8f6f4 v[216:219], v[192:195], v[14:19], v[138:141], v240, v216 op_sel_hi:[0,0,0] cbsz:4 blgp:2
	v_mfma_scale_f32_16x16x128_f8f6f4 v[220:223], v[154:157], v[20:25], v[90:93], v240, v242 op_sel_hi:[0,0,0] cbsz:4 blgp:2
	v_mfma_scale_f32_16x16x128_f8f6f4 v[224:227], v[176:179], v[20:25], v[42:45], v240, v242 op_sel_hi:[0,0,0] cbsz:4 blgp:2
	v_mfma_scale_f32_16x16x128_f8f6f4 v[228:231], v[180:183], v[20:25], v[26:29], v240, v242 op_sel_hi:[0,0,0] cbsz:4 blgp:2
	v_mfma_scale_f32_16x16x128_f8f6f4 v[232:235], v[184:187], v[20:25], v[142:145], v240, v242 op_sel_hi:[0,0,0] cbsz:4 blgp:2
	v_mfma_scale_f32_16x16x128_f8f6f4 v[236:239], v[188:191], v[20:25], v[146:149], v240, v242 op_sel_hi:[0,0,0] cbsz:4 blgp:2
	v_mfma_scale_f32_16x16x128_f8f6f4 v[150:153], v[192:195], v[20:25], v[150:153], v240, v242 op_sel_hi:[0,0,0] cbsz:4 blgp:2
	s_barrier
	ds_read_b64 v[34:35], v1
	ds_read_b64 v[36:37], v1 offset:8
	ds_read_b64 v[38:39], v1 offset:16
	ds_read_b64 v[40:41], v160
	ds_read_b64 v[42:43], v160 offset:8
	ds_read_b64 v[44:45], v160 offset:16
	ds_read_b64 v[46:47], v159
	ds_read_b64 v[48:49], v159 offset:8
	ds_read_b64 v[50:51], v159 offset:16
	ds_read_b64 v[144:145], v158
	ds_read_b64 v[146:147], v158 offset:8
	ds_read_b64 v[148:149], v158 offset:16
	s_waitcnt lgkmcnt(0)
	v_lshrrev_b32_e32 v1, 8, v166
	v_lshrrev_b32_e32 v52, 8, v167
	v_lshrrev_b32_e32 v53, 8, v241
	v_lshrrev_b32_e32 v158, 8, v161
	s_barrier
	v_mfma_scale_f32_16x16x128_f8f6f4 v[30:33], v[154:157], v[34:39], v[126:129], v240, v1 op_sel_hi:[0,0,0] cbsz:4 blgp:2
	v_mfma_scale_f32_16x16x128_f8f6f4 v[22:25], v[168:171], v[34:39], v[122:125], v240, v1 op_sel_hi:[0,0,0] cbsz:4 blgp:2
	v_mfma_scale_f32_16x16x128_f8f6f4 v[14:17], v[172:175], v[34:39], v[114:117], v240, v1 op_sel_hi:[0,0,0] cbsz:4 blgp:2
	v_mfma_scale_f32_16x16x128_f8f6f4 v[6:9], v[176:179], v[34:39], v[102:105], v240, v1 op_sel_hi:[0,0,0] cbsz:4 blgp:2
	v_mfma_scale_f32_16x16x128_f8f6f4 v[26:29], v[180:183], v[34:39], v[86:89], v240, v1 op_sel_hi:[0,0,0] cbsz:4 blgp:2
	v_mfma_scale_f32_16x16x128_f8f6f4 v[18:21], v[184:187], v[34:39], v[70:73], v240, v1 op_sel_hi:[0,0,0] cbsz:4 blgp:2
	v_mfma_scale_f32_16x16x128_f8f6f4 v[10:13], v[188:191], v[34:39], v[54:57], v240, v1 op_sel_hi:[0,0,0] cbsz:4 blgp:2
	v_mfma_scale_f32_16x16x128_f8f6f4 v[2:5], v[192:195], v[34:39], v[2:5], v240, v1 op_sel_hi:[0,0,0] cbsz:4 blgp:2
	v_mfma_scale_f32_16x16x128_f8f6f4 v[132:135], v[154:157], v[40:45], v[118:121], v240, v52 op_sel_hi:[0,0,0] cbsz:4 blgp:2
	v_mfma_scale_f32_16x16x128_f8f6f4 v[128:131], v[168:171], v[40:45], v[110:113], v240, v52 op_sel_hi:[0,0,0] cbsz:4 blgp:2
	v_mfma_scale_f32_16x16x128_f8f6f4 v[124:127], v[172:175], v[40:45], v[98:101], v240, v52 op_sel_hi:[0,0,0] cbsz:4 blgp:2
	v_mfma_scale_f32_16x16x128_f8f6f4 v[116:119], v[176:179], v[40:45], v[82:85], v240, v52 op_sel_hi:[0,0,0] cbsz:4 blgp:2
	v_mfma_scale_f32_16x16x128_f8f6f4 v[140:143], v[180:183], v[40:45], v[66:69], v240, v52 op_sel_hi:[0,0,0] cbsz:4 blgp:2
	v_mfma_scale_f32_16x16x128_f8f6f4 v[136:139], v[184:187], v[40:45], v[162:165], v240, v52 op_sel_hi:[0,0,0] cbsz:4 blgp:2
	v_mfma_scale_f32_16x16x128_f8f6f4 v[120:123], v[188:191], v[40:45], v[196:199], v240, v52 op_sel_hi:[0,0,0] cbsz:4 blgp:2
	v_mfma_scale_f32_16x16x128_f8f6f4 v[112:115], v[192:195], v[40:45], v[200:203], v240, v52 op_sel_hi:[0,0,0] cbsz:4 blgp:2
	v_mfma_scale_f32_16x16x128_f8f6f4 v[100:103], v[154:157], v[46:51], v[106:109], v240, v53 op_sel_hi:[0,0,0] cbsz:4 blgp:2
	v_mfma_scale_f32_16x16x128_f8f6f4 v[96:99], v[168:171], v[46:51], v[94:97], v240, v53 op_sel_hi:[0,0,0] cbsz:4 blgp:2
	v_mfma_scale_f32_16x16x128_f8f6f4 v[92:95], v[172:175], v[46:51], v[78:81], v240, v53 op_sel_hi:[0,0,0] cbsz:4 blgp:2
	v_mfma_scale_f32_16x16x128_f8f6f4 v[84:87], v[176:179], v[46:51], v[62:65], v240, v53 op_sel_hi:[0,0,0] cbsz:4 blgp:2
	v_mfma_scale_f32_16x16x128_f8f6f4 v[108:111], v[180:183], v[46:51], v[204:207], v240, v53 op_sel_hi:[0,0,0] cbsz:4 blgp:2
	v_mfma_scale_f32_16x16x128_f8f6f4 v[104:107], v[184:187], v[46:51], v[208:211], v240, v53 op_sel_hi:[0,0,0] cbsz:4 blgp:2
	v_mfma_scale_f32_16x16x128_f8f6f4 v[88:91], v[188:191], v[46:51], v[212:215], v240, v53 op_sel_hi:[0,0,0] cbsz:4 blgp:2
	v_mfma_scale_f32_16x16x128_f8f6f4 v[80:83], v[192:195], v[46:51], v[216:219], v240, v53 op_sel_hi:[0,0,0] cbsz:4 blgp:2
	v_mfma_scale_f32_16x16x128_f8f6f4 v[68:71], v[154:157], v[144:149], v[220:223], v240, v158 op_sel_hi:[0,0,0] cbsz:4 blgp:2
	v_mfma_scale_f32_16x16x128_f8f6f4 v[64:67], v[168:171], v[144:149], v[74:77], v240, v158 op_sel_hi:[0,0,0] cbsz:4 blgp:2
	v_mfma_scale_f32_16x16x128_f8f6f4 v[60:63], v[172:175], v[144:149], v[58:61], v240, v158 op_sel_hi:[0,0,0] cbsz:4 blgp:2
	v_mfma_scale_f32_16x16x128_f8f6f4 v[52:55], v[176:179], v[144:149], v[224:227], v240, v158 op_sel_hi:[0,0,0] cbsz:4 blgp:2
	v_mfma_scale_f32_16x16x128_f8f6f4 v[76:79], v[180:183], v[144:149], v[228:231], v240, v158 op_sel_hi:[0,0,0] cbsz:4 blgp:2
	v_mfma_scale_f32_16x16x128_f8f6f4 v[72:75], v[184:187], v[144:149], v[232:235], v240, v158 op_sel_hi:[0,0,0] cbsz:4 blgp:2
	v_mfma_scale_f32_16x16x128_f8f6f4 v[56:59], v[188:191], v[144:149], v[236:239], v240, v158 op_sel_hi:[0,0,0] cbsz:4 blgp:2
	v_mfma_scale_f32_16x16x128_f8f6f4 v[48:51], v[192:195], v[144:149], v[150:153], v240, v158 op_sel_hi:[0,0,0] cbsz:4 blgp:2
	v_ashrrev_i32_e32 v244, 7, v0
	v_and_b32_e32 v244, -2, v244
	v_lshl_add_u32 v244, s14, 2, v244
	v_bfe_u32 v245, v0, 5, 1
	v_or_b32_e32 v244, v244, v245
	v_lshlrev_b32_e32 v244, 5, v244
	v_bfe_u32 v245, v0, 4, 1
	v_lshl_or_b32 v244, v245, 2, v244
	v_lshlrev_b32_e32 v244, 2, v244
	global_load_dwordx4 v[184:187], v244, s[8:9]
	global_load_dwordx4 v[188:191], v244, s[10:11]
	global_load_dwordx4 v[192:195], v244, s[8:9] offset:64
	global_load_dwordx4 v[196:199], v244, s[10:11] offset:64
	global_load_dwordx4 v[200:203], v244, s[8:9] offset:32
	global_load_dwordx4 v[204:207], v244, s[10:11] offset:32
	global_load_dwordx4 v[208:211], v244, s[8:9] offset:96
	global_load_dwordx4 v[212:215], v244, s[10:11] offset:96
	s_barrier
	s_cmpk_gt_u32 s33, 0xff
	s_cbranch_scc1 .LBB2_6
	s_barrier
.LBB2_6:
	s_mov_b32 s6, 0
	s_ashr_i32 s7, s6, 31
	v_add_u32_e32 v144, s6, v0
	v_ashrrev_i32_e32 v0, 7, v144
	v_and_b32_e32 v0, -2, v0
	v_bfe_u32 v147, v144, 5, 1
	v_lshl_add_u32 v148, s14, 2, v0
	v_bfe_u32 v146, v144, 4, 1
	v_or_b32_e32 v0, v148, v147
	v_lshlrev_b32_e32 v42, 5, v0
	v_lshlrev_b32_e32 v0, 2, v146
	s_lshl_b64 s[4:5], s[6:7], 2
	v_or_b32_e32 v0, v42, v0
	s_add_u32 s0, s8, s4
	v_ashrrev_i32_e32 v1, 31, v0
	s_addc_u32 s1, s9, s5
	v_lshlrev_b64 v[38:39], 2, v[0:1]
	v_lshl_add_u64 v[150:151], s[0:1], 0, v[38:39]
	s_add_u32 s4, s10, s4
	s_addc_u32 s5, s11, s5
	v_lshl_add_u64 v[152:153], s[4:5], 0, v[38:39]
	v_ashrrev_i32_e32 v1, 31, v42
	v_lshlrev_b64 v[42:43], 2, v[0:1]
	v_lshl_add_u64 v[154:155], s[0:1], 0, v[42:43]
	v_lshl_add_u64 v[156:157], s[4:5], 0, v[42:43]
	v_or_b32_e32 v0, 8, v0
	v_lshlrev_b64 v[0:1], 2, v[0:1]
	v_lshl_add_u64 v[158:159], s[0:1], 0, v[0:1]
	v_lshl_add_u64 v[160:161], s[4:5], 0, v[0:1]
	v_ashrrev_i32_e32 v0, 1, v148
	v_lshl_add_u32 v0, s2, 6, v0
	s_movk_i32 s3, 0x6000
	v_mov_b64_e32 v[46:47], s[12:13]
	v_ashrrev_i32_e32 v1, 31, v0
	v_mad_i64_i32 v[148:149], s[2:3], v0, s3, v[46:47]
	v_lshlrev_b64 v[0:1], 10, v[0:1]
	s_mov_b64 s[6:7], 0x3000000
	v_permlane32_swap_b32_e32 v30, v14
	v_permlane32_swap_b32_e32 v31, v15
	v_lshl_add_u64 v[0:1], s[12:13], 0, v[0:1]
	v_permlane32_swap_b32_e32 v32, v16
	v_permlane32_swap_b32_e32 v33, v17
	s_mov_b32 s4, 0xbfb8aa3b
	v_and_b32_e32 v163, 0xcf, v144
	v_lshlrev_b32_e32 v162, 9, v147
	v_mul_u32_u24_e32 v144, 12, v146
	v_cmp_eq_u32_e64 s[0:1], 0, v146
	v_lshl_add_u64 v[146:147], v[0:1], 0, s[6:7]
	v_permlane32_swap_b32_e32 v26, v10
	v_permlane32_swap_b32_e32 v27, v11
	v_permlane32_swap_b32_e32 v22, v6
	v_permlane32_swap_b32_e32 v23, v7
	v_permlane32_swap_b32_e32 v28, v12
	v_permlane32_swap_b32_e32 v29, v13
	v_permlane32_swap_b32_e32 v24, v8
	v_permlane32_swap_b32_e32 v25, v9
	v_permlane32_swap_b32_e32 v18, v2
	v_permlane32_swap_b32_e32 v19, v3
	v_permlane32_swap_b32_e32 v20, v4
	v_permlane32_swap_b32_e32 v21, v5
	s_mov_b32 s3, 0x700000
	s_mov_b32 s8, 0x42000000
	s_mov_b32 s2, 0xc2000000
	v_mov_b32_e32 v145, 0
	s_waitcnt vmcnt(0)
	v_pk_mul_f32 v[0:1], v[184:185], v[30:31]
	v_pk_mul_f32 v[30:31], v[186:187], v[32:33]
	v_pk_mul_f32 v[32:33], v[0:1], s[4:5] op_sel_hi:[1,0]
	v_pk_mul_f32 v[34:35], v[30:31], s[4:5] op_sel_hi:[1,0]
	v_exp_f32_e32 v32, v32
	v_exp_f32_e32 v33, v33
	v_exp_f32_e32 v34, v34
	v_exp_f32_e32 v35, v35
	v_pk_mul_f32 v[26:27], v[188:189], v[26:27]
	v_pk_add_f32 v[32:33], v[32:33], 1.0 op_sel_hi:[1,0]
	v_pk_mul_f32 v[22:23], v[192:193], v[22:23]
	v_rcp_f32_e32 v32, v32
	v_rcp_f32_e32 v33, v33
	v_pk_add_f32 v[34:35], v[34:35], 1.0 op_sel_hi:[1,0]
	v_pk_mul_f32 v[24:25], v[194:195], v[24:25]
	v_rcp_f32_e32 v34, v34
	v_rcp_f32_e32 v35, v35
	v_pk_mul_f32 v[0:1], v[0:1], v[32:33]
	v_pk_mul_f32 v[18:19], v[196:197], v[18:19]
	v_pk_mul_f32 v[0:1], v[26:27], v[0:1]
	v_pk_mul_f32 v[26:27], v[190:191], v[28:29]
	v_pk_mul_f32 v[28:29], v[30:31], v[34:35]
	v_pk_mul_f32 v[30:31], v[24:25], s[4:5] op_sel_hi:[1,0]
	v_pk_mul_f32 v[26:27], v[26:27], v[28:29]
	v_pk_mul_f32 v[28:29], v[22:23], s[4:5] op_sel_hi:[1,0]
	v_exp_f32_e32 v30, v30
	v_exp_f32_e32 v28, v28
	v_exp_f32_e32 v29, v29
	v_exp_f32_e32 v31, v31
	v_pk_mul_f32 v[20:21], v[198:199], v[20:21]
	v_pk_mul_f32 v[14:15], v[200:201], v[14:15]
	v_pk_add_f32 v[28:29], v[28:29], 1.0 op_sel_hi:[1,0]
	v_pk_add_f32 v[30:31], v[30:31], 1.0 op_sel_hi:[1,0]
	v_rcp_f32_e32 v28, v28
	v_rcp_f32_e32 v29, v29
	v_rcp_f32_e32 v30, v30
	v_rcp_f32_e32 v31, v31
	v_pk_mul_f32 v[16:17], v[202:203], v[16:17]
	v_pk_mul_f32 v[22:23], v[22:23], v[28:29]
	v_pk_mul_f32 v[10:11], v[204:205], v[10:11]
	v_pk_mul_f32 v[18:19], v[18:19], v[22:23]
	v_pk_mul_f32 v[22:23], v[24:25], v[30:31]
	v_pk_mul_f32 v[24:25], v[16:17], s[4:5] op_sel_hi:[1,0]
	v_pk_mul_f32 v[20:21], v[20:21], v[22:23]
	v_pk_mul_f32 v[22:23], v[14:15], s[4:5] op_sel_hi:[1,0]
	v_exp_f32_e32 v24, v24
	v_exp_f32_e32 v22, v22
	v_exp_f32_e32 v23, v23
	v_exp_f32_e32 v25, v25
	v_pk_mul_f32 v[12:13], v[206:207], v[12:13]
	v_pk_mul_f32 v[6:7], v[208:209], v[6:7]
	v_pk_add_f32 v[22:23], v[22:23], 1.0 op_sel_hi:[1,0]
	v_pk_add_f32 v[24:25], v[24:25], 1.0 op_sel_hi:[1,0]
	v_rcp_f32_e32 v22, v22
	v_rcp_f32_e32 v23, v23
	v_rcp_f32_e32 v24, v24
	v_rcp_f32_e32 v25, v25
	v_pk_mul_f32 v[8:9], v[210:211], v[8:9]
	v_pk_mul_f32 v[14:15], v[14:15], v[22:23]
	v_pk_mul_f32 v[2:3], v[212:213], v[2:3]
	v_pk_mul_f32 v[10:11], v[10:11], v[14:15]
	v_pk_mul_f32 v[14:15], v[16:17], v[24:25]
	v_pk_mul_f32 v[16:17], v[8:9], s[4:5] op_sel_hi:[1,0]
	v_pk_mul_f32 v[12:13], v[12:13], v[14:15]
	v_pk_mul_f32 v[14:15], v[6:7], s[4:5] op_sel_hi:[1,0]
	v_exp_f32_e32 v16, v16
	v_exp_f32_e32 v14, v14
	v_exp_f32_e32 v15, v15
	v_exp_f32_e32 v17, v17
	v_pk_mul_f32 v[4:5], v[214:215], v[4:5]
	v_mov_b32_e32 v164, 0xffffff7f
	v_pk_add_f32 v[14:15], v[14:15], 1.0 op_sel_hi:[1,0]
	v_pk_add_f32 v[16:17], v[16:17], 1.0 op_sel_hi:[1,0]
	v_rcp_f32_e32 v14, v14
	v_rcp_f32_e32 v15, v15
	v_rcp_f32_e32 v16, v16
	v_rcp_f32_e32 v17, v17
	s_movk_i32 s5, 0xff9c
	v_pk_mul_f32 v[6:7], v[6:7], v[14:15]
	v_mov_b32_e32 v165, 0x64
	v_pk_mul_f32 v[2:3], v[2:3], v[6:7]
	v_pk_mul_f32 v[6:7], v[8:9], v[16:17]
	v_pk_mul_f32 v[4:5], v[4:5], v[6:7]
	v_max3_f32 v6, |v20|, |v21|, |v0|
	v_max3_f32 v6, v6, |v1|, |v26|
	v_max3_f32 v6, v6, |v27|, |v18|
	v_max3_f32 v6, v6, |v19|, |v10|
	v_max3_f32 v6, v6, |v11|, |v12|
	v_max3_f32 v6, v6, |v13|, |v2|
	v_max3_f32 v6, v6, |v3|, |v4|
	v_max_f32_e64 v6, v6, |v5|
	v_mov_b32_e32 v7, v6
	s_nop 1
	v_permlane16_swap_b32_e32 v6, v7
	v_max_f32_e32 v6, v6, v7
	v_lshrrev_b32_e32 v7, 23, v6
	v_and_b32_e32 v6, 0x7fffff, v6
	v_cmp_lt_u32_e32 vcc, s3, v6
	s_nop 1
	v_addc_co_u32_e32 v6, vcc, v7, v164, vcc
	v_med3_i32 v166, v6, s5, v165
	v_lshlrev_b32_e32 v6, 23, v166
	v_sub_u32_e32 v6, 1.0, v6
	v_pk_mul_f32 v[40:41], v[6:7], v[10:11] op_sel_hi:[0,1]
	v_pk_mul_f32 v[42:43], v[6:7], v[12:13] op_sel_hi:[0,1]
	v_pk_mul_f32 v[44:45], v[6:7], v[2:3] op_sel_hi:[0,1]
	v_pk_mul_f32 v[46:47], v[6:7], v[4:5] op_sel_hi:[0,1]
	v_pk_mul_f32 v[32:33], v[6:7], v[0:1] op_sel_hi:[0,1]
	v_pk_mul_f32 v[34:35], v[6:7], v[26:27] op_sel_hi:[0,1]
	v_pk_mul_f32 v[36:37], v[6:7], v[18:19] op_sel_hi:[0,1]
	v_pk_mul_f32 v[38:39], v[6:7], v[20:21] op_sel_hi:[0,1]
	v_cvt_scalef32_2xpk16_fp6_f32 v[168:173], v[32:47], v[40:55], 1.0
	v_cvt_scalef32_pk32_f32_fp6 v[0:31], v[168:173], s8
	v_fma_f32 v16, v32, s2, v0
	v_fma_f32 v17, v33, s2, v2
	v_fma_f32 v18, v34, s2, v4
	v_fma_f32 v19, v35, s2, v6
	v_fma_f32 v20, v36, s2, v8
	v_fma_f32 v21, v37, s2, v10
	v_fma_f32 v22, v38, s2, v12
	v_fma_f32 v23, v39, s2, v14
	v_fma_f32 v24, v40, s2, v1
	v_fma_f32 v25, v41, s2, v3
	v_fma_f32 v26, v42, s2, v5
	v_fma_f32 v27, v43, s2, v7
	v_fma_f32 v28, v44, s2, v9
	v_fma_f32 v29, v45, s2, v11
	v_fma_f32 v30, v46, s2, v13
	v_fma_f32 v31, v47, s2, v15
	v_cvt_scalef32_2xpk16_fp6_f32 v[0:5], v[16:31], v[24:39], 1.0
	v_or_b32_e32 v3, v163, v162
	v_mul_u32_u24_e32 v4, 24, v3
	v_mov_b32_e32 v5, v145
	v_lshl_add_u64 v[4:5], v[148:149], 0, v[4:5]
	v_lshl_add_u64 v[4:5], v[4:5], 0, v[144:145]
	global_store_dwordx3 v[4:5], v[168:170], off nt
	v_add_co_u32_e32 v4, vcc, 0x1000, v4
	v_xor_b32_e32 v0, 0x20820820, v0
	v_xor_b32_e32 v1, 0x8208208, v1
	v_xor_b32_e32 v2, 0x82082082, v2
	v_addc_co_u32_e32 v5, vcc, 0, v5, vcc
	global_store_dwordx3 v[4:5], v[0:2], off offset:2048 nt
	s_and_saveexec_b64 s[6:7], s[0:1]
	s_cbranch_execz .LBB2_8
	v_mov_b32_e32 v1, 0x7a00
	v_add_u32_e32 v0, 0x7f, v166
	v_lshl_add_u32 v1, v166, 8, v1
	v_or_b32_e32 v2, v1, v0
	v_lshl_or_b32 v0, v163, 1, v162
	v_mov_b32_e32 v1, v145
	v_lshl_add_u64 v[0:1], v[146:147], 0, v[0:1]
	global_store_short v[0:1], v2, off
.LBB2_8:
	s_or_b64 exec, exec, s[6:7]
	v_permlane32_swap_b32_e32 v132, v124
	v_permlane32_swap_b32_e32 v133, v125
	v_permlane32_swap_b32_e32 v128, v116
	v_permlane32_swap_b32_e32 v129, v117
	v_permlane32_swap_b32_e32 v134, v126
	v_permlane32_swap_b32_e32 v135, v127
	v_permlane32_swap_b32_e32 v130, v118
	v_permlane32_swap_b32_e32 v131, v119
	v_permlane32_swap_b32_e32 v140, v120
	v_permlane32_swap_b32_e32 v141, v121
	v_permlane32_swap_b32_e32 v136, v112
	v_permlane32_swap_b32_e32 v137, v113
	v_permlane32_swap_b32_e32 v142, v122
	v_permlane32_swap_b32_e32 v143, v123
	v_permlane32_swap_b32_e32 v138, v114
	v_permlane32_swap_b32_e32 v139, v115
	v_pk_mul_f32 v[0:1], v[184:185], v[132:133]
	s_nop 0
	v_pk_mul_f32 v[32:33], v[0:1], s[4:5] op_sel_hi:[1,0]
	v_pk_mul_f32 v[8:9], v[192:193], v[128:129]
	v_exp_f32_e32 v32, v32
	v_pk_mul_f32 v[36:37], v[8:9], s[4:5] op_sel_hi:[1,0]
	v_exp_f32_e32 v33, v33
	v_exp_f32_e32 v36, v36
	v_exp_f32_e32 v37, v37
	v_pk_mul_f32 v[18:19], v[202:203], v[126:127]
	v_pk_mul_f32 v[2:3], v[186:187], v[134:135]
	v_pk_mul_f32 v[10:11], v[194:195], v[130:131]
	v_pk_mul_f32 v[42:43], v[18:19], s[4:5] op_sel_hi:[1,0]
	v_pk_add_f32 v[32:33], v[32:33], 1.0 op_sel_hi:[1,0]
	v_pk_add_f32 v[36:37], v[36:37], 1.0 op_sel_hi:[1,0]
	v_pk_mul_f32 v[16:17], v[200:201], v[124:125]
	v_pk_mul_f32 v[34:35], v[2:3], s[4:5] op_sel_hi:[1,0]
	v_pk_mul_f32 v[38:39], v[10:11], s[4:5] op_sel_hi:[1,0]
	v_exp_f32_e32 v42, v42
	v_exp_f32_e32 v43, v43
	v_rcp_f32_e32 v32, v32
	v_rcp_f32_e32 v33, v33
	v_rcp_f32_e32 v36, v36
	v_rcp_f32_e32 v37, v37
	v_pk_mul_f32 v[40:41], v[16:17], s[4:5] op_sel_hi:[1,0]
	v_exp_f32_e32 v34, v34
	v_exp_f32_e32 v35, v35
	v_exp_f32_e32 v38, v38
	v_exp_f32_e32 v39, v39
	v_exp_f32_e32 v40, v40
	v_exp_f32_e32 v41, v41
	v_pk_mul_f32 v[4:5], v[188:189], v[140:141]
	v_pk_mul_f32 v[12:13], v[196:197], v[136:137]
	v_pk_add_f32 v[42:43], v[42:43], 1.0 op_sel_hi:[1,0]
	v_pk_mul_f32 v[0:1], v[0:1], v[32:33]
	v_pk_mul_f32 v[8:9], v[8:9], v[36:37]
	v_pk_add_f32 v[34:35], v[34:35], 1.0 op_sel_hi:[1,0]
	v_pk_add_f32 v[38:39], v[38:39], 1.0 op_sel_hi:[1,0]
	v_pk_mul_f32 v[0:1], v[4:5], v[0:1]
	v_pk_mul_f32 v[4:5], v[12:13], v[8:9]
	v_rcp_f32_e32 v8, v42
	v_rcp_f32_e32 v9, v43
	v_pk_add_f32 v[40:41], v[40:41], 1.0 op_sel_hi:[1,0]
	v_rcp_f32_e32 v34, v34
	v_rcp_f32_e32 v35, v35
	v_rcp_f32_e32 v38, v38
	v_rcp_f32_e32 v39, v39
	v_rcp_f32_e32 v40, v40
	v_rcp_f32_e32 v41, v41
	v_pk_mul_f32 v[12:13], v[206:207], v[122:123]
	v_pk_mul_f32 v[8:9], v[18:19], v[8:9]
	v_pk_mul_f32 v[6:7], v[190:191], v[142:143]
	v_pk_mul_f32 v[14:15], v[198:199], v[138:139]
	v_pk_mul_f32 v[2:3], v[2:3], v[34:35]
	v_pk_mul_f32 v[10:11], v[10:11], v[38:39]
	v_pk_mul_f32 v[8:9], v[12:13], v[8:9]
	v_pk_mul_f32 v[12:13], v[208:209], v[116:117]
	v_pk_mul_f32 v[20:21], v[204:205], v[120:121]
	v_pk_mul_f32 v[2:3], v[6:7], v[2:3]
	v_pk_mul_f32 v[6:7], v[14:15], v[10:11]
	v_pk_mul_f32 v[10:11], v[16:17], v[40:41]
	v_pk_mul_f32 v[16:17], v[12:13], s[4:5] op_sel_hi:[1,0]
	v_pk_mul_f32 v[18:19], v[210:211], v[118:119]
	v_pk_mul_f32 v[10:11], v[20:21], v[10:11]
	v_exp_f32_e32 v16, v16
	v_exp_f32_e32 v17, v17
	v_pk_mul_f32 v[20:21], v[18:19], s[4:5] op_sel_hi:[1,0]
	v_pk_mul_f32 v[14:15], v[212:213], v[112:113]
	v_exp_f32_e32 v20, v20
	v_exp_f32_e32 v21, v21
	v_pk_add_f32 v[16:17], v[16:17], 1.0 op_sel_hi:[1,0]
	v_pk_add_f32 v[20:21], v[20:21], 1.0 op_sel_hi:[1,0]
	v_rcp_f32_e32 v16, v16
	v_rcp_f32_e32 v17, v17
	v_rcp_f32_e32 v20, v20
	v_rcp_f32_e32 v21, v21
	v_pk_mul_f32 v[12:13], v[12:13], v[16:17]
	s_nop 0
	v_pk_mul_f32 v[12:13], v[14:15], v[12:13]
	v_pk_mul_f32 v[14:15], v[214:215], v[114:115]
	v_pk_mul_f32 v[16:17], v[18:19], v[20:21]
	v_pk_mul_f32 v[14:15], v[14:15], v[16:17]
	v_max3_f32 v16, |v6|, |v7|, |v0|
	v_max3_f32 v16, v16, |v1|, |v2|
	v_max3_f32 v16, v16, |v3|, |v4|
	v_max3_f32 v16, v16, |v5|, |v10|
	v_max3_f32 v16, v16, |v11|, |v8|
	v_max3_f32 v16, v16, |v9|, |v12|
	v_max3_f32 v16, v16, |v13|, |v14|
	v_max_f32_e64 v16, v16, |v15|
	v_mov_b32_e32 v17, v16
	s_nop 1
	v_permlane16_swap_b32_e32 v16, v17
	v_max_f32_e32 v16, v16, v17
	v_lshrrev_b32_e32 v17, 23, v16
	v_and_b32_e32 v16, 0x7fffff, v16
	v_cmp_lt_u32_e32 vcc, s3, v16
	s_nop 1
	v_addc_co_u32_e32 v16, vcc, v17, v164, vcc
	v_med3_i32 v112, v16, s5, v165
	v_lshlrev_b32_e32 v16, 23, v112
	v_sub_u32_e32 v16, 1.0, v16
	v_pk_mul_f32 v[40:41], v[16:17], v[10:11] op_sel_hi:[0,1]
	v_pk_mul_f32 v[42:43], v[16:17], v[8:9] op_sel_hi:[0,1]
	v_pk_mul_f32 v[44:45], v[16:17], v[12:13] op_sel_hi:[0,1]
	v_pk_mul_f32 v[46:47], v[16:17], v[14:15] op_sel_hi:[0,1]
	v_pk_mul_f32 v[32:33], v[16:17], v[0:1] op_sel_hi:[0,1]
	v_pk_mul_f32 v[34:35], v[16:17], v[2:3] op_sel_hi:[0,1]
	v_pk_mul_f32 v[36:37], v[16:17], v[4:5] op_sel_hi:[0,1]
	v_pk_mul_f32 v[38:39], v[16:17], v[6:7] op_sel_hi:[0,1]
	v_cvt_scalef32_2xpk16_fp6_f32 v[114:119], v[32:47], v[40:55], 1.0
	v_cvt_scalef32_pk32_f32_fp6 v[0:31], v[114:119], s8
	v_fma_f32 v16, v32, s2, v0
	v_fma_f32 v17, v33, s2, v2
	v_fma_f32 v18, v34, s2, v4
	v_fma_f32 v19, v35, s2, v6
	v_fma_f32 v20, v36, s2, v8
	v_fma_f32 v21, v37, s2, v10
	v_fma_f32 v22, v38, s2, v12
	v_fma_f32 v23, v39, s2, v14
	v_fma_f32 v24, v40, s2, v1
	v_fma_f32 v25, v41, s2, v3
	v_fma_f32 v26, v42, s2, v5
	v_fma_f32 v27, v43, s2, v7
	v_fma_f32 v28, v44, s2, v9
	v_fma_f32 v29, v45, s2, v11
	v_fma_f32 v30, v46, s2, v13
	v_fma_f32 v31, v47, s2, v15
	v_cvt_scalef32_2xpk16_fp6_f32 v[0:5], v[16:31], v[24:39], 1.0
	v_xor_b32_e32 v4, 0x20820820, v0
	v_or_b32_e32 v0, 16, v163
	v_xor_b32_e32 v5, 0x8208208, v1
	v_or_b32_e32 v1, v0, v162
	v_xor_b32_e32 v6, 0x82082082, v2
	v_mul_u32_u24_e32 v2, 24, v1
	v_mov_b32_e32 v3, v145
	v_lshl_add_u64 v[2:3], v[148:149], 0, v[2:3]
	v_lshl_add_u64 v[2:3], v[2:3], 0, v[144:145]
	global_store_dwordx3 v[2:3], v[114:116], off nt
	v_add_co_u32_e32 v2, vcc, 0x1000, v2
	s_nop 1
	v_addc_co_u32_e32 v3, vcc, 0, v3, vcc
	global_store_dwordx3 v[2:3], v[4:6], off offset:2048 nt
	s_and_saveexec_b64 s[2:3], s[0:1]
	s_cbranch_execz .LBB2_10
	v_mov_b32_e32 v2, 0x7a00
	v_add_u32_e32 v1, 0x7f, v112
	v_lshl_add_u32 v2, v112, 8, v2
	v_or_b32_e32 v2, v2, v1
	v_lshl_or_b32 v0, v0, 1, v162
	v_mov_b32_e32 v1, 0
	v_lshl_add_u64 v[0:1], v[146:147], 0, v[0:1]
	global_store_short v[0:1], v2, off
.LBB2_10:
	s_or_b64 exec, exec, s[2:3]
	v_permlane32_swap_b32_e32 v100, v92
	v_permlane32_swap_b32_e32 v101, v93
	v_permlane32_swap_b32_e32 v96, v84
	v_permlane32_swap_b32_e32 v97, v85
	s_mov_b32 s2, 0xbfb8aa3b
	v_permlane32_swap_b32_e32 v102, v94
	v_permlane32_swap_b32_e32 v103, v95
	v_permlane32_swap_b32_e32 v98, v86
	v_permlane32_swap_b32_e32 v99, v87
	v_permlane32_swap_b32_e32 v108, v88
	v_permlane32_swap_b32_e32 v109, v89
	v_permlane32_swap_b32_e32 v104, v80
	v_permlane32_swap_b32_e32 v105, v81
	v_permlane32_swap_b32_e32 v110, v90
	v_permlane32_swap_b32_e32 v111, v91
	v_permlane32_swap_b32_e32 v106, v82
	v_permlane32_swap_b32_e32 v107, v83
	s_mov_b32 s4, 0xc2000000
	v_pk_mul_f32 v[0:1], v[184:185], v[100:101]
	s_nop 0
	v_pk_mul_f32 v[32:33], v[0:1], s[2:3] op_sel_hi:[1,0]
	v_pk_mul_f32 v[8:9], v[192:193], v[96:97]
	v_exp_f32_e32 v32, v32
	v_pk_mul_f32 v[36:37], v[8:9], s[2:3] op_sel_hi:[1,0]
	v_exp_f32_e32 v33, v33
	v_exp_f32_e32 v36, v36
	v_exp_f32_e32 v37, v37
	v_pk_mul_f32 v[18:19], v[202:203], v[94:95]
	v_pk_add_f32 v[32:33], v[32:33], 1.0 op_sel_hi:[1,0]
	v_pk_mul_f32 v[2:3], v[186:187], v[102:103]
	v_pk_add_f32 v[36:37], v[36:37], 1.0 op_sel_hi:[1,0]
	v_pk_mul_f32 v[10:11], v[194:195], v[98:99]
	v_pk_mul_f32 v[42:43], v[18:19], s[2:3] op_sel_hi:[1,0]
	v_rcp_f32_e32 v32, v32
	v_rcp_f32_e32 v33, v33
	v_rcp_f32_e32 v36, v36
	v_rcp_f32_e32 v37, v37
	v_pk_mul_f32 v[16:17], v[200:201], v[92:93]
	v_pk_mul_f32 v[34:35], v[2:3], s[2:3] op_sel_hi:[1,0]
	v_pk_mul_f32 v[38:39], v[10:11], s[2:3] op_sel_hi:[1,0]
	v_exp_f32_e32 v42, v42
	v_exp_f32_e32 v43, v43
	v_pk_mul_f32 v[40:41], v[16:17], s[2:3] op_sel_hi:[1,0]
	v_exp_f32_e32 v34, v34
	v_exp_f32_e32 v35, v35
	v_exp_f32_e32 v38, v38
	v_exp_f32_e32 v39, v39
	v_exp_f32_e32 v40, v40
	v_exp_f32_e32 v41, v41
	v_pk_mul_f32 v[4:5], v[188:189], v[108:109]
	v_pk_mul_f32 v[12:13], v[196:197], v[104:105]
	v_pk_mul_f32 v[0:1], v[0:1], v[32:33]
	v_pk_mul_f32 v[8:9], v[8:9], v[36:37]
	v_pk_mul_f32 v[0:1], v[4:5], v[0:1]
	v_pk_mul_f32 v[4:5], v[12:13], v[8:9]
	v_pk_add_f32 v[8:9], v[42:43], 1.0 op_sel_hi:[1,0]
	v_pk_add_f32 v[34:35], v[34:35], 1.0 op_sel_hi:[1,0]
	v_pk_add_f32 v[38:39], v[38:39], 1.0 op_sel_hi:[1,0]
	v_rcp_f32_e32 v8, v8
	v_rcp_f32_e32 v9, v9
	v_pk_add_f32 v[40:41], v[40:41], 1.0 op_sel_hi:[1,0]
	v_rcp_f32_e32 v34, v34
	v_rcp_f32_e32 v35, v35
	v_rcp_f32_e32 v38, v38
	v_rcp_f32_e32 v39, v39
	v_rcp_f32_e32 v40, v40
	v_rcp_f32_e32 v41, v41
	v_pk_mul_f32 v[12:13], v[206:207], v[90:91]
	v_pk_mul_f32 v[8:9], v[18:19], v[8:9]
	v_pk_mul_f32 v[6:7], v[190:191], v[110:111]
	v_pk_mul_f32 v[14:15], v[198:199], v[106:107]
	v_pk_mul_f32 v[2:3], v[2:3], v[34:35]
	v_pk_mul_f32 v[10:11], v[10:11], v[38:39]
	v_pk_mul_f32 v[8:9], v[12:13], v[8:9]
	v_pk_mul_f32 v[12:13], v[208:209], v[84:85]
	v_pk_mul_f32 v[20:21], v[204:205], v[88:89]
	v_pk_mul_f32 v[2:3], v[6:7], v[2:3]
	v_pk_mul_f32 v[6:7], v[14:15], v[10:11]
	v_pk_mul_f32 v[10:11], v[16:17], v[40:41]
	v_pk_mul_f32 v[16:17], v[12:13], s[2:3] op_sel_hi:[1,0]
	v_pk_mul_f32 v[18:19], v[210:211], v[86:87]
	v_pk_mul_f32 v[10:11], v[20:21], v[10:11]
	v_exp_f32_e32 v16, v16
	v_exp_f32_e32 v17, v17
	v_pk_mul_f32 v[20:21], v[18:19], s[2:3] op_sel_hi:[1,0]
	v_pk_mul_f32 v[14:15], v[212:213], v[80:81]
	v_exp_f32_e32 v20, v20
	v_exp_f32_e32 v21, v21
	v_pk_add_f32 v[16:17], v[16:17], 1.0 op_sel_hi:[1,0]
	s_mov_b32 s3, 0x700000
	v_rcp_f32_e32 v16, v16
	v_rcp_f32_e32 v17, v17
	v_pk_add_f32 v[20:21], v[20:21], 1.0 op_sel_hi:[1,0]
	v_mov_b32_e32 v81, 0
	v_rcp_f32_e32 v20, v20
	v_rcp_f32_e32 v21, v21
	v_pk_mul_f32 v[12:13], v[12:13], v[16:17]
	v_pk_mul_f32 v[16:17], v[18:19], v[20:21]
	v_pk_mul_f32 v[12:13], v[14:15], v[12:13]
	v_pk_mul_f32 v[14:15], v[214:215], v[82:83]
	v_pk_mul_f32 v[14:15], v[14:15], v[16:17]
	v_max3_f32 v16, |v6|, |v7|, |v0|
	v_max3_f32 v16, v16, |v1|, |v2|
	v_max3_f32 v16, v16, |v3|, |v4|
	v_max3_f32 v16, v16, |v5|, |v10|
	v_max3_f32 v16, v16, |v11|, |v8|
	v_max3_f32 v16, v16, |v9|, |v12|
	v_max3_f32 v16, v16, |v13|, |v14|
	v_max_f32_e64 v16, v16, |v15|
	v_mov_b32_e32 v17, v16
	s_nop 1
	v_permlane16_swap_b32_e32 v16, v17
	v_max_f32_e32 v16, v16, v17
	v_lshrrev_b32_e32 v17, 23, v16
	v_and_b32_e32 v16, 0x7fffff, v16
	v_mov_b32_e32 v82, 0xffffff7f
	v_cmp_lt_u32_e32 vcc, s3, v16
	v_mov_b32_e32 v83, 0x64
	s_nop 0
	v_addc_co_u32_e32 v16, vcc, v17, v82, vcc
	v_med3_i32 v84, v16, s5, v83
	v_lshlrev_b32_e32 v16, 23, v84
	v_sub_u32_e32 v16, 1.0, v16
	v_pk_mul_f32 v[40:41], v[16:17], v[10:11] op_sel_hi:[0,1]
	v_pk_mul_f32 v[42:43], v[16:17], v[8:9] op_sel_hi:[0,1]
	v_pk_mul_f32 v[44:45], v[16:17], v[12:13] op_sel_hi:[0,1]
	v_pk_mul_f32 v[46:47], v[16:17], v[14:15] op_sel_hi:[0,1]
	v_pk_mul_f32 v[32:33], v[16:17], v[0:1] op_sel_hi:[0,1]
	v_pk_mul_f32 v[34:35], v[16:17], v[2:3] op_sel_hi:[0,1]
	v_pk_mul_f32 v[36:37], v[16:17], v[4:5] op_sel_hi:[0,1]
	v_pk_mul_f32 v[38:39], v[16:17], v[6:7] op_sel_hi:[0,1]
	v_cvt_scalef32_2xpk16_fp6_f32 v[86:91], v[32:47], v[40:55], 1.0
	v_cvt_scalef32_pk32_f32_fp6 v[0:31], v[86:91], s8
	v_fma_f32 v16, v32, s4, v0
	v_fma_f32 v17, v33, s4, v2
	v_fma_f32 v18, v34, s4, v4
	v_fma_f32 v19, v35, s4, v6
	v_fma_f32 v20, v36, s4, v8
	v_fma_f32 v21, v37, s4, v10
	v_fma_f32 v22, v38, s4, v12
	v_fma_f32 v23, v39, s4, v14
	v_fma_f32 v24, v40, s4, v1
	v_fma_f32 v25, v41, s4, v3
	v_fma_f32 v26, v42, s4, v5
	v_fma_f32 v27, v43, s4, v7
	v_fma_f32 v28, v44, s4, v9
	v_fma_f32 v29, v45, s4, v11
	v_fma_f32 v30, v46, s4, v13
	v_fma_f32 v31, v47, s4, v15
	v_cvt_scalef32_2xpk16_fp6_f32 v[0:5], v[16:31], v[24:39], 1.0
	v_xor_b32_e32 v4, 0x20820820, v0
	v_or_b32_e32 v0, 32, v163
	v_xor_b32_e32 v5, 0x8208208, v1
	v_or_b32_e32 v1, v0, v162
	v_mul_u32_u24_e32 v80, 24, v1
	v_xor_b32_e32 v6, 0x82082082, v2
	v_lshl_add_u64 v[2:3], v[148:149], 0, v[80:81]
	v_lshl_add_u64 v[2:3], v[2:3], 0, v[144:145]
	global_store_dwordx3 v[2:3], v[86:88], off nt
	v_add_co_u32_e32 v2, vcc, 0x1000, v2
	s_nop 1
	v_addc_co_u32_e32 v3, vcc, 0, v3, vcc
	global_store_dwordx3 v[2:3], v[4:6], off offset:2048 nt
	s_and_saveexec_b64 s[6:7], s[0:1]
	s_cbranch_execz .LBB2_12
	v_mov_b32_e32 v2, 0x7a00
	v_add_u32_e32 v1, 0x7f, v84
	v_lshl_add_u32 v2, v84, 8, v2
	v_lshl_or_b32 v80, v0, 1, v162
	v_or_b32_e32 v2, v2, v1
	v_lshl_add_u64 v[0:1], v[146:147], 0, v[80:81]
	global_store_short v[0:1], v2, off
.LBB2_12:
	s_or_b64 exec, exec, s[6:7]
	v_permlane32_swap_b32_e32 v68, v60
	v_permlane32_swap_b32_e32 v69, v61
	v_permlane32_swap_b32_e32 v64, v52
	v_permlane32_swap_b32_e32 v65, v53
	v_permlane32_swap_b32_e32 v70, v62
	v_permlane32_swap_b32_e32 v71, v63
	v_permlane32_swap_b32_e32 v66, v54
	v_permlane32_swap_b32_e32 v67, v55
	v_permlane32_swap_b32_e32 v76, v56
	v_permlane32_swap_b32_e32 v77, v57
	v_permlane32_swap_b32_e32 v72, v48
	v_permlane32_swap_b32_e32 v73, v49
	v_permlane32_swap_b32_e32 v78, v58
	v_permlane32_swap_b32_e32 v79, v59
	v_permlane32_swap_b32_e32 v74, v50
	v_permlane32_swap_b32_e32 v75, v51
	v_pk_mul_f32 v[0:1], v[184:185], v[68:69]
	s_nop 0
	v_pk_mul_f32 v[32:33], v[0:1], s[2:3] op_sel_hi:[1,0]
	v_pk_mul_f32 v[8:9], v[192:193], v[64:65]
	v_exp_f32_e32 v32, v32
	v_pk_mul_f32 v[36:37], v[8:9], s[2:3] op_sel_hi:[1,0]
	v_exp_f32_e32 v33, v33
	v_exp_f32_e32 v36, v36
	v_exp_f32_e32 v37, v37
	v_pk_mul_f32 v[18:19], v[202:203], v[62:63]
	v_pk_mul_f32 v[2:3], v[186:187], v[70:71]
	v_pk_mul_f32 v[10:11], v[194:195], v[66:67]
	v_pk_mul_f32 v[42:43], v[18:19], s[2:3] op_sel_hi:[1,0]
	v_pk_add_f32 v[32:33], v[32:33], 1.0 op_sel_hi:[1,0]
	v_pk_add_f32 v[36:37], v[36:37], 1.0 op_sel_hi:[1,0]
	v_pk_mul_f32 v[16:17], v[200:201], v[60:61]
	v_pk_mul_f32 v[34:35], v[2:3], s[2:3] op_sel_hi:[1,0]
	v_pk_mul_f32 v[38:39], v[10:11], s[2:3] op_sel_hi:[1,0]
	v_exp_f32_e32 v42, v42
	v_exp_f32_e32 v43, v43
	v_rcp_f32_e32 v32, v32
	v_rcp_f32_e32 v33, v33
	v_rcp_f32_e32 v36, v36
	v_rcp_f32_e32 v37, v37
	v_pk_mul_f32 v[40:41], v[16:17], s[2:3] op_sel_hi:[1,0]
	v_exp_f32_e32 v34, v34
	v_exp_f32_e32 v35, v35
	v_exp_f32_e32 v38, v38
	v_exp_f32_e32 v39, v39
	v_exp_f32_e32 v40, v40
	v_exp_f32_e32 v41, v41
	v_pk_mul_f32 v[4:5], v[188:189], v[76:77]
	v_pk_mul_f32 v[12:13], v[196:197], v[72:73]
	v_pk_add_f32 v[42:43], v[42:43], 1.0 op_sel_hi:[1,0]
	v_pk_mul_f32 v[0:1], v[0:1], v[32:33]
	v_pk_mul_f32 v[8:9], v[8:9], v[36:37]
	v_pk_add_f32 v[34:35], v[34:35], 1.0 op_sel_hi:[1,0]
	v_pk_add_f32 v[38:39], v[38:39], 1.0 op_sel_hi:[1,0]
	v_pk_mul_f32 v[0:1], v[4:5], v[0:1]
	v_pk_mul_f32 v[4:5], v[12:13], v[8:9]
	v_rcp_f32_e32 v8, v42
	v_rcp_f32_e32 v9, v43
	v_pk_add_f32 v[40:41], v[40:41], 1.0 op_sel_hi:[1,0]
	v_rcp_f32_e32 v34, v34
	v_rcp_f32_e32 v35, v35
	v_rcp_f32_e32 v38, v38
	v_rcp_f32_e32 v39, v39
	v_rcp_f32_e32 v40, v40
	v_rcp_f32_e32 v41, v41
	v_pk_mul_f32 v[12:13], v[206:207], v[58:59]
	v_pk_mul_f32 v[8:9], v[18:19], v[8:9]
	v_pk_mul_f32 v[6:7], v[190:191], v[78:79]
	v_pk_mul_f32 v[14:15], v[198:199], v[74:75]
	v_pk_mul_f32 v[2:3], v[2:3], v[34:35]
	v_pk_mul_f32 v[10:11], v[10:11], v[38:39]
	v_pk_mul_f32 v[8:9], v[12:13], v[8:9]
	v_pk_mul_f32 v[12:13], v[208:209], v[52:53]
	v_pk_mul_f32 v[20:21], v[204:205], v[56:57]
	v_pk_mul_f32 v[2:3], v[6:7], v[2:3]
	v_pk_mul_f32 v[6:7], v[14:15], v[10:11]
	v_pk_mul_f32 v[10:11], v[16:17], v[40:41]
	v_pk_mul_f32 v[16:17], v[12:13], s[2:3] op_sel_hi:[1,0]
	v_pk_mul_f32 v[18:19], v[210:211], v[54:55]
	v_pk_mul_f32 v[10:11], v[20:21], v[10:11]
	v_exp_f32_e32 v16, v16
	v_exp_f32_e32 v17, v17
	v_pk_mul_f32 v[20:21], v[18:19], s[2:3] op_sel_hi:[1,0]
	v_pk_mul_f32 v[14:15], v[212:213], v[48:49]
	v_exp_f32_e32 v20, v20
	v_exp_f32_e32 v21, v21
	v_pk_add_f32 v[16:17], v[16:17], 1.0 op_sel_hi:[1,0]
	v_pk_add_f32 v[20:21], v[20:21], 1.0 op_sel_hi:[1,0]
	v_rcp_f32_e32 v16, v16
	v_rcp_f32_e32 v17, v17
	v_rcp_f32_e32 v20, v20
	v_rcp_f32_e32 v21, v21
	v_pk_mul_f32 v[12:13], v[12:13], v[16:17]
	s_nop 0
	v_pk_mul_f32 v[12:13], v[14:15], v[12:13]
	v_pk_mul_f32 v[14:15], v[214:215], v[50:51]
	v_pk_mul_f32 v[16:17], v[18:19], v[20:21]
	v_pk_mul_f32 v[14:15], v[14:15], v[16:17]
	v_max3_f32 v16, |v6|, |v7|, |v0|
	v_max3_f32 v16, v16, |v1|, |v2|
	v_max3_f32 v16, v16, |v3|, |v4|
	v_max3_f32 v16, v16, |v5|, |v10|
	v_max3_f32 v16, v16, |v11|, |v8|
	v_max3_f32 v16, v16, |v9|, |v12|
	v_max3_f32 v16, v16, |v13|, |v14|
	v_max_f32_e64 v16, v16, |v15|
	v_mov_b32_e32 v17, v16
	s_nop 1
	v_permlane16_swap_b32_e32 v16, v17
	v_max_f32_e32 v16, v16, v17
	v_lshrrev_b32_e32 v17, 23, v16
	v_and_b32_e32 v16, 0x7fffff, v16
	v_cmp_lt_u32_e32 vcc, s3, v16
	s_nop 1
	v_addc_co_u32_e32 v16, vcc, v17, v82, vcc
	v_med3_i32 v48, v16, s5, v83
	v_lshlrev_b32_e32 v16, 23, v48
	v_sub_u32_e32 v16, 1.0, v16
	v_pk_mul_f32 v[40:41], v[16:17], v[10:11] op_sel_hi:[0,1]
	v_pk_mul_f32 v[42:43], v[16:17], v[8:9] op_sel_hi:[0,1]
	v_pk_mul_f32 v[44:45], v[16:17], v[12:13] op_sel_hi:[0,1]
	v_pk_mul_f32 v[46:47], v[16:17], v[14:15] op_sel_hi:[0,1]
	v_pk_mul_f32 v[32:33], v[16:17], v[0:1] op_sel_hi:[0,1]
	v_pk_mul_f32 v[34:35], v[16:17], v[2:3] op_sel_hi:[0,1]
	v_pk_mul_f32 v[36:37], v[16:17], v[4:5] op_sel_hi:[0,1]
	v_pk_mul_f32 v[38:39], v[16:17], v[6:7] op_sel_hi:[0,1]
	v_cvt_scalef32_2xpk16_fp6_f32 v[50:55], v[32:47], v[40:55], 1.0
	v_cvt_scalef32_pk32_f32_fp6 v[0:31], v[50:55], s8
	v_fma_f32 v16, v32, s4, v0
	v_fma_f32 v17, v33, s4, v2
	v_fma_f32 v18, v34, s4, v4
	v_fma_f32 v19, v35, s4, v6
	v_fma_f32 v20, v36, s4, v8
	v_fma_f32 v21, v37, s4, v10
	v_fma_f32 v22, v38, s4, v12
	v_fma_f32 v23, v39, s4, v14
	v_fma_f32 v24, v40, s4, v1
	v_fma_f32 v25, v41, s4, v3
	v_fma_f32 v26, v42, s4, v5
	v_fma_f32 v27, v43, s4, v7
	v_fma_f32 v28, v44, s4, v9
	v_fma_f32 v29, v45, s4, v11
	v_fma_f32 v30, v46, s4, v13
	v_fma_f32 v31, v47, s4, v15
	v_cvt_scalef32_2xpk16_fp6_f32 v[0:5], v[16:31], v[24:39], 1.0
	v_xor_b32_e32 v4, 0x20820820, v0
	v_or_b32_e32 v0, 48, v163
	v_xor_b32_e32 v5, 0x8208208, v1
	v_or_b32_e32 v1, v0, v162
	v_mul_u32_u24_e32 v80, 24, v1
	v_xor_b32_e32 v6, 0x82082082, v2
	v_lshl_add_u64 v[2:3], v[148:149], 0, v[80:81]
	v_lshl_add_u64 v[2:3], v[2:3], 0, v[144:145]
	global_store_dwordx3 v[2:3], v[50:52], off nt
	v_add_co_u32_e32 v2, vcc, 0x1000, v2
	s_nop 1
	v_addc_co_u32_e32 v3, vcc, 0, v3, vcc
	global_store_dwordx3 v[2:3], v[4:6], off offset:2048 nt
	s_and_saveexec_b64 s[2:3], s[0:1]
	s_cbranch_execz .LBB2_14
	v_mov_b32_e32 v2, 0x7a00
	v_add_u32_e32 v1, 0x7f, v48
	v_lshl_add_u32 v2, v48, 8, v2
	v_or_b32_e32 v2, v2, v1
	v_lshl_or_b32 v0, v0, 1, v162
	v_mov_b32_e32 v1, 0
	v_lshl_add_u64 v[0:1], v[146:147], 0, v[0:1]
	global_store_short v[0:1], v2, off

.LBB3_3:
	ds_read_b128 v[202:205], v175
	ds_read_b128 v[206:209], v175 offset:256
	ds_read_b128 v[210:213], v175 offset:512
	ds_read_b128 v[214:217], v175 offset:768
	ds_read_b128 v[218:221], v175 offset:1024
	ds_read_b128 v[222:225], v175 offset:1280
	ds_read_b128 v[226:229], v175 offset:1536
	ds_read_b128 v[230:233], v175 offset:1792
	ds_read2_b64 v[178:181], v171 offset1:1
	ds_read2_b64 v[182:185], v171 offset0:2 offset1:48
	ds_read2_b64 v[186:189], v171 offset0:49 offset1:50
	s_mov_b32 m0, s57
	ds_read2_b64 v[190:193], v171 offset0:96 offset1:97
	global_load_lds_dwordx4 v144, s[76:77]
	s_mov_b32 m0, s56
	ds_read2_b64 v[194:197], v171 offset0:98 offset1:144
	global_load_lds_dwordx4 v145, s[76:77]
	s_mov_b32 m0, s55
	ds_read2_b64 v[198:201], v171 offset0:145 offset1:146
	global_load_lds_dwordx4 v146, s[76:77]
	v_add_u32_e32 v152, s42, v176
	ds_read_u16 v240, v152
	ds_read_u16 v241, v152 offset:32
	ds_read_u16 v242, v152 offset:64
	s_add_i32 s42, s60, 0xfffff800
	s_and_b32 s42, s42, 0x1800
	s_add_i32 m0, s48, s42
	ds_read_u16 v243, v152 offset:96
	global_load_lds_dword v150, s[80:81]
	s_waitcnt vmcnt(6)
	s_waitcnt lgkmcnt(0)
	s_barrier
	v_mfma_scale_f32_16x16x128_f8f6f4 v[126:129], v[202:205], v[178:183], v[126:129], v177, v240 op_sel_hi:[0,0,0] cbsz:4 blgp:2
	v_mfma_scale_f32_16x16x128_f8f6f4 v[122:125], v[206:209], v[178:183], v[122:125], v177, v240 op_sel_hi:[0,0,0] cbsz:4 blgp:2
	v_mfma_scale_f32_16x16x128_f8f6f4 v[114:117], v[210:213], v[178:183], v[114:117], v177, v240 op_sel_hi:[0,0,0] cbsz:4 blgp:2
	v_mfma_scale_f32_16x16x128_f8f6f4 v[102:105], v[214:217], v[178:183], v[102:105], v177, v240 op_sel_hi:[0,0,0] cbsz:4 blgp:2
	v_mfma_scale_f32_16x16x128_f8f6f4 v[86:89], v[218:221], v[178:183], v[86:89], v177, v240 op_sel_hi:[0,0,0] cbsz:4 blgp:2
	v_mfma_scale_f32_16x16x128_f8f6f4 v[70:73], v[222:225], v[178:183], v[70:73], v177, v240 op_sel_hi:[0,0,0] cbsz:4 blgp:2
	v_mfma_scale_f32_16x16x128_f8f6f4 v[54:57], v[226:229], v[178:183], v[54:57], v177, v240 op_sel_hi:[0,0,0] cbsz:4 blgp:2
	v_mfma_scale_f32_16x16x128_f8f6f4 v[38:41], v[230:233], v[178:183], v[38:41], v177, v240 op_sel_hi:[0,0,0] cbsz:4 blgp:2
	v_mfma_scale_f32_16x16x128_f8f6f4 v[118:121], v[202:205], v[184:189], v[118:121], v177, v241 op_sel_hi:[0,0,0] cbsz:4 blgp:2
	v_mfma_scale_f32_16x16x128_f8f6f4 v[110:113], v[206:209], v[184:189], v[110:113], v177, v241 op_sel_hi:[0,0,0] cbsz:4 blgp:2
	v_mfma_scale_f32_16x16x128_f8f6f4 v[98:101], v[210:213], v[184:189], v[98:101], v177, v241 op_sel_hi:[0,0,0] cbsz:4 blgp:2
	v_mfma_scale_f32_16x16x128_f8f6f4 v[82:85], v[214:217], v[184:189], v[82:85], v177, v241 op_sel_hi:[0,0,0] cbsz:4 blgp:2
	v_mfma_scale_f32_16x16x128_f8f6f4 v[66:69], v[218:221], v[184:189], v[66:69], v177, v241 op_sel_hi:[0,0,0] cbsz:4 blgp:2
	v_mfma_scale_f32_16x16x128_f8f6f4 v[50:53], v[222:225], v[184:189], v[50:53], v177, v241 op_sel_hi:[0,0,0] cbsz:4 blgp:2
	v_mfma_scale_f32_16x16x128_f8f6f4 v[34:37], v[226:229], v[184:189], v[34:37], v177, v241 op_sel_hi:[0,0,0] cbsz:4 blgp:2
	v_mfma_scale_f32_16x16x128_f8f6f4 v[106:109], v[202:205], v[190:195], v[106:109], v177, v242 op_sel_hi:[0,0,0] cbsz:4 blgp:2
	v_mfma_scale_f32_16x16x128_f8f6f4 v[94:97], v[206:209], v[190:195], v[94:97], v177, v242 op_sel_hi:[0,0,0] cbsz:4 blgp:2
	v_mfma_scale_f32_16x16x128_f8f6f4 v[78:81], v[210:213], v[190:195], v[78:81], v177, v242 op_sel_hi:[0,0,0] cbsz:4 blgp:2
	v_mfma_scale_f32_16x16x128_f8f6f4 v[62:65], v[214:217], v[190:195], v[62:65], v177, v242 op_sel_hi:[0,0,0] cbsz:4 blgp:2
	v_mfma_scale_f32_16x16x128_f8f6f4 v[46:49], v[218:221], v[190:195], v[46:49], v177, v242 op_sel_hi:[0,0,0] cbsz:4 blgp:2
	v_mfma_scale_f32_16x16x128_f8f6f4 v[30:33], v[222:225], v[190:195], v[30:33], v177, v242 op_sel_hi:[0,0,0] cbsz:4 blgp:2
	v_mfma_scale_f32_16x16x128_f8f6f4 v[90:93], v[202:205], v[196:201], v[90:93], v177, v243 op_sel_hi:[0,0,0] cbsz:4 blgp:2
	v_mfma_scale_f32_16x16x128_f8f6f4 v[74:77], v[206:209], v[196:201], v[74:77], v177, v243 op_sel_hi:[0,0,0] cbsz:4 blgp:2
	v_mfma_scale_f32_16x16x128_f8f6f4 v[58:61], v[210:213], v[196:201], v[58:61], v177, v243 op_sel_hi:[0,0,0] cbsz:4 blgp:2
	v_mfma_scale_f32_16x16x128_f8f6f4 v[42:45], v[214:217], v[196:201], v[42:45], v177, v243 op_sel_hi:[0,0,0] cbsz:4 blgp:2
	v_mfma_scale_f32_16x16x128_f8f6f4 v[26:29], v[218:221], v[196:201], v[26:29], v177, v243 op_sel_hi:[0,0,0] cbsz:4 blgp:2
	v_mfma_scale_f32_16x16x128_f8f6f4 v[178:181], v[230:233], v[184:189], v[22:25], v177, v241 op_sel_hi:[0,0,0] cbsz:4 blgp:2
	v_mfma_scale_f32_16x16x128_f8f6f4 v[182:185], v[226:229], v[190:195], v[18:21], v177, v242 op_sel_hi:[0,0,0] cbsz:4 blgp:2
	v_mfma_scale_f32_16x16x128_f8f6f4 v[186:189], v[230:233], v[190:195], v[10:13], v177, v242 op_sel_hi:[0,0,0] cbsz:4 blgp:2
	v_mfma_scale_f32_16x16x128_f8f6f4 v[190:193], v[222:225], v[196:201], v[14:17], v177, v243 op_sel_hi:[0,0,0] cbsz:4 blgp:2
	v_mfma_scale_f32_16x16x128_f8f6f4 v[234:237], v[226:229], v[196:201], v[6:9], v177, v243 op_sel_hi:[0,0,0] cbsz:4 blgp:2
	v_mfma_scale_f32_16x16x128_f8f6f4 v[194:197], v[230:233], v[196:201], v[2:5], v177, v243 op_sel_hi:[0,0,0] cbsz:4 blgp:2
	s_barrier
	ds_read2_b64 v[2:5], v167 offset1:1
	s_mov_b32 m0, s52
	ds_read2_b64 v[6:9], v167 offset0:2 offset1:48
	global_load_lds_dwordx4 v147, s[76:77]
	s_mov_b32 m0, s50
	ds_read2_b64 v[10:13], v167 offset0:49 offset1:50
	global_load_lds_dwordx4 v148, s[76:77]
	s_mov_b32 m0, s49
	ds_read2_b64 v[14:17], v167 offset0:96 offset1:97
	global_load_lds_dwordx4 v149, s[76:77]
	s_mov_b32 m0, s13
	ds_read2_b64 v[18:21], v167 offset0:98 offset1:144
	global_load_lds_dwordx4 v142, s[72:73]
	s_mov_b32 m0, s44
	ds_read2_b64 v[22:25], v167 offset0:145 offset1:146
	global_load_lds_dwordx4 v143, s[72:73]
	s_waitcnt vmcnt(5)
	s_waitcnt lgkmcnt(0)
	s_barrier
	v_mfma_scale_f32_16x16x128_f8f6f4 v[126:129], v[202:205], v[2:7], v[126:129], v177, v240 op_sel:[0,1,0] op_sel_hi:[0,0,0] cbsz:4 blgp:2
	v_mfma_scale_f32_16x16x128_f8f6f4 v[122:125], v[206:209], v[2:7], v[122:125], v177, v240 op_sel:[0,1,0] op_sel_hi:[0,0,0] cbsz:4 blgp:2
	v_mfma_scale_f32_16x16x128_f8f6f4 v[114:117], v[210:213], v[2:7], v[114:117], v177, v240 op_sel:[0,1,0] op_sel_hi:[0,0,0] cbsz:4 blgp:2
	v_mfma_scale_f32_16x16x128_f8f6f4 v[102:105], v[214:217], v[2:7], v[102:105], v177, v240 op_sel:[0,1,0] op_sel_hi:[0,0,0] cbsz:4 blgp:2
	v_mfma_scale_f32_16x16x128_f8f6f4 v[86:89], v[218:221], v[2:7], v[86:89], v177, v240 op_sel:[0,1,0] op_sel_hi:[0,0,0] cbsz:4 blgp:2
	v_mfma_scale_f32_16x16x128_f8f6f4 v[70:73], v[222:225], v[2:7], v[70:73], v177, v240 op_sel:[0,1,0] op_sel_hi:[0,0,0] cbsz:4 blgp:2
	v_mfma_scale_f32_16x16x128_f8f6f4 v[54:57], v[226:229], v[2:7], v[54:57], v177, v240 op_sel:[0,1,0] op_sel_hi:[0,0,0] cbsz:4 blgp:2
	v_mfma_scale_f32_16x16x128_f8f6f4 v[38:41], v[230:233], v[2:7], v[38:41], v177, v240 op_sel:[0,1,0] op_sel_hi:[0,0,0] cbsz:4 blgp:2
	v_mfma_scale_f32_16x16x128_f8f6f4 v[118:121], v[202:205], v[8:13], v[118:121], v177, v241 op_sel:[0,1,0] op_sel_hi:[0,0,0] cbsz:4 blgp:2
	v_mfma_scale_f32_16x16x128_f8f6f4 v[110:113], v[206:209], v[8:13], v[110:113], v177, v241 op_sel:[0,1,0] op_sel_hi:[0,0,0] cbsz:4 blgp:2
	v_mfma_scale_f32_16x16x128_f8f6f4 v[98:101], v[210:213], v[8:13], v[98:101], v177, v241 op_sel:[0,1,0] op_sel_hi:[0,0,0] cbsz:4 blgp:2
	v_mfma_scale_f32_16x16x128_f8f6f4 v[82:85], v[214:217], v[8:13], v[82:85], v177, v241 op_sel:[0,1,0] op_sel_hi:[0,0,0] cbsz:4 blgp:2
	v_mfma_scale_f32_16x16x128_f8f6f4 v[66:69], v[218:221], v[8:13], v[66:69], v177, v241 op_sel:[0,1,0] op_sel_hi:[0,0,0] cbsz:4 blgp:2
	v_mfma_scale_f32_16x16x128_f8f6f4 v[50:53], v[222:225], v[8:13], v[50:53], v177, v241 op_sel:[0,1,0] op_sel_hi:[0,0,0] cbsz:4 blgp:2
	v_mfma_scale_f32_16x16x128_f8f6f4 v[34:37], v[226:229], v[8:13], v[34:37], v177, v241 op_sel:[0,1,0] op_sel_hi:[0,0,0] cbsz:4 blgp:2
	v_mfma_scale_f32_16x16x128_f8f6f4 v[106:109], v[202:205], v[14:19], v[106:109], v177, v242 op_sel:[0,1,0] op_sel_hi:[0,0,0] cbsz:4 blgp:2
	v_mfma_scale_f32_16x16x128_f8f6f4 v[94:97], v[206:209], v[14:19], v[94:97], v177, v242 op_sel:[0,1,0] op_sel_hi:[0,0,0] cbsz:4 blgp:2
	v_mfma_scale_f32_16x16x128_f8f6f4 v[78:81], v[210:213], v[14:19], v[78:81], v177, v242 op_sel:[0,1,0] op_sel_hi:[0,0,0] cbsz:4 blgp:2
	v_mfma_scale_f32_16x16x128_f8f6f4 v[62:65], v[214:217], v[14:19], v[62:65], v177, v242 op_sel:[0,1,0] op_sel_hi:[0,0,0] cbsz:4 blgp:2
	v_mfma_scale_f32_16x16x128_f8f6f4 v[46:49], v[218:221], v[14:19], v[46:49], v177, v242 op_sel:[0,1,0] op_sel_hi:[0,0,0] cbsz:4 blgp:2
	v_mfma_scale_f32_16x16x128_f8f6f4 v[30:33], v[222:225], v[14:19], v[30:33], v177, v242 op_sel:[0,1,0] op_sel_hi:[0,0,0] cbsz:4 blgp:2
	v_mfma_scale_f32_16x16x128_f8f6f4 v[90:93], v[202:205], v[20:25], v[90:93], v177, v243 op_sel:[0,1,0] op_sel_hi:[0,0,0] cbsz:4 blgp:2
	v_mfma_scale_f32_16x16x128_f8f6f4 v[74:77], v[206:209], v[20:25], v[74:77], v177, v243 op_sel:[0,1,0] op_sel_hi:[0,0,0] cbsz:4 blgp:2
	v_mfma_scale_f32_16x16x128_f8f6f4 v[58:61], v[210:213], v[20:25], v[58:61], v177, v243 op_sel:[0,1,0] op_sel_hi:[0,0,0] cbsz:4 blgp:2
	v_mfma_scale_f32_16x16x128_f8f6f4 v[42:45], v[214:217], v[20:25], v[42:45], v177, v243 op_sel:[0,1,0] op_sel_hi:[0,0,0] cbsz:4 blgp:2
	v_mfma_scale_f32_16x16x128_f8f6f4 v[26:29], v[218:221], v[20:25], v[26:29], v177, v243 op_sel:[0,1,0] op_sel_hi:[0,0,0] cbsz:4 blgp:2
	v_mfma_scale_f32_16x16x128_f8f6f4 v[178:181], v[230:233], v[8:13], v[178:181], v177, v241 op_sel:[0,1,0] op_sel_hi:[0,0,0] cbsz:4 blgp:2
	v_mfma_scale_f32_16x16x128_f8f6f4 v[182:185], v[226:229], v[14:19], v[182:185], v177, v242 op_sel:[0,1,0] op_sel_hi:[0,0,0] cbsz:4 blgp:2
	v_mfma_scale_f32_16x16x128_f8f6f4 v[186:189], v[230:233], v[14:19], v[186:189], v177, v242 op_sel:[0,1,0] op_sel_hi:[0,0,0] cbsz:4 blgp:2
	v_mfma_scale_f32_16x16x128_f8f6f4 v[190:193], v[222:225], v[20:25], v[190:193], v177, v243 op_sel:[0,1,0] op_sel_hi:[0,0,0] cbsz:4 blgp:2
	v_mfma_scale_f32_16x16x128_f8f6f4 v[198:201], v[226:229], v[20:25], v[234:237], v177, v243 op_sel:[0,1,0] op_sel_hi:[0,0,0] cbsz:4 blgp:2
	v_mfma_scale_f32_16x16x128_f8f6f4 v[194:197], v[230:233], v[20:25], v[194:197], v177, v243 op_sel:[0,1,0] op_sel_hi:[0,0,0] cbsz:4 blgp:2
	s_barrier
	ds_read_b128 v[202:205], v166
	ds_read_b128 v[206:209], v166 offset:256
	ds_read_b128 v[210:213], v166 offset:512
	ds_read_b128 v[214:217], v166 offset:768
	ds_read_b128 v[218:221], v166 offset:1024
	ds_read_b128 v[222:225], v166 offset:1280
	ds_read_b128 v[226:229], v166 offset:1536
	ds_read_b128 v[230:233], v166 offset:1792
	ds_read2_b64 v[2:5], v162 offset1:1
	ds_read2_b64 v[6:9], v162 offset0:2 offset1:48
	ds_read2_b64 v[10:13], v162 offset0:49 offset1:50
	s_mov_b32 m0, s45
	ds_read2_b64 v[14:17], v162 offset0:96 offset1:97
	global_load_lds_dwordx4 v144, s[78:79]
	s_mov_b32 m0, s46
	ds_read2_b64 v[18:21], v162 offset0:98 offset1:144
	global_load_lds_dwordx4 v145, s[78:79]
	s_mov_b32 m0, s47
	ds_read2_b64 v[22:25], v162 offset0:145 offset1:146
	global_load_lds_dwordx4 v146, s[78:79]
	v_add_u32_e32 v234, s42, v176
	ds_read_u16 v242, v234
	ds_read_u16 v243, v234 offset:32
	ds_read_u16 v244, v234 offset:64
	s_and_b32 s42, s60, 0x1000
	s_add_i32 m0, s48, s42
	ds_read_u16 v245, v234 offset:96
	global_load_lds_dword v151, s[80:81]
	s_waitcnt vmcnt(6)
	s_waitcnt lgkmcnt(0)
	s_barrier
	v_mfma_scale_f32_16x16x128_f8f6f4 v[126:129], v[202:205], v[2:7], v[126:129], v177, v242 op_sel_hi:[0,0,0] cbsz:4 blgp:2
	v_mfma_scale_f32_16x16x128_f8f6f4 v[122:125], v[206:209], v[2:7], v[122:125], v177, v242 op_sel_hi:[0,0,0] cbsz:4 blgp:2
	v_mfma_scale_f32_16x16x128_f8f6f4 v[114:117], v[210:213], v[2:7], v[114:117], v177, v242 op_sel_hi:[0,0,0] cbsz:4 blgp:2
	v_mfma_scale_f32_16x16x128_f8f6f4 v[102:105], v[214:217], v[2:7], v[102:105], v177, v242 op_sel_hi:[0,0,0] cbsz:4 blgp:2
	v_mfma_scale_f32_16x16x128_f8f6f4 v[86:89], v[218:221], v[2:7], v[86:89], v177, v242 op_sel_hi:[0,0,0] cbsz:4 blgp:2
	v_mfma_scale_f32_16x16x128_f8f6f4 v[70:73], v[222:225], v[2:7], v[70:73], v177, v242 op_sel_hi:[0,0,0] cbsz:4 blgp:2
	v_mfma_scale_f32_16x16x128_f8f6f4 v[54:57], v[226:229], v[2:7], v[54:57], v177, v242 op_sel_hi:[0,0,0] cbsz:4 blgp:2
	v_mfma_scale_f32_16x16x128_f8f6f4 v[38:41], v[230:233], v[2:7], v[38:41], v177, v242 op_sel_hi:[0,0,0] cbsz:4 blgp:2
	v_mfma_scale_f32_16x16x128_f8f6f4 v[118:121], v[202:205], v[8:13], v[118:121], v177, v243 op_sel_hi:[0,0,0] cbsz:4 blgp:2
	v_mfma_scale_f32_16x16x128_f8f6f4 v[110:113], v[206:209], v[8:13], v[110:113], v177, v243 op_sel_hi:[0,0,0] cbsz:4 blgp:2
	v_mfma_scale_f32_16x16x128_f8f6f4 v[98:101], v[210:213], v[8:13], v[98:101], v177, v243 op_sel_hi:[0,0,0] cbsz:4 blgp:2
	v_mfma_scale_f32_16x16x128_f8f6f4 v[82:85], v[214:217], v[8:13], v[82:85], v177, v243 op_sel_hi:[0,0,0] cbsz:4 blgp:2
	v_mfma_scale_f32_16x16x128_f8f6f4 v[66:69], v[218:221], v[8:13], v[66:69], v177, v243 op_sel_hi:[0,0,0] cbsz:4 blgp:2
	v_mfma_scale_f32_16x16x128_f8f6f4 v[50:53], v[222:225], v[8:13], v[50:53], v177, v243 op_sel_hi:[0,0,0] cbsz:4 blgp:2
	v_mfma_scale_f32_16x16x128_f8f6f4 v[34:37], v[226:229], v[8:13], v[34:37], v177, v243 op_sel_hi:[0,0,0] cbsz:4 blgp:2
	v_mfma_scale_f32_16x16x128_f8f6f4 v[106:109], v[202:205], v[14:19], v[106:109], v177, v244 op_sel_hi:[0,0,0] cbsz:4 blgp:2
	v_mfma_scale_f32_16x16x128_f8f6f4 v[94:97], v[206:209], v[14:19], v[94:97], v177, v244 op_sel_hi:[0,0,0] cbsz:4 blgp:2
	v_mfma_scale_f32_16x16x128_f8f6f4 v[78:81], v[210:213], v[14:19], v[78:81], v177, v244 op_sel_hi:[0,0,0] cbsz:4 blgp:2
	v_mfma_scale_f32_16x16x128_f8f6f4 v[62:65], v[214:217], v[14:19], v[62:65], v177, v244 op_sel_hi:[0,0,0] cbsz:4 blgp:2
	v_mfma_scale_f32_16x16x128_f8f6f4 v[46:49], v[218:221], v[14:19], v[46:49], v177, v244 op_sel_hi:[0,0,0] cbsz:4 blgp:2
	v_mfma_scale_f32_16x16x128_f8f6f4 v[30:33], v[222:225], v[14:19], v[30:33], v177, v244 op_sel_hi:[0,0,0] cbsz:4 blgp:2
	v_mfma_scale_f32_16x16x128_f8f6f4 v[238:241], v[226:229], v[14:19], v[182:185], v177, v244 op_sel_hi:[0,0,0] cbsz:4 blgp:2
	v_mfma_scale_f32_16x16x128_f8f6f4 v[14:17], v[230:233], v[14:19], v[186:189], v177, v244 op_sel_hi:[0,0,0] cbsz:4 blgp:2
	v_mfma_scale_f32_16x16x128_f8f6f4 v[90:93], v[202:205], v[20:25], v[90:93], v177, v245 op_sel_hi:[0,0,0] cbsz:4 blgp:2
	v_mfma_scale_f32_16x16x128_f8f6f4 v[74:77], v[206:209], v[20:25], v[74:77], v177, v245 op_sel_hi:[0,0,0] cbsz:4 blgp:2
	v_mfma_scale_f32_16x16x128_f8f6f4 v[58:61], v[210:213], v[20:25], v[58:61], v177, v245 op_sel_hi:[0,0,0] cbsz:4 blgp:2
	v_mfma_scale_f32_16x16x128_f8f6f4 v[42:45], v[214:217], v[20:25], v[42:45], v177, v245 op_sel_hi:[0,0,0] cbsz:4 blgp:2
	v_mfma_scale_f32_16x16x128_f8f6f4 v[26:29], v[218:221], v[20:25], v[26:29], v177, v245 op_sel_hi:[0,0,0] cbsz:4 blgp:2
	v_mfma_scale_f32_16x16x128_f8f6f4 v[234:237], v[230:233], v[8:13], v[178:181], v177, v243 op_sel_hi:[0,0,0] cbsz:4 blgp:2
	v_mfma_scale_f32_16x16x128_f8f6f4 v[190:193], v[222:225], v[20:25], v[190:193], v177, v245 op_sel_hi:[0,0,0] cbsz:4 blgp:2
	v_mfma_scale_f32_16x16x128_f8f6f4 v[198:201], v[226:229], v[20:25], v[198:201], v177, v245 op_sel_hi:[0,0,0] cbsz:4 blgp:2
	v_mfma_scale_f32_16x16x128_f8f6f4 v[194:197], v[230:233], v[20:25], v[194:197], v177, v245 op_sel_hi:[0,0,0] cbsz:4 blgp:2
	s_barrier
	ds_read2_b64 v[2:5], v1 offset1:1
	s_mov_b32 m0, s51
	ds_read2_b64 v[6:9], v1 offset0:2 offset1:48
	global_load_lds_dwordx4 v147, s[78:79]
	s_mov_b32 m0, s53
	ds_read2_b64 v[10:13], v1 offset0:49 offset1:50
	global_load_lds_dwordx4 v148, s[78:79]
	s_mov_b32 m0, s54
	ds_read2_b64 v[178:181], v159 offset1:1
	global_load_lds_dwordx4 v149, s[78:79]
	s_mov_b32 m0, s61
	ds_read2_b64 v[182:185], v159 offset0:2 offset1:48
	global_load_lds_dwordx4 v142, s[74:75]
	s_mov_b32 m0, s58
	ds_read2_b64 v[186:189], v159 offset0:49 offset1:50
	global_load_lds_dwordx4 v143, s[74:75]
	s_waitcnt vmcnt(5)
	s_waitcnt lgkmcnt(0)
	s_barrier
	v_mfma_scale_f32_16x16x128_f8f6f4 v[126:129], v[202:205], v[2:7], v[126:129], v177, v242 op_sel:[0,1,0] op_sel_hi:[0,0,0] cbsz:4 blgp:2
	v_mfma_scale_f32_16x16x128_f8f6f4 v[122:125], v[206:209], v[2:7], v[122:125], v177, v242 op_sel:[0,1,0] op_sel_hi:[0,0,0] cbsz:4 blgp:2
	v_mfma_scale_f32_16x16x128_f8f6f4 v[114:117], v[210:213], v[2:7], v[114:117], v177, v242 op_sel:[0,1,0] op_sel_hi:[0,0,0] cbsz:4 blgp:2
	v_mfma_scale_f32_16x16x128_f8f6f4 v[102:105], v[214:217], v[2:7], v[102:105], v177, v242 op_sel:[0,1,0] op_sel_hi:[0,0,0] cbsz:4 blgp:2
	v_mfma_scale_f32_16x16x128_f8f6f4 v[86:89], v[218:221], v[2:7], v[86:89], v177, v242 op_sel:[0,1,0] op_sel_hi:[0,0,0] cbsz:4 blgp:2
	v_mfma_scale_f32_16x16x128_f8f6f4 v[70:73], v[222:225], v[2:7], v[70:73], v177, v242 op_sel:[0,1,0] op_sel_hi:[0,0,0] cbsz:4 blgp:2
	v_mfma_scale_f32_16x16x128_f8f6f4 v[54:57], v[226:229], v[2:7], v[54:57], v177, v242 op_sel:[0,1,0] op_sel_hi:[0,0,0] cbsz:4 blgp:2
	v_mfma_scale_f32_16x16x128_f8f6f4 v[38:41], v[230:233], v[2:7], v[38:41], v177, v242 op_sel:[0,1,0] op_sel_hi:[0,0,0] cbsz:4 blgp:2
	v_mfma_scale_f32_16x16x128_f8f6f4 v[118:121], v[202:205], v[8:13], v[118:121], v177, v243 op_sel:[0,1,0] op_sel_hi:[0,0,0] cbsz:4 blgp:2
	v_mfma_scale_f32_16x16x128_f8f6f4 v[110:113], v[206:209], v[8:13], v[110:113], v177, v243 op_sel:[0,1,0] op_sel_hi:[0,0,0] cbsz:4 blgp:2
	v_mfma_scale_f32_16x16x128_f8f6f4 v[98:101], v[210:213], v[8:13], v[98:101], v177, v243 op_sel:[0,1,0] op_sel_hi:[0,0,0] cbsz:4 blgp:2
	v_mfma_scale_f32_16x16x128_f8f6f4 v[82:85], v[214:217], v[8:13], v[82:85], v177, v243 op_sel:[0,1,0] op_sel_hi:[0,0,0] cbsz:4 blgp:2
	v_mfma_scale_f32_16x16x128_f8f6f4 v[66:69], v[218:221], v[8:13], v[66:69], v177, v243 op_sel:[0,1,0] op_sel_hi:[0,0,0] cbsz:4 blgp:2
	v_mfma_scale_f32_16x16x128_f8f6f4 v[50:53], v[222:225], v[8:13], v[50:53], v177, v243 op_sel:[0,1,0] op_sel_hi:[0,0,0] cbsz:4 blgp:2
	v_mfma_scale_f32_16x16x128_f8f6f4 v[34:37], v[226:229], v[8:13], v[34:37], v177, v243 op_sel:[0,1,0] op_sel_hi:[0,0,0] cbsz:4 blgp:2
	v_mfma_scale_f32_16x16x128_f8f6f4 v[22:25], v[230:233], v[8:13], v[234:237], v177, v243 op_sel:[0,1,0] op_sel_hi:[0,0,0] cbsz:4 blgp:2
	v_mfma_scale_f32_16x16x128_f8f6f4 v[106:109], v[202:205], v[178:183], v[106:109], v177, v244 op_sel:[0,1,0] op_sel_hi:[0,0,0] cbsz:4 blgp:2
	v_mfma_scale_f32_16x16x128_f8f6f4 v[94:97], v[206:209], v[178:183], v[94:97], v177, v244 op_sel:[0,1,0] op_sel_hi:[0,0,0] cbsz:4 blgp:2
	v_mfma_scale_f32_16x16x128_f8f6f4 v[78:81], v[210:213], v[178:183], v[78:81], v177, v244 op_sel:[0,1,0] op_sel_hi:[0,0,0] cbsz:4 blgp:2
	v_mfma_scale_f32_16x16x128_f8f6f4 v[62:65], v[214:217], v[178:183], v[62:65], v177, v244 op_sel:[0,1,0] op_sel_hi:[0,0,0] cbsz:4 blgp:2
	v_mfma_scale_f32_16x16x128_f8f6f4 v[46:49], v[218:221], v[178:183], v[46:49], v177, v244 op_sel:[0,1,0] op_sel_hi:[0,0,0] cbsz:4 blgp:2
	v_mfma_scale_f32_16x16x128_f8f6f4 v[30:33], v[222:225], v[178:183], v[30:33], v177, v244 op_sel:[0,1,0] op_sel_hi:[0,0,0] cbsz:4 blgp:2
	v_mfma_scale_f32_16x16x128_f8f6f4 v[18:21], v[226:229], v[178:183], v[238:241], v177, v244 op_sel:[0,1,0] op_sel_hi:[0,0,0] cbsz:4 blgp:2
	v_mfma_scale_f32_16x16x128_f8f6f4 v[10:13], v[230:233], v[178:183], v[14:17], v177, v244 op_sel:[0,1,0] op_sel_hi:[0,0,0] cbsz:4 blgp:2
	v_mfma_scale_f32_16x16x128_f8f6f4 v[90:93], v[202:205], v[184:189], v[90:93], v177, v245 op_sel:[0,1,0] op_sel_hi:[0,0,0] cbsz:4 blgp:2
	v_mfma_scale_f32_16x16x128_f8f6f4 v[74:77], v[206:209], v[184:189], v[74:77], v177, v245 op_sel:[0,1,0] op_sel_hi:[0,0,0] cbsz:4 blgp:2
	v_mfma_scale_f32_16x16x128_f8f6f4 v[58:61], v[210:213], v[184:189], v[58:61], v177, v245 op_sel:[0,1,0] op_sel_hi:[0,0,0] cbsz:4 blgp:2
	v_mfma_scale_f32_16x16x128_f8f6f4 v[42:45], v[214:217], v[184:189], v[42:45], v177, v245 op_sel:[0,1,0] op_sel_hi:[0,0,0] cbsz:4 blgp:2
	v_mfma_scale_f32_16x16x128_f8f6f4 v[26:29], v[218:221], v[184:189], v[26:29], v177, v245 op_sel:[0,1,0] op_sel_hi:[0,0,0] cbsz:4 blgp:2
	v_mfma_scale_f32_16x16x128_f8f6f4 v[14:17], v[222:225], v[184:189], v[190:193], v177, v245 op_sel:[0,1,0] op_sel_hi:[0,0,0] cbsz:4 blgp:2
	v_mfma_scale_f32_16x16x128_f8f6f4 v[6:9], v[226:229], v[184:189], v[198:201], v177, v245 op_sel:[0,1,0] op_sel_hi:[0,0,0] cbsz:4 blgp:2
	v_mfma_scale_f32_16x16x128_f8f6f4 v[2:5], v[230:233], v[184:189], v[194:197], v177, v245 op_sel:[0,1,0] op_sel_hi:[0,0,0] cbsz:4 blgp:2
	s_add_i32 s59, s59, 2
	s_addk_i32 s60, 0x1000
	s_add_u32 s72, s72, 0x8000
	s_addc_u32 s73, s73, 0
	s_add_u32 s74, s74, 0x8000
	s_addc_u32 s75, s75, 0
	s_add_u32 s76, s76, 0x18000
	s_addc_u32 s77, s77, 0
	s_add_u32 s78, s78, 0x18000
	s_addc_u32 s79, s79, 0
	s_add_u32 s80, s80, 0x1000
	s_addc_u32 s81, s81, 0
	s_add_i32 s42, s60, 0xfffff000
	s_and_b32 s42, s42, 0x1000
	s_cmp_lt_u32 s59, 28
	s_barrier
	s_cbranch_scc1 .LBB3_3
	ds_read_b128 v[154:157], v175
	ds_read_b128 v[186:189], v175 offset:256
	ds_read_b128 v[190:193], v175 offset:512
	ds_read_b128 v[194:197], v175 offset:768
	ds_read_b128 v[198:201], v175 offset:1024
	ds_read_b128 v[202:205], v175 offset:1280
	ds_read_b128 v[206:209], v175 offset:1536
	ds_read_b128 v[210:213], v175 offset:1792
	ds_read_b64 v[142:143], v171
	ds_read_b64 v[144:145], v171 offset:8
	ds_read_b64 v[146:147], v171 offset:16
	ds_read_b64 v[148:149], v174
	ds_read_b64 v[150:151], v174 offset:8
	ds_read_b64 v[152:153], v174 offset:16
	ds_read_b64 v[174:175], v173
	ds_read_b64 v[176:177], v173 offset:8
	ds_read_b64 v[178:179], v173 offset:16
	ds_read_b64 v[180:181], v172
	ds_read_b64 v[182:183], v172 offset:8
	ds_read_b64 v[184:185], v172 offset:16
	v_add_u32_e32 v171, 0x21000, v248
	v_add_u32_e32 v172, 0x21020, v248
	v_add_u32_e32 v173, 0x21040, v248
	v_add_u32_e32 v214, 0x21060, v248
	s_mov_b64 s[0:1], 0x7c000
	s_mov_b32 m0, s61
	ds_read_u16 v171, v171
	ds_read_u16 v215, v172
	ds_read_u16 v216, v173
	ds_read_u16 v214, v214
	v_lshl_add_u64 v[172:173], v[138:139], 0, s[0:1]
	s_mov_b64 s[0:1], 0x7e000
	v_lshl_add_u64 v[138:139], v[138:139], 0, s[0:1]
	s_mov_b32 m0, s58
	s_mov_b64 s[0:1], 0x174000
	v_lshl_add_u64 v[138:139], v[140:141], 0, s[0:1]
	v_lshl_add_u64 v[140:141], v[138:139], 0, s[16:17]
	s_mov_b32 m0, s57
	v_lshl_add_u64 v[130:131], s[14:15], 0, v[130:131]
	global_load_lds_dwordx4 v[140:141], off
	v_lshl_add_u64 v[140:141], v[138:139], 0, s[18:19]
	s_mov_b32 m0, s56
	v_lshl_add_u64 v[138:139], v[138:139], 0, s[20:21]
	global_load_lds_dwordx4 v[140:141], off
	s_mov_b32 m0, s55
	s_mov_b64 s[0:1], 0xf800
	global_load_lds_dwordx4 v[138:139], off
	v_lshl_add_u64 v[130:131], v[130:131], 0, s[0:1]
	s_add_i32 m0, s9, 0x21800
	s_waitcnt lgkmcnt(0)
	v_mov_b32_e32 v172, v216
	global_load_lds_dword v[130:131], off
	s_waitcnt vmcnt(6)
	s_waitcnt lgkmcnt(0)
	v_mov_b32_e32 v130, v171
	v_mov_b32_e32 v131, v215
	v_mov_b32_e32 v217, v214
	s_barrier
	v_mov_b32_e32 v161, 0x7f7f7f7f
	s_nop 1
	v_mfma_scale_f32_16x16x128_f8f6f4 v[126:129], v[154:157], v[142:147], v[126:129], v161, v130 op_sel_hi:[0,0,0] cbsz:4 blgp:2
	v_mfma_scale_f32_16x16x128_f8f6f4 v[122:125], v[186:189], v[142:147], v[122:125], v161, v130 op_sel_hi:[0,0,0] cbsz:4 blgp:2
	v_mfma_scale_f32_16x16x128_f8f6f4 v[114:117], v[190:193], v[142:147], v[114:117], v161, v130 op_sel_hi:[0,0,0] cbsz:4 blgp:2
	v_mfma_scale_f32_16x16x128_f8f6f4 v[102:105], v[194:197], v[142:147], v[102:105], v161, v130 op_sel_hi:[0,0,0] cbsz:4 blgp:2
	v_mfma_scale_f32_16x16x128_f8f6f4 v[86:89], v[198:201], v[142:147], v[86:89], v161, v130 op_sel_hi:[0,0,0] cbsz:4 blgp:2
	v_mfma_scale_f32_16x16x128_f8f6f4 v[70:73], v[202:205], v[142:147], v[70:73], v161, v130 op_sel_hi:[0,0,0] cbsz:4 blgp:2
	v_mfma_scale_f32_16x16x128_f8f6f4 v[54:57], v[206:209], v[142:147], v[54:57], v161, v130 op_sel_hi:[0,0,0] cbsz:4 blgp:2
	v_mfma_scale_f32_16x16x128_f8f6f4 v[38:41], v[210:213], v[142:147], v[38:41], v161, v130 op_sel_hi:[0,0,0] cbsz:4 blgp:2
	v_mfma_scale_f32_16x16x128_f8f6f4 v[118:121], v[154:157], v[148:153], v[118:121], v161, v131 op_sel_hi:[0,0,0] cbsz:4 blgp:2
	v_mfma_scale_f32_16x16x128_f8f6f4 v[110:113], v[186:189], v[148:153], v[110:113], v161, v131 op_sel_hi:[0,0,0] cbsz:4 blgp:2
	v_mfma_scale_f32_16x16x128_f8f6f4 v[98:101], v[190:193], v[148:153], v[98:101], v161, v131 op_sel_hi:[0,0,0] cbsz:4 blgp:2
	v_mfma_scale_f32_16x16x128_f8f6f4 v[82:85], v[194:197], v[148:153], v[82:85], v161, v131 op_sel_hi:[0,0,0] cbsz:4 blgp:2
	v_mfma_scale_f32_16x16x128_f8f6f4 v[66:69], v[198:201], v[148:153], v[66:69], v161, v131 op_sel_hi:[0,0,0] cbsz:4 blgp:2
	v_mfma_scale_f32_16x16x128_f8f6f4 v[50:53], v[202:205], v[148:153], v[50:53], v161, v131 op_sel_hi:[0,0,0] cbsz:4 blgp:2
	v_mfma_scale_f32_16x16x128_f8f6f4 v[34:37], v[206:209], v[148:153], v[34:37], v161, v131 op_sel_hi:[0,0,0] cbsz:4 blgp:2
	v_mfma_scale_f32_16x16x128_f8f6f4 v[138:141], v[210:213], v[148:153], v[22:25], v161, v131 op_sel_hi:[0,0,0] cbsz:4 blgp:2
	v_mfma_scale_f32_16x16x128_f8f6f4 v[106:109], v[154:157], v[174:179], v[106:109], v161, v172 op_sel_hi:[0,0,0] cbsz:4 blgp:2
	v_mfma_scale_f32_16x16x128_f8f6f4 v[94:97], v[186:189], v[174:179], v[94:97], v161, v172 op_sel_hi:[0,0,0] cbsz:4 blgp:2
	v_mfma_scale_f32_16x16x128_f8f6f4 v[78:81], v[190:193], v[174:179], v[78:81], v161, v172 op_sel_hi:[0,0,0] cbsz:4 blgp:2
	v_mfma_scale_f32_16x16x128_f8f6f4 v[62:65], v[194:197], v[174:179], v[62:65], v161, v172 op_sel_hi:[0,0,0] cbsz:4 blgp:2
	v_mfma_scale_f32_16x16x128_f8f6f4 v[46:49], v[198:201], v[174:179], v[46:49], v161, v172 op_sel_hi:[0,0,0] cbsz:4 blgp:2
	v_mfma_scale_f32_16x16x128_f8f6f4 v[142:145], v[206:209], v[174:179], v[18:21], v161, v172 op_sel_hi:[0,0,0] cbsz:4 blgp:2
	v_mfma_scale_f32_16x16x128_f8f6f4 v[146:149], v[210:213], v[174:179], v[10:13], v161, v172 op_sel_hi:[0,0,0] cbsz:4 blgp:2
	v_mfma_scale_f32_16x16x128_f8f6f4 v[90:93], v[154:157], v[180:185], v[90:93], v161, v217 op_sel_hi:[0,0,0] cbsz:4 blgp:2
	v_mfma_scale_f32_16x16x128_f8f6f4 v[74:77], v[186:189], v[180:185], v[74:77], v161, v217 op_sel_hi:[0,0,0] cbsz:4 blgp:2
	v_mfma_scale_f32_16x16x128_f8f6f4 v[58:61], v[190:193], v[180:185], v[58:61], v161, v217 op_sel_hi:[0,0,0] cbsz:4 blgp:2
	v_mfma_scale_f32_16x16x128_f8f6f4 v[150:153], v[202:205], v[180:185], v[14:17], v161, v217 op_sel_hi:[0,0,0] cbsz:4 blgp:2
	v_mfma_scale_f32_16x16x128_f8f6f4 v[30:33], v[202:205], v[174:179], v[30:33], v161, v172 op_sel_hi:[0,0,0] cbsz:4 blgp:2
	v_mfma_scale_f32_16x16x128_f8f6f4 v[42:45], v[194:197], v[180:185], v[42:45], v161, v217 op_sel_hi:[0,0,0] cbsz:4 blgp:2
	v_mfma_scale_f32_16x16x128_f8f6f4 v[26:29], v[198:201], v[180:185], v[26:29], v161, v217 op_sel_hi:[0,0,0] cbsz:4 blgp:2
	v_mfma_scale_f32_16x16x128_f8f6f4 v[172:175], v[206:209], v[180:185], v[6:9], v161, v217 op_sel_hi:[0,0,0] cbsz:4 blgp:2
	v_mfma_scale_f32_16x16x128_f8f6f4 v[176:179], v[210:213], v[180:185], v[2:5], v161, v217 op_sel_hi:[0,0,0] cbsz:4 blgp:2
	s_barrier
	ds_read_b64 v[2:3], v167
	ds_read_b64 v[4:5], v167 offset:8
	ds_read_b64 v[6:7], v167 offset:16
	ds_read_b64 v[8:9], v170
	ds_read_b64 v[10:11], v170 offset:8
	ds_read_b64 v[12:13], v170 offset:16
	ds_read_b64 v[14:15], v169
	ds_read_b64 v[16:17], v169 offset:8
	ds_read_b64 v[18:19], v169 offset:16
	s_mov_b64 s[0:1], 0x175800
	s_mov_b32 m0, s52
	ds_read_b64 v[20:21], v168
	ds_read_b64 v[22:23], v168 offset:8
	ds_read_b64 v[24:25], v168 offset:16
	v_lshl_add_u64 v[130:131], v[132:133], 0, s[0:1]
	global_load_lds_dwordx4 v[130:131], off
	v_lshl_add_u64 v[130:131], v[134:135], 0, s[0:1]
	s_mov_b32 m0, s50
	v_lshrrev_b32_e32 v167, 8, v216
	global_load_lds_dwordx4 v[130:131], off
	v_lshl_add_u64 v[130:131], v[136:137], 0, s[0:1]
	s_mov_b32 m0, s49
	v_lshrrev_b32_e32 v168, 8, v214
	global_load_lds_dwordx4 v[130:131], off
	s_waitcnt vmcnt(3)
	s_waitcnt lgkmcnt(0)
	v_lshrrev_b32_e32 v130, 8, v171
	v_lshrrev_b32_e32 v131, 8, v215
	s_barrier
	v_mfma_scale_f32_16x16x128_f8f6f4 v[126:129], v[154:157], v[2:7], v[126:129], v161, v130 op_sel_hi:[0,0,0] cbsz:4 blgp:2
	v_mfma_scale_f32_16x16x128_f8f6f4 v[122:125], v[186:189], v[2:7], v[122:125], v161, v130 op_sel_hi:[0,0,0] cbsz:4 blgp:2
	v_mfma_scale_f32_16x16x128_f8f6f4 v[114:117], v[190:193], v[2:7], v[114:117], v161, v130 op_sel_hi:[0,0,0] cbsz:4 blgp:2
	v_mfma_scale_f32_16x16x128_f8f6f4 v[102:105], v[194:197], v[2:7], v[102:105], v161, v130 op_sel_hi:[0,0,0] cbsz:4 blgp:2
	v_mfma_scale_f32_16x16x128_f8f6f4 v[86:89], v[198:201], v[2:7], v[86:89], v161, v130 op_sel_hi:[0,0,0] cbsz:4 blgp:2
	v_mfma_scale_f32_16x16x128_f8f6f4 v[70:73], v[202:205], v[2:7], v[70:73], v161, v130 op_sel_hi:[0,0,0] cbsz:4 blgp:2
	v_mfma_scale_f32_16x16x128_f8f6f4 v[54:57], v[206:209], v[2:7], v[54:57], v161, v130 op_sel_hi:[0,0,0] cbsz:4 blgp:2
	v_mfma_scale_f32_16x16x128_f8f6f4 v[38:41], v[210:213], v[2:7], v[38:41], v161, v130 op_sel_hi:[0,0,0] cbsz:4 blgp:2
	v_mfma_scale_f32_16x16x128_f8f6f4 v[118:121], v[154:157], v[8:13], v[118:121], v161, v131 op_sel_hi:[0,0,0] cbsz:4 blgp:2
	v_mfma_scale_f32_16x16x128_f8f6f4 v[110:113], v[186:189], v[8:13], v[110:113], v161, v131 op_sel_hi:[0,0,0] cbsz:4 blgp:2
	v_mfma_scale_f32_16x16x128_f8f6f4 v[98:101], v[190:193], v[8:13], v[98:101], v161, v131 op_sel_hi:[0,0,0] cbsz:4 blgp:2
	v_mfma_scale_f32_16x16x128_f8f6f4 v[82:85], v[194:197], v[8:13], v[82:85], v161, v131 op_sel_hi:[0,0,0] cbsz:4 blgp:2
	v_mfma_scale_f32_16x16x128_f8f6f4 v[66:69], v[198:201], v[8:13], v[66:69], v161, v131 op_sel_hi:[0,0,0] cbsz:4 blgp:2
	v_mfma_scale_f32_16x16x128_f8f6f4 v[50:53], v[202:205], v[8:13], v[50:53], v161, v131 op_sel_hi:[0,0,0] cbsz:4 blgp:2
	v_mfma_scale_f32_16x16x128_f8f6f4 v[34:37], v[206:209], v[8:13], v[34:37], v161, v131 op_sel_hi:[0,0,0] cbsz:4 blgp:2
	v_mfma_scale_f32_16x16x128_f8f6f4 v[130:133], v[210:213], v[8:13], v[138:141], v161, v131 op_sel_hi:[0,0,0] cbsz:4 blgp:2
	v_mfma_scale_f32_16x16x128_f8f6f4 v[106:109], v[154:157], v[14:19], v[106:109], v161, v167 op_sel_hi:[0,0,0] cbsz:4 blgp:2
	v_mfma_scale_f32_16x16x128_f8f6f4 v[94:97], v[186:189], v[14:19], v[94:97], v161, v167 op_sel_hi:[0,0,0] cbsz:4 blgp:2
	v_mfma_scale_f32_16x16x128_f8f6f4 v[78:81], v[190:193], v[14:19], v[78:81], v161, v167 op_sel_hi:[0,0,0] cbsz:4 blgp:2
	v_mfma_scale_f32_16x16x128_f8f6f4 v[62:65], v[194:197], v[14:19], v[62:65], v161, v167 op_sel_hi:[0,0,0] cbsz:4 blgp:2
	v_mfma_scale_f32_16x16x128_f8f6f4 v[46:49], v[198:201], v[14:19], v[46:49], v161, v167 op_sel_hi:[0,0,0] cbsz:4 blgp:2
	v_mfma_scale_f32_16x16x128_f8f6f4 v[134:137], v[206:209], v[14:19], v[142:145], v161, v167 op_sel_hi:[0,0,0] cbsz:4 blgp:2
	v_mfma_scale_f32_16x16x128_f8f6f4 v[138:141], v[210:213], v[14:19], v[146:149], v161, v167 op_sel_hi:[0,0,0] cbsz:4 blgp:2
	v_mfma_scale_f32_16x16x128_f8f6f4 v[90:93], v[154:157], v[20:25], v[90:93], v161, v168 op_sel_hi:[0,0,0] cbsz:4 blgp:2
	v_mfma_scale_f32_16x16x128_f8f6f4 v[58:61], v[190:193], v[20:25], v[58:61], v161, v168 op_sel_hi:[0,0,0] cbsz:4 blgp:2
	v_mfma_scale_f32_16x16x128_f8f6f4 v[142:145], v[202:205], v[20:25], v[150:153], v161, v168 op_sel_hi:[0,0,0] cbsz:4 blgp:2
	v_mfma_scale_f32_16x16x128_f8f6f4 v[146:149], v[206:209], v[20:25], v[172:175], v161, v168 op_sel_hi:[0,0,0] cbsz:4 blgp:2
	v_mfma_scale_f32_16x16x128_f8f6f4 v[150:153], v[210:213], v[20:25], v[176:179], v161, v168 op_sel_hi:[0,0,0] cbsz:4 blgp:2
	v_mfma_scale_f32_16x16x128_f8f6f4 v[30:33], v[202:205], v[14:19], v[30:33], v161, v167 op_sel_hi:[0,0,0] cbsz:4 blgp:2
	v_mfma_scale_f32_16x16x128_f8f6f4 v[236:239], v[186:189], v[20:25], v[74:77], v161, v168 op_sel_hi:[0,0,0] cbsz:4 blgp:2
	v_mfma_scale_f32_16x16x128_f8f6f4 v[42:45], v[194:197], v[20:25], v[42:45], v161, v168 op_sel_hi:[0,0,0] cbsz:4 blgp:2
	v_mfma_scale_f32_16x16x128_f8f6f4 v[26:29], v[198:201], v[20:25], v[26:29], v161, v168 op_sel_hi:[0,0,0] cbsz:4 blgp:2
	s_barrier
	ds_read_b128 v[168:171], v166
	ds_read_b128 v[172:175], v166 offset:256
	ds_read_b128 v[176:179], v166 offset:512
	ds_read_b128 v[180:183], v166 offset:768
	ds_read_b128 v[184:187], v166 offset:1024
	ds_read_b128 v[188:191], v166 offset:1280
	ds_read_b128 v[192:195], v166 offset:1536
	ds_read_b128 v[196:199], v166 offset:1792
	ds_read_b64 v[2:3], v162
	ds_read_b64 v[4:5], v162 offset:8
	ds_read_b64 v[6:7], v162 offset:16
	ds_read_b64 v[8:9], v165
	ds_read_b64 v[10:11], v165 offset:8
	ds_read_b64 v[12:13], v165 offset:16
	ds_read_b64 v[14:15], v164
	ds_read_b64 v[16:17], v164 offset:8
	ds_read_b64 v[18:19], v164 offset:16
	ds_read_b64 v[20:21], v163
	ds_read_b64 v[22:23], v163 offset:8
	ds_read_b64 v[24:25], v163 offset:16
	v_add_u32_e32 v154, 0x21800, v248
	v_add_u32_e32 v155, 0x21820, v248
	v_add_u32_e32 v156, 0x21840, v248
	v_add_u32_e32 v157, 0x21860, v248
	ds_read_u16 v166, v154
	ds_read_u16 v167, v155
	ds_read_u16 v74, v156
	ds_read_u16 v75, v157
	s_waitcnt vmcnt(0)
	s_waitcnt lgkmcnt(0)
	s_waitcnt lgkmcnt(0)
	v_mov_b32_e32 v76, v166
	v_mov_b32_e32 v77, v167
	v_mov_b32_e32 v228, v74
	v_mov_b32_e32 v252, v75
	s_barrier
	v_mfma_scale_f32_16x16x128_f8f6f4 v[126:129], v[168:171], v[2:7], v[126:129], v161, v76 op_sel_hi:[0,0,0] cbsz:4 blgp:2
	v_mfma_scale_f32_16x16x128_f8f6f4 v[122:125], v[172:175], v[2:7], v[122:125], v161, v76 op_sel_hi:[0,0,0] cbsz:4 blgp:2
	v_mfma_scale_f32_16x16x128_f8f6f4 v[114:117], v[176:179], v[2:7], v[114:117], v161, v76 op_sel_hi:[0,0,0] cbsz:4 blgp:2
	v_mfma_scale_f32_16x16x128_f8f6f4 v[102:105], v[180:183], v[2:7], v[102:105], v161, v76 op_sel_hi:[0,0,0] cbsz:4 blgp:2
	v_mfma_scale_f32_16x16x128_f8f6f4 v[86:89], v[184:187], v[2:7], v[86:89], v161, v76 op_sel_hi:[0,0,0] cbsz:4 blgp:2
	v_mfma_scale_f32_16x16x128_f8f6f4 v[70:73], v[188:191], v[2:7], v[70:73], v161, v76 op_sel_hi:[0,0,0] cbsz:4 blgp:2
	v_mfma_scale_f32_16x16x128_f8f6f4 v[54:57], v[192:195], v[2:7], v[54:57], v161, v76 op_sel_hi:[0,0,0] cbsz:4 blgp:2
	v_mfma_scale_f32_16x16x128_f8f6f4 v[154:157], v[196:199], v[2:7], v[38:41], v161, v76 op_sel_hi:[0,0,0] cbsz:4 blgp:2
	v_mfma_scale_f32_16x16x128_f8f6f4 v[118:121], v[168:171], v[8:13], v[118:121], v161, v77 op_sel_hi:[0,0,0] cbsz:4 blgp:2
	v_mfma_scale_f32_16x16x128_f8f6f4 v[82:85], v[180:183], v[8:13], v[82:85], v161, v77 op_sel_hi:[0,0,0] cbsz:4 blgp:2
	v_mfma_scale_f32_16x16x128_f8f6f4 v[66:69], v[184:187], v[8:13], v[66:69], v161, v77 op_sel_hi:[0,0,0] cbsz:4 blgp:2
	v_mfma_scale_f32_16x16x128_f8f6f4 v[50:53], v[188:191], v[8:13], v[50:53], v161, v77 op_sel_hi:[0,0,0] cbsz:4 blgp:2
	v_mfma_scale_f32_16x16x128_f8f6f4 v[130:133], v[196:199], v[8:13], v[130:133], v161, v77 op_sel_hi:[0,0,0] cbsz:4 blgp:2
	v_mfma_scale_f32_16x16x128_f8f6f4 v[62:65], v[180:183], v[14:19], v[62:65], v161, v228 op_sel_hi:[0,0,0] cbsz:4 blgp:2
	v_mfma_scale_f32_16x16x128_f8f6f4 v[46:49], v[184:187], v[14:19], v[46:49], v161, v228 op_sel_hi:[0,0,0] cbsz:4 blgp:2
	v_mfma_scale_f32_16x16x128_f8f6f4 v[58:61], v[176:179], v[20:25], v[58:61], v161, v252 op_sel_hi:[0,0,0] cbsz:4 blgp:2
	v_mfma_scale_f32_16x16x128_f8f6f4 v[162:165], v[172:175], v[8:13], v[110:113], v161, v77 op_sel_hi:[0,0,0] cbsz:4 blgp:2
	v_mfma_scale_f32_16x16x128_f8f6f4 v[200:203], v[176:179], v[8:13], v[98:101], v161, v77 op_sel_hi:[0,0,0] cbsz:4 blgp:2
	v_mfma_scale_f32_16x16x128_f8f6f4 v[204:207], v[192:195], v[8:13], v[34:37], v161, v77 op_sel_hi:[0,0,0] cbsz:4 blgp:2
	v_mfma_scale_f32_16x16x128_f8f6f4 v[208:211], v[168:171], v[14:19], v[106:109], v161, v228 op_sel_hi:[0,0,0] cbsz:4 blgp:2
	v_mfma_scale_f32_16x16x128_f8f6f4 v[212:215], v[172:175], v[14:19], v[94:97], v161, v228 op_sel_hi:[0,0,0] cbsz:4 blgp:2
	v_mfma_scale_f32_16x16x128_f8f6f4 v[216:219], v[176:179], v[14:19], v[78:81], v161, v228 op_sel_hi:[0,0,0] cbsz:4 blgp:2
	v_mfma_scale_f32_16x16x128_f8f6f4 v[220:223], v[188:191], v[14:19], v[30:33], v161, v228 op_sel_hi:[0,0,0] cbsz:4 blgp:2
	v_mfma_scale_f32_16x16x128_f8f6f4 v[224:227], v[192:195], v[14:19], v[134:137], v161, v228 op_sel_hi:[0,0,0] cbsz:4 blgp:2
	v_mfma_scale_f32_16x16x128_f8f6f4 v[228:231], v[196:199], v[14:19], v[138:141], v161, v228 op_sel_hi:[0,0,0] cbsz:4 blgp:2
	v_mfma_scale_f32_16x16x128_f8f6f4 v[232:235], v[168:171], v[20:25], v[90:93], v161, v252 op_sel_hi:[0,0,0] cbsz:4 blgp:2
	v_mfma_scale_f32_16x16x128_f8f6f4 v[236:239], v[172:175], v[20:25], v[236:239], v161, v252 op_sel_hi:[0,0,0] cbsz:4 blgp:2
	v_mfma_scale_f32_16x16x128_f8f6f4 v[42:45], v[180:183], v[20:25], v[42:45], v161, v252 op_sel_hi:[0,0,0] cbsz:4 blgp:2
	v_mfma_scale_f32_16x16x128_f8f6f4 v[240:243], v[184:187], v[20:25], v[26:29], v161, v252 op_sel_hi:[0,0,0] cbsz:4 blgp:2
	v_mfma_scale_f32_16x16x128_f8f6f4 v[244:247], v[188:191], v[20:25], v[142:145], v161, v252 op_sel_hi:[0,0,0] cbsz:4 blgp:2
	v_mfma_scale_f32_16x16x128_f8f6f4 v[248:251], v[192:195], v[20:25], v[146:149], v161, v252 op_sel_hi:[0,0,0] cbsz:4 blgp:2
	v_mfma_scale_f32_16x16x128_f8f6f4 v[252:255], v[196:199], v[20:25], v[150:153], v161, v252 op_sel_hi:[0,0,0] cbsz:4 blgp:2
	s_barrier
	ds_read_b64 v[18:19], v1
	ds_read_b64 v[20:21], v1 offset:8
	ds_read_b64 v[22:23], v1 offset:16
	ds_read_b64 v[24:25], v160
	ds_read_b64 v[26:27], v160 offset:8
	ds_read_b64 v[28:29], v160 offset:16
	ds_read_b64 v[30:31], v159
	ds_read_b64 v[32:33], v159 offset:8
	ds_read_b64 v[34:35], v159 offset:16
	ds_read_b64 v[36:37], v158
	ds_read_b64 v[38:39], v158 offset:8
	ds_read_b64 v[40:41], v158 offset:16
	s_waitcnt lgkmcnt(0)
	v_lshrrev_b32_e32 v1, 8, v166
	v_lshrrev_b32_e32 v76, 8, v167
	v_lshrrev_b32_e32 v112, 8, v74
	v_lshrrev_b32_e32 v160, 8, v75
	s_barrier
	v_mfma_scale_f32_16x16x128_f8f6f4 v[14:17], v[168:171], v[18:23], v[126:129], v161, v1 op_sel_hi:[0,0,0] cbsz:4 blgp:2
	v_mfma_scale_f32_16x16x128_f8f6f4 v[10:13], v[172:175], v[18:23], v[122:125], v161, v1 op_sel_hi:[0,0,0] cbsz:4 blgp:2
	v_mfma_scale_f32_16x16x128_f8f6f4 v[6:9], v[176:179], v[18:23], v[114:117], v161, v1 op_sel_hi:[0,0,0] cbsz:4 blgp:2
	v_mfma_scale_f32_16x16x128_f8f6f4 v[2:5], v[180:183], v[18:23], v[102:105], v161, v1 op_sel_hi:[0,0,0] cbsz:4 blgp:2
	v_mfma_scale_f32_16x16x128_f8f6f4 v[108:111], v[184:187], v[18:23], v[86:89], v161, v1 op_sel_hi:[0,0,0] cbsz:4 blgp:2
	v_mfma_scale_f32_16x16x128_f8f6f4 v[104:107], v[188:191], v[18:23], v[70:73], v161, v1 op_sel_hi:[0,0,0] cbsz:4 blgp:2
	v_mfma_scale_f32_16x16x128_f8f6f4 v[100:103], v[192:195], v[18:23], v[54:57], v161, v1 op_sel_hi:[0,0,0] cbsz:4 blgp:2
	v_mfma_scale_f32_16x16x128_f8f6f4 v[96:99], v[196:199], v[18:23], v[154:157], v161, v1 op_sel_hi:[0,0,0] cbsz:4 blgp:2
	v_mfma_scale_f32_16x16x128_f8f6f4 v[156:159], v[168:171], v[24:29], v[118:121], v161, v76 op_sel_hi:[0,0,0] cbsz:4 blgp:2
	v_mfma_scale_f32_16x16x128_f8f6f4 v[152:155], v[172:175], v[24:29], v[162:165], v161, v76 op_sel_hi:[0,0,0] cbsz:4 blgp:2
	v_mfma_scale_f32_16x16x128_f8f6f4 v[148:151], v[176:179], v[24:29], v[200:203], v161, v76 op_sel_hi:[0,0,0] cbsz:4 blgp:2
	v_mfma_scale_f32_16x16x128_f8f6f4 v[144:147], v[180:183], v[24:29], v[82:85], v161, v76 op_sel_hi:[0,0,0] cbsz:4 blgp:2
	v_mfma_scale_f32_16x16x128_f8f6f4 v[92:95], v[184:187], v[24:29], v[66:69], v161, v76 op_sel_hi:[0,0,0] cbsz:4 blgp:2
	v_mfma_scale_f32_16x16x128_f8f6f4 v[88:91], v[188:191], v[24:29], v[50:53], v161, v76 op_sel_hi:[0,0,0] cbsz:4 blgp:2
	v_mfma_scale_f32_16x16x128_f8f6f4 v[84:87], v[192:195], v[24:29], v[204:207], v161, v76 op_sel_hi:[0,0,0] cbsz:4 blgp:2
	v_mfma_scale_f32_16x16x128_f8f6f4 v[80:83], v[196:199], v[24:29], v[130:133], v161, v76 op_sel_hi:[0,0,0] cbsz:4 blgp:2
	v_mfma_scale_f32_16x16x128_f8f6f4 v[140:143], v[168:171], v[30:35], v[208:211], v161, v112 op_sel_hi:[0,0,0] cbsz:4 blgp:2
	v_mfma_scale_f32_16x16x128_f8f6f4 v[136:139], v[172:175], v[30:35], v[212:215], v161, v112 op_sel_hi:[0,0,0] cbsz:4 blgp:2
	v_mfma_scale_f32_16x16x128_f8f6f4 v[132:135], v[176:179], v[30:35], v[216:219], v161, v112 op_sel_hi:[0,0,0] cbsz:4 blgp:2
	v_mfma_scale_f32_16x16x128_f8f6f4 v[128:131], v[180:183], v[30:35], v[62:65], v161, v112 op_sel_hi:[0,0,0] cbsz:4 blgp:2
	v_mfma_scale_f32_16x16x128_f8f6f4 v[76:79], v[184:187], v[30:35], v[46:49], v161, v112 op_sel_hi:[0,0,0] cbsz:4 blgp:2
	v_mfma_scale_f32_16x16x128_f8f6f4 v[72:75], v[188:191], v[30:35], v[220:223], v161, v112 op_sel_hi:[0,0,0] cbsz:4 blgp:2
	v_mfma_scale_f32_16x16x128_f8f6f4 v[68:71], v[192:195], v[30:35], v[224:227], v161, v112 op_sel_hi:[0,0,0] cbsz:4 blgp:2
	v_mfma_scale_f32_16x16x128_f8f6f4 v[64:67], v[196:199], v[30:35], v[228:231], v161, v112 op_sel_hi:[0,0,0] cbsz:4 blgp:2
	v_mfma_scale_f32_16x16x128_f8f6f4 v[124:127], v[168:171], v[36:41], v[232:235], v161, v160 op_sel_hi:[0,0,0] cbsz:4 blgp:2
	v_mfma_scale_f32_16x16x128_f8f6f4 v[120:123], v[172:175], v[36:41], v[236:239], v161, v160 op_sel_hi:[0,0,0] cbsz:4 blgp:2
	v_mfma_scale_f32_16x16x128_f8f6f4 v[116:119], v[176:179], v[36:41], v[58:61], v161, v160 op_sel_hi:[0,0,0] cbsz:4 blgp:2
	v_mfma_scale_f32_16x16x128_f8f6f4 v[112:115], v[180:183], v[36:41], v[42:45], v161, v160 op_sel_hi:[0,0,0] cbsz:4 blgp:2
	v_mfma_scale_f32_16x16x128_f8f6f4 v[60:63], v[184:187], v[36:41], v[240:243], v161, v160 op_sel_hi:[0,0,0] cbsz:4 blgp:2
	v_mfma_scale_f32_16x16x128_f8f6f4 v[56:59], v[188:191], v[36:41], v[244:247], v161, v160 op_sel_hi:[0,0,0] cbsz:4 blgp:2
	v_mfma_scale_f32_16x16x128_f8f6f4 v[52:55], v[192:195], v[36:41], v[248:251], v161, v160 op_sel_hi:[0,0,0] cbsz:4 blgp:2
	v_mfma_scale_f32_16x16x128_f8f6f4 v[48:51], v[196:199], v[36:41], v[252:255], v161, v160 op_sel_hi:[0,0,0] cbsz:4 blgp:2
	v_ashrrev_i32_e32 v166, 6, v0
	v_and_b32_e32 v166, -4, v166
	v_lshl_add_u32 v166, s12, 3, v166
	v_bfe_u32 v167, v0, 5, 1
	v_or_b32_e32 v166, v166, v167
	v_lshlrev_b32_e32 v166, 5, v166
	v_bfe_u32 v167, v0, 4, 1
	v_lshl_or_b32 v166, v167, 2, v166
	v_lshlrev_b32_e32 v166, 2, v166
	global_load_dwordx4 v[192:195], v166, s[10:11]
	global_load_dwordx4 v[196:199], v166, s[10:11] offset:64
	global_load_dwordx4 v[200:203], v166, s[10:11] offset:32
	global_load_dwordx4 v[204:207], v166, s[10:11] offset:96
	global_load_dwordx4 v[208:211], v166, s[10:11] offset:256
	global_load_dwordx4 v[212:215], v166, s[10:11] offset:320
	global_load_dwordx4 v[216:219], v166, s[10:11] offset:288
	global_load_dwordx4 v[220:223], v166, s[10:11] offset:352
	s_barrier
	s_cmpk_gt_u32 s33, 0xff
	s_cbranch_scc1 .LBB3_6
	s_barrier
.LBB3_6:
	s_mov_b32 s0, 0
	s_ashr_i32 s1, s0, 31
	v_add_u32_e32 v26, s0, v0
	v_ashrrev_i32_e32 v0, 6, v26
	v_and_b32_e32 v0, -4, v0
	v_bfe_u32 v177, v26, 5, 1
	v_lshl_add_u32 v178, s12, 3, v0
	v_bfe_u32 v27, v26, 4, 1
	v_or_b32_e32 v0, v178, v177
	s_lshl_b64 s[4:5], s[0:1], 2
	v_lshlrev_b32_e32 v36, 5, v0
	v_lshlrev_b32_e32 v179, 2, v27
	s_add_u32 s4, s10, s4
	v_or_b32_e32 v30, v36, v179
	s_addc_u32 s5, s11, s5
	v_ashrrev_i32_e32 v31, 31, v30
	v_lshl_add_u64 v[170:171], v[30:31], 2, s[4:5]
	v_ashrrev_i32_e32 v31, 31, v36
	v_lshl_add_u64 v[172:173], v[30:31], 2, s[4:5]
	v_and_b32_e32 v181, 0xcf, v26
	v_mul_u32_u24_e32 v160, 12, v27
	v_cmp_eq_u32_e64 s[0:1], 0, v27
	s_lshl_b32 s11, s8, 6
	v_ashrrev_i32_e32 v30, 1, v178
	v_or_b32_e32 v176, 8, v179
	v_add_u32_e32 v34, s11, v30
	s_movk_i32 s9, 0x6000
	v_mov_b64_e32 v[32:33], s[2:3]
	s_add_u32 s6, s2, 0x3000000
	v_ashrrev_i32_e32 v35, 31, v34
	v_or_b32_e32 v30, v36, v176
	s_addc_u32 s7, s3, 0
	v_mad_i64_i32 v[168:169], s[8:9], v34, s9, v[32:33]
	v_lshlrev_b64 v[32:33], 10, v[34:35]
	v_lshl_add_u64 v[174:175], v[30:31], 2, s[4:5]
	v_lshl_add_u64 v[166:167], s[6:7], 0, v[32:33]
	v_permlane32_swap_b32_e32 v14, v6
	v_permlane32_swap_b32_e32 v15, v7
	v_permlane32_swap_b32_e32 v16, v8
	v_permlane32_swap_b32_e32 v17, v9
	v_permlane32_swap_b32_e32 v10, v2
	v_permlane32_swap_b32_e32 v11, v3
	s_mov_b32 s20, 0x3e6d3388
	s_mov_b32 s22, 0xbf3a00e3
	s_mov_b32 s16, 0x3f07dc22
	s_mov_b32 s14, 0xbf38aa3b
	v_mov_b64_e32 v[0:1], s[22:23]
	s_mov_b32 s18, 0x3f35f0e3
	s_mov_b32 s10, 0xbe11a98e
	s_mov_b32 s12, 0x3e027906
	v_permlane32_swap_b32_e32 v12, v4
	v_permlane32_swap_b32_e32 v13, v5
	s_mov_b32 s9, 0x700000
	v_mov_b32_e32 v182, 0xffffff7f
	v_mov_b32_e32 v183, 0x64
	s_mov_b32 s8, 0xc2000000
	v_lshlrev_b32_e32 v180, 9, v177
	v_mov_b32_e32 v161, 0
	v_mov_b32_e32 v165, v161
	v_lshl_or_b32 v162, v181, 1, v180
	s_waitcnt vmcnt(4)
	v_pk_mul_f32 v[14:15], v[192:193], v[14:15]
	s_nop 0
	v_and_b32_e32 v19, 0x7fffffff, v15
	v_and_b32_e32 v18, 0x7fffffff, v14
	v_pk_mul_f32 v[16:17], v[194:195], v[16:17]
	v_pk_mul_f32 v[10:11], v[196:197], v[10:11]
	v_pk_fma_f32 v[22:23], v[18:19], s[20:21], 1.0 op_sel_hi:[1,0,0]
	v_and_b32_e32 v35, 0x7fffffff, v17
	v_and_b32_e32 v34, 0x7fffffff, v16
	v_rcp_f32_e32 v22, v22
	v_rcp_f32_e32 v23, v23
	v_pk_fma_f32 v[38:39], v[34:35], s[20:21], 1.0 op_sel_hi:[1,0,0]
	v_pk_mul_f32 v[20:21], v[14:15], v[14:15]
	v_rcp_f32_e32 v38, v38
	v_rcp_f32_e32 v39, v39
	v_pk_mul_f32 v[20:21], v[20:21], s[14:15] op_sel_hi:[1,0]
	v_pk_fma_f32 v[44:45], v[22:23], s[16:17], v[0:1] op_sel_hi:[1,0,0]
	v_pk_mul_f32 v[36:37], v[16:17], v[16:17]
	v_exp_f32_e32 v20, v20
	v_exp_f32_e32 v21, v21
	v_pk_fma_f32 v[44:45], v[22:23], v[44:45], s[18:19] op_sel_hi:[1,1,0]
	v_pk_mul_f32 v[36:37], v[36:37], s[14:15] op_sel_hi:[1,0]
	v_pk_fma_f32 v[46:47], v[38:39], s[16:17], v[0:1] op_sel_hi:[1,0,0]
	v_pk_fma_f32 v[44:45], v[22:23], v[44:45], s[10:11] op_sel_hi:[1,1,0]
	v_and_b32_e32 v41, 0x7fffffff, v11
	v_and_b32_e32 v40, 0x7fffffff, v10
	v_exp_f32_e32 v36, v36
	v_exp_f32_e32 v37, v37
	v_pk_fma_f32 v[46:47], v[38:39], v[46:47], s[18:19] op_sel_hi:[1,1,0]
	v_pk_fma_f32 v[44:45], v[22:23], v[44:45], s[12:13] op_sel_hi:[1,1,0]
	v_pk_fma_f32 v[42:43], v[40:41], s[20:21], 1.0 op_sel_hi:[1,0,0]
	v_pk_fma_f32 v[46:47], v[38:39], v[46:47], s[10:11] op_sel_hi:[1,1,0]
	v_pk_mul_f32 v[22:23], v[22:23], v[44:45]
	v_rcp_f32_e32 v42, v42
	v_pk_fma_f32 v[46:47], v[38:39], v[46:47], s[12:13] op_sel_hi:[1,1,0]
	v_pk_fma_f32 v[20:21], v[20:21], v[22:23], 0.5 op_sel_hi:[1,1,0] neg_lo:[1,0,0] neg_hi:[1,0,0]
	v_rcp_f32_e32 v43, v43
	v_pk_mul_f32 v[38:39], v[38:39], v[46:47]
	v_pk_mul_f32 v[18:19], v[18:19], v[20:21]
	v_pk_mul_f32 v[20:21], v[10:11], v[10:11]
	v_pk_fma_f32 v[14:15], v[14:15], 0.5, v[18:19] op_sel_hi:[1,0,1]
	v_pk_fma_f32 v[18:19], v[36:37], v[38:39], 0.5 op_sel_hi:[1,1,0] neg_lo:[1,0,0] neg_hi:[1,0,0]
	v_pk_mul_f32 v[20:21], v[20:21], s[14:15] op_sel_hi:[1,0]
	v_pk_mul_f32 v[18:19], v[34:35], v[18:19]
	v_pk_mul_f32 v[12:13], v[198:199], v[12:13]
	v_pk_fma_f32 v[16:17], v[16:17], 0.5, v[18:19] op_sel_hi:[1,0,1]
	v_pk_fma_f32 v[18:19], v[42:43], s[16:17], v[0:1] op_sel_hi:[1,0,0]
	v_exp_f32_e32 v20, v20
	v_pk_fma_f32 v[18:19], v[42:43], v[18:19], s[18:19] op_sel_hi:[1,1,0]
	v_exp_f32_e32 v21, v21
	v_and_b32_e32 v23, 0x7fffffff, v13
	v_and_b32_e32 v22, 0x7fffffff, v12
	v_pk_fma_f32 v[18:19], v[42:43], v[18:19], s[10:11] op_sel_hi:[1,1,0]
	v_pk_fma_f32 v[24:25], v[22:23], s[20:21], 1.0 op_sel_hi:[1,0,0]
	v_pk_fma_f32 v[18:19], v[42:43], v[18:19], s[12:13] op_sel_hi:[1,1,0]
	v_rcp_f32_e32 v24, v24
	v_rcp_f32_e32 v25, v25
	v_pk_mul_f32 v[18:19], v[42:43], v[18:19]
	v_pk_mul_f32 v[6:7], v[200:201], v[6:7]
	v_pk_fma_f32 v[18:19], v[20:21], v[18:19], 0.5 op_sel_hi:[1,1,0] neg_lo:[1,0,0] neg_hi:[1,0,0]
	v_pk_mul_f32 v[20:21], v[12:13], v[12:13]
	v_pk_mul_f32 v[18:19], v[40:41], v[18:19]
	v_pk_mul_f32 v[20:21], v[20:21], s[14:15] op_sel_hi:[1,0]
	v_pk_fma_f32 v[10:11], v[10:11], 0.5, v[18:19] op_sel_hi:[1,0,1]
	v_pk_fma_f32 v[18:19], v[24:25], s[16:17], v[0:1] op_sel_hi:[1,0,0]
	v_exp_f32_e32 v20, v20
	v_pk_fma_f32 v[18:19], v[24:25], v[18:19], s[18:19] op_sel_hi:[1,1,0]
	v_exp_f32_e32 v21, v21
	v_pk_fma_f32 v[18:19], v[24:25], v[18:19], s[10:11] op_sel_hi:[1,1,0]
	v_pk_mul_f32 v[8:9], v[202:203], v[8:9]
	v_pk_fma_f32 v[18:19], v[24:25], v[18:19], s[12:13] op_sel_hi:[1,1,0]
	v_pk_mul_f32 v[2:3], v[204:205], v[2:3]
	v_pk_mul_f32 v[18:19], v[24:25], v[18:19]
	v_and_b32_e32 v25, 0x7fffffff, v7
	v_and_b32_e32 v24, 0x7fffffff, v6
	v_pk_fma_f32 v[26:27], v[24:25], s[20:21], 1.0 op_sel_hi:[1,0,0]
	v_pk_fma_f32 v[18:19], v[20:21], v[18:19], 0.5 op_sel_hi:[1,1,0] neg_lo:[1,0,0] neg_hi:[1,0,0]
	v_rcp_f32_e32 v26, v26
	v_rcp_f32_e32 v27, v27
	v_pk_mul_f32 v[18:19], v[22:23], v[18:19]
	v_pk_mul_f32 v[20:21], v[6:7], v[6:7]
	v_pk_fma_f32 v[12:13], v[12:13], 0.5, v[18:19] op_sel_hi:[1,0,1]
	v_pk_fma_f32 v[18:19], v[26:27], s[16:17], v[0:1] op_sel_hi:[1,0,0]
	v_pk_mul_f32 v[20:21], v[20:21], s[14:15] op_sel_hi:[1,0]
	v_pk_fma_f32 v[18:19], v[26:27], v[18:19], s[18:19] op_sel_hi:[1,1,0]
	v_exp_f32_e32 v20, v20
	v_pk_fma_f32 v[18:19], v[26:27], v[18:19], s[10:11] op_sel_hi:[1,1,0]
	v_exp_f32_e32 v21, v21
	v_pk_fma_f32 v[18:19], v[26:27], v[18:19], s[12:13] op_sel_hi:[1,1,0]
	v_and_b32_e32 v23, 0x7fffffff, v9
	v_and_b32_e32 v22, 0x7fffffff, v8
	v_pk_mul_f32 v[18:19], v[26:27], v[18:19]
	v_pk_fma_f32 v[26:27], v[22:23], s[20:21], 1.0 op_sel_hi:[1,0,0]
	v_pk_fma_f32 v[18:19], v[20:21], v[18:19], 0.5 op_sel_hi:[1,1,0] neg_lo:[1,0,0] neg_hi:[1,0,0]
	v_rcp_f32_e32 v26, v26
	v_rcp_f32_e32 v27, v27
	v_pk_mul_f32 v[18:19], v[24:25], v[18:19]
	v_pk_mul_f32 v[20:21], v[8:9], v[8:9]
	v_pk_fma_f32 v[6:7], v[6:7], 0.5, v[18:19] op_sel_hi:[1,0,1]
	v_pk_fma_f32 v[18:19], v[26:27], s[16:17], v[0:1] op_sel_hi:[1,0,0]
	v_pk_mul_f32 v[20:21], v[20:21], s[14:15] op_sel_hi:[1,0]
	v_pk_fma_f32 v[18:19], v[26:27], v[18:19], s[18:19] op_sel_hi:[1,1,0]
	v_exp_f32_e32 v20, v20
	v_pk_fma_f32 v[18:19], v[26:27], v[18:19], s[10:11] op_sel_hi:[1,1,0]
	v_exp_f32_e32 v21, v21
	v_pk_fma_f32 v[18:19], v[26:27], v[18:19], s[12:13] op_sel_hi:[1,1,0]
	v_and_b32_e32 v25, 0x7fffffff, v3
	v_and_b32_e32 v24, 0x7fffffff, v2
	v_pk_mul_f32 v[18:19], v[26:27], v[18:19]
	v_pk_fma_f32 v[26:27], v[24:25], s[20:21], 1.0 op_sel_hi:[1,0,0]
	v_pk_fma_f32 v[18:19], v[20:21], v[18:19], 0.5 op_sel_hi:[1,1,0] neg_lo:[1,0,0] neg_hi:[1,0,0]
	v_rcp_f32_e32 v26, v26
	v_rcp_f32_e32 v27, v27
	v_pk_mul_f32 v[18:19], v[22:23], v[18:19]
	v_pk_mul_f32 v[20:21], v[2:3], v[2:3]
	v_pk_fma_f32 v[8:9], v[8:9], 0.5, v[18:19] op_sel_hi:[1,0,1]
	v_pk_fma_f32 v[18:19], v[26:27], s[16:17], v[0:1] op_sel_hi:[1,0,0]
	v_pk_mul_f32 v[20:21], v[20:21], s[14:15] op_sel_hi:[1,0]
	v_pk_fma_f32 v[18:19], v[26:27], v[18:19], s[18:19] op_sel_hi:[1,1,0]
	v_exp_f32_e32 v20, v20
	v_pk_fma_f32 v[18:19], v[26:27], v[18:19], s[10:11] op_sel_hi:[1,1,0]
	v_exp_f32_e32 v21, v21
	v_pk_mul_f32 v[4:5], v[206:207], v[4:5]
	v_pk_fma_f32 v[18:19], v[26:27], v[18:19], s[12:13] op_sel_hi:[1,1,0]
	v_and_b32_e32 v23, 0x7fffffff, v5
	v_and_b32_e32 v22, 0x7fffffff, v4
	v_pk_mul_f32 v[18:19], v[26:27], v[18:19]
	v_pk_fma_f32 v[26:27], v[22:23], s[20:21], 1.0 op_sel_hi:[1,0,0]
	v_pk_fma_f32 v[18:19], v[20:21], v[18:19], 0.5 op_sel_hi:[1,1,0] neg_lo:[1,0,0] neg_hi:[1,0,0]
	v_rcp_f32_e32 v26, v26
	v_rcp_f32_e32 v27, v27
	v_pk_mul_f32 v[18:19], v[24:25], v[18:19]
	v_pk_fma_f32 v[0:1], v[26:27], s[16:17], v[0:1] op_sel_hi:[1,0,0]
	v_pk_fma_f32 v[2:3], v[2:3], 0.5, v[18:19] op_sel_hi:[1,0,1]
	v_pk_mul_f32 v[18:19], v[4:5], v[4:5]
	v_pk_fma_f32 v[0:1], v[26:27], v[0:1], s[18:19] op_sel_hi:[1,1,0]
	v_pk_mul_f32 v[18:19], v[18:19], s[14:15] op_sel_hi:[1,0]
	v_pk_fma_f32 v[0:1], v[26:27], v[0:1], s[10:11] op_sel_hi:[1,1,0]
	v_exp_f32_e32 v18, v18
	v_exp_f32_e32 v19, v19
	v_pk_fma_f32 v[0:1], v[26:27], v[0:1], s[12:13] op_sel_hi:[1,1,0]
	s_movk_i32 s13, 0xff9c
	v_pk_mul_f32 v[0:1], v[26:27], v[0:1]
	s_mov_b32 s15, 0x42000000
	v_pk_fma_f32 v[0:1], v[18:19], v[0:1], 0.5 op_sel_hi:[1,1,0] neg_lo:[1,0,0] neg_hi:[1,0,0]
	v_pk_mul_f32 v[0:1], v[22:23], v[0:1]
	s_nop 0
	v_pk_fma_f32 v[0:1], v[4:5], 0.5, v[0:1] op_sel_hi:[1,0,1]
	v_max3_f32 v4, |v12|, |v13|, |v14|
	v_max3_f32 v4, v4, |v15|, |v16|
	v_max3_f32 v4, v4, |v17|, |v10|
	v_max3_f32 v4, v4, |v11|, |v6|
	v_max3_f32 v4, v4, |v7|, |v8|
	v_max3_f32 v4, v4, |v9|, |v2|
	v_max3_f32 v4, v4, |v3|, |v0|
	v_max_f32_e64 v4, v4, |v1|
	v_mov_b32_e32 v5, v4
	s_nop 1
	v_permlane16_swap_b32_e32 v4, v5
	v_max_f32_e32 v4, v4, v5
	v_lshrrev_b32_e32 v5, 23, v4
	v_and_b32_e32 v4, 0x7fffff, v4
	v_cmp_lt_u32_e32 vcc, s9, v4
	s_nop 1
	v_addc_co_u32_e32 v4, vcc, v5, v182, vcc
	v_med3_i32 v163, v4, s13, v183
	v_lshlrev_b32_e32 v4, 23, v163
	v_sub_u32_e32 v4, 1.0, v4
	v_pk_mul_f32 v[40:41], v[4:5], v[6:7] op_sel_hi:[0,1]
	v_pk_mul_f32 v[42:43], v[4:5], v[8:9] op_sel_hi:[0,1]
	v_pk_mul_f32 v[44:45], v[4:5], v[2:3] op_sel_hi:[0,1]
	v_pk_mul_f32 v[46:47], v[4:5], v[0:1] op_sel_hi:[0,1]
	v_pk_mul_f32 v[32:33], v[4:5], v[14:15] op_sel_hi:[0,1]
	v_pk_mul_f32 v[34:35], v[4:5], v[16:17] op_sel_hi:[0,1]
	v_pk_mul_f32 v[36:37], v[4:5], v[10:11] op_sel_hi:[0,1]
	v_pk_mul_f32 v[38:39], v[4:5], v[12:13] op_sel_hi:[0,1]
	v_cvt_scalef32_2xpk16_fp6_f32 v[184:189], v[32:47], v[40:55], 1.0
	v_cvt_scalef32_pk32_f32_fp6 v[0:31], v[184:189], s15
	v_fma_f32 v16, v32, s8, v0
	v_fma_f32 v17, v33, s8, v2
	v_fma_f32 v18, v34, s8, v4
	v_fma_f32 v19, v35, s8, v6
	v_fma_f32 v20, v36, s8, v8
	v_fma_f32 v21, v37, s8, v10
	v_fma_f32 v22, v38, s8, v12
	v_fma_f32 v23, v39, s8, v14
	v_fma_f32 v24, v40, s8, v1
	v_fma_f32 v25, v41, s8, v3
	v_fma_f32 v26, v42, s8, v5
	v_fma_f32 v27, v43, s8, v7
	v_fma_f32 v28, v44, s8, v9
	v_fma_f32 v29, v45, s8, v11
	v_fma_f32 v30, v46, s8, v13
	v_fma_f32 v31, v47, s8, v15
	v_cvt_scalef32_2xpk16_fp6_f32 v[0:5], v[16:31], v[24:39], 1.0
	v_or_b32_e32 v3, v181, v180
	v_mul_u32_u24_e32 v164, 24, v3
	v_lshl_add_u64 v[4:5], v[168:169], 0, v[164:165]
	v_lshl_add_u64 v[4:5], v[4:5], 0, v[160:161]
	global_store_dwordx3 v[4:5], v[184:186], off nt
	v_add_co_u32_e32 v4, vcc, 0x1000, v4
	v_xor_b32_e32 v0, 0x20820820, v0
	v_xor_b32_e32 v1, 0x8208208, v1
	v_xor_b32_e32 v2, 0x82082082, v2
	v_addc_co_u32_e32 v5, vcc, 0, v5, vcc
	global_store_dwordx3 v[4:5], v[0:2], off offset:2048 nt
	s_and_saveexec_b64 s[24:25], s[0:1]
	s_cbranch_execz .LBB3_8
	v_mov_b32_e32 v1, 0x7a00
	v_add_u32_e32 v0, 0x7f, v163
	v_lshl_add_u32 v1, v163, 8, v1
	v_mov_b32_e32 v163, v161
	v_or_b32_e32 v2, v1, v0
	v_lshl_add_u64 v[0:1], v[166:167], 0, v[162:163]
	global_store_short v[0:1], v2, off
